# indexer pass-1 binning without the +0.0 canonicalisation (score formed by fma with +0), E3 mask-table addresses by v_and_or, write-through row-scale stores so two more barriers skip the L2 write-back
# speedup vs baseline: 1.0166x; 1.0001x over previous
; __device__ __forceinline__ float shfl_xor_f(float v, int mask, int lane) { return __int_as_float(__builtin_amdgcn_ds_bpermute((lane ^ mask) << 2, __float_as_int(v))); }
; __device__ __forceinline__ void quant_rows(unsigned char* ws, size_t xq_off, size_t sar_off, int gw, int NGW, int lane) {
;     ...
;         for (int q = 0; q < 8; ++q) { const u32x4* p = (const u32x4*)(xb + (size_t)(m + q * NGW) * D + 16 * lane); a[q][0] = p[0]; a[q][1] = p[1]; }
;         float ssv = 0.f;
;         if (lane < 32) { const f32x4 s4 = *(const f32x4*)(ssp + (size_t)(m + (lane >> 2) * NGW) * 16 + 4 * (lane & 3)); ssv = (s4[0] + s4[1]) + (s4[2] + s4[3]); }
;         ssv += shfl_xor_f(ssv, 1, lane); ssv += shfl_xor_f(ssv, 2, lane);
; #pragma unroll
;         for (int q = 0; q < 8; ++q) { float t = 0.f;
; #pragma unroll
;             for (int i = 0; i < 8; ++i) { const unsigned wd = a[q][i >> 2][i & 3]; t = __builtin_fmaxf(t, __builtin_fmaxf(__builtin_fabsf(__uint_as_float(wd << 16)), __builtin_fabsf(__uint_as_float(wd & 0xFFFF0000u)))); }
;             mx[q] = t; }
.LBB0_224:
	s_or_b64 exec, exec, s[24:25]
	s_waitcnt vmcnt(21)
	ds_bpermute_b32 v80, v75, v73
	s_waitcnt vmcnt(14)
	v_lshlrev_b32_e32 v151, 16, v62
	v_and_b32_e32 v149, 0xffff0000, v62
	v_max_f32_e64 v81, |v149|, |v149|
	v_max_f32_e64 v82, |v151|, |v151|
	v_lshlrev_b32_e32 v152, 16, v63
	v_and_b32_e32 v150, 0xffff0000, v63
	s_waitcnt lgkmcnt(0)
	v_add_f32_e32 v62, v73, v80
	v_max_f32_e32 v80, v82, v81
	v_max_f32_e64 v63, |v150|, |v150|
	v_max_f32_e64 v81, |v152|, |v152|
	v_max_f32_e32 v63, v81, v63
	v_lshlrev_b32_e32 v148, 16, v64
	v_and_b32_e32 v146, 0xffff0000, v64
	v_max3_f32 v63, v80, 0, v63
	v_max_f32_e64 v64, |v146|, |v146|
	v_max_f32_e64 v80, |v148|, |v148|
	v_lshlrev_b32_e32 v147, 16, v65
	v_and_b32_e32 v145, 0xffff0000, v65
	v_max_f32_e32 v64, v80, v64
	v_max_f32_e64 v65, |v145|, |v145|
	v_max_f32_e64 v80, |v147|, |v147|
	v_max_f32_e32 v65, v80, v65
	v_lshlrev_b32_e32 v144, 16, v58
	v_and_b32_e32 v142, 0xffff0000, v58
	v_max3_f32 v63, v63, v64, v65
	v_max_f32_e64 v58, |v142|, |v142|
	v_max_f32_e64 v64, |v144|, |v144|
	v_lshlrev_b32_e32 v143, 16, v59
	v_and_b32_e32 v141, 0xffff0000, v59
	v_max_f32_e32 v58, v64, v58
	v_max_f32_e64 v59, |v141|, |v141|
	v_max_f32_e64 v64, |v143|, |v143|
	v_max_f32_e32 v59, v64, v59
	v_lshlrev_b32_e32 v140, 16, v60
	v_and_b32_e32 v138, 0xffff0000, v60
	v_max3_f32 v58, v63, v58, v59
	v_max_f32_e64 v59, |v138|, |v138|
	v_max_f32_e64 v60, |v140|, |v140|
	v_lshlrev_b32_e32 v139, 16, v61
	v_and_b32_e32 v137, 0xffff0000, v61
	v_max_f32_e32 v59, v60, v59
	v_max_f32_e64 v60, |v137|, |v137|
	v_max_f32_e64 v61, |v139|, |v139|
	v_max_f32_e32 v60, v61, v60
	s_waitcnt vmcnt(12)
	v_lshlrev_b32_e32 v136, 16, v54
	v_and_b32_e32 v134, 0xffff0000, v54
	v_max3_f32 v64, v58, v59, v60
	v_max_f32_e64 v54, |v134|, |v134|
	v_max_f32_e64 v58, |v136|, |v136|
	v_lshlrev_b32_e32 v135, 16, v55
	v_and_b32_e32 v133, 0xffff0000, v55
	v_max_f32_e32 v54, v58, v54
	v_max_f32_e64 v55, |v133|, |v133|
	v_max_f32_e64 v58, |v135|, |v135|
	v_max_f32_e32 v55, v58, v55
	v_lshlrev_b32_e32 v132, 16, v56
	v_and_b32_e32 v130, 0xffff0000, v56
	v_max3_f32 v54, v54, 0, v55
	v_max_f32_e64 v55, |v130|, |v130|
	v_max_f32_e64 v56, |v132|, |v132|
	v_lshlrev_b32_e32 v131, 16, v57
	v_and_b32_e32 v129, 0xffff0000, v57
	v_max_f32_e32 v55, v56, v55
	v_max_f32_e64 v56, |v129|, |v129|
	v_max_f32_e64 v57, |v131|, |v131|
	v_max_f32_e32 v56, v57, v56
	v_lshlrev_b32_e32 v128, 16, v50
	v_and_b32_e32 v126, 0xffff0000, v50
	v_max3_f32 v54, v54, v55, v56
	v_max_f32_e64 v50, |v126|, |v126|
	v_max_f32_e64 v55, |v128|, |v128|
	v_lshlrev_b32_e32 v127, 16, v51
	v_and_b32_e32 v125, 0xffff0000, v51
	v_max_f32_e32 v50, v55, v50
	v_max_f32_e64 v51, |v125|, |v125|
	v_max_f32_e64 v55, |v127|, |v127|
	v_max_f32_e32 v51, v55, v51
	v_lshlrev_b32_e32 v124, 16, v52
	v_and_b32_e32 v122, 0xffff0000, v52
	v_max3_f32 v50, v54, v50, v51
	v_max_f32_e64 v51, |v122|, |v122|
	v_max_f32_e64 v52, |v124|, |v124|
	v_lshlrev_b32_e32 v123, 16, v53
	v_and_b32_e32 v121, 0xffff0000, v53
	v_max_f32_e32 v51, v52, v51
	v_max_f32_e64 v52, |v121|, |v121|
	v_max_f32_e64 v53, |v123|, |v123|
	v_max_f32_e32 v52, v53, v52
	s_waitcnt vmcnt(10)
	v_lshlrev_b32_e32 v120, 16, v46
	v_and_b32_e32 v118, 0xffff0000, v46
	v_max3_f32 v83, v50, v51, v52
	v_max_f32_e64 v46, |v118|, |v118|
	v_max_f32_e64 v50, |v120|, |v120|
	v_lshlrev_b32_e32 v119, 16, v47
	v_and_b32_e32 v117, 0xffff0000, v47
	v_max_f32_e32 v46, v50, v46
	v_max_f32_e64 v47, |v117|, |v117|
	v_max_f32_e64 v50, |v119|, |v119|
	v_max_f32_e32 v47, v50, v47
	v_lshlrev_b32_e32 v116, 16, v48
	v_and_b32_e32 v114, 0xffff0000, v48
	v_max3_f32 v46, v46, 0, v47
	v_max_f32_e64 v47, |v114|, |v114|
	v_max_f32_e64 v48, |v116|, |v116|
	v_lshlrev_b32_e32 v115, 16, v49
	v_and_b32_e32 v113, 0xffff0000, v49
	v_max_f32_e32 v47, v48, v47
	v_max_f32_e64 v48, |v113|, |v113|
	v_max_f32_e64 v49, |v115|, |v115|
	v_max_f32_e32 v48, v49, v48
	v_lshlrev_b32_e32 v112, 16, v42
	v_and_b32_e32 v110, 0xffff0000, v42
	v_max3_f32 v46, v46, v47, v48
	v_max_f32_e64 v42, |v110|, |v110|
	v_max_f32_e64 v47, |v112|, |v112|
	v_lshlrev_b32_e32 v111, 16, v43
	v_and_b32_e32 v109, 0xffff0000, v43
	v_max_f32_e32 v42, v47, v42
	v_max_f32_e64 v43, |v109|, |v109|
	v_max_f32_e64 v47, |v111|, |v111|
	v_max_f32_e32 v43, v47, v43
	v_lshlrev_b32_e32 v108, 16, v44
	v_and_b32_e32 v106, 0xffff0000, v44
	v_max3_f32 v42, v46, v42, v43
	v_max_f32_e64 v43, |v106|, |v106|
	v_max_f32_e64 v44, |v108|, |v108|
	v_lshlrev_b32_e32 v107, 16, v45
	v_and_b32_e32 v105, 0xffff0000, v45
	v_max_f32_e32 v43, v44, v43
	v_max_f32_e64 v44, |v105|, |v105|
	v_max_f32_e64 v45, |v107|, |v107|
	v_max_f32_e32 v44, v45, v44
	s_waitcnt vmcnt(8)
	v_lshlrev_b32_e32 v104, 16, v38
	v_and_b32_e32 v102, 0xffff0000, v38
	v_max3_f32 v84, v42, v43, v44
	v_max_f32_e64 v38, |v102|, |v102|
	v_max_f32_e64 v42, |v104|, |v104|
	v_lshlrev_b32_e32 v103, 16, v39
	v_and_b32_e32 v101, 0xffff0000, v39
	v_max_f32_e32 v38, v42, v38
	v_max_f32_e64 v39, |v101|, |v101|
	v_max_f32_e64 v42, |v103|, |v103|
	v_max_f32_e32 v39, v42, v39
	v_lshlrev_b32_e32 v100, 16, v40
	v_and_b32_e32 v97, 0xffff0000, v40
	v_max3_f32 v38, v38, 0, v39
	v_max_f32_e64 v39, |v97|, |v97|
	v_max_f32_e64 v40, |v100|, |v100|
	v_lshlrev_b32_e32 v98, 16, v41
	v_and_b32_e32 v96, 0xffff0000, v41
	v_max_f32_e32 v39, v40, v39
	v_max_f32_e64 v40, |v96|, |v96|
	v_max_f32_e64 v41, |v98|, |v98|
	v_max_f32_e32 v40, v41, v40
	v_lshlrev_b32_e32 v95, 16, v34
	v_and_b32_e32 v92, 0xffff0000, v34
	v_max3_f32 v38, v38, v39, v40
	v_max_f32_e64 v34, |v92|, |v92|
	v_max_f32_e64 v39, |v95|, |v95|
	v_lshlrev_b32_e32 v94, 16, v35
	v_and_b32_e32 v91, 0xffff0000, v35
	v_max_f32_e32 v34, v39, v34
	v_max_f32_e64 v35, |v91|, |v91|
	v_max_f32_e64 v39, |v94|, |v94|
	v_max_f32_e32 v35, v39, v35
	v_lshlrev_b32_e32 v90, 16, v36
	v_and_b32_e32 v88, 0xffff0000, v36
	v_max3_f32 v34, v38, v34, v35
	v_max_f32_e64 v35, |v88|, |v88|
	v_max_f32_e64 v36, |v90|, |v90|
	v_lshlrev_b32_e32 v89, 16, v37
	v_and_b32_e32 v87, 0xffff0000, v37
	v_max_f32_e32 v35, v36, v35
	v_max_f32_e64 v36, |v87|, |v87|
	v_max_f32_e64 v37, |v89|, |v89|
	v_max_f32_e32 v36, v37, v36
	s_waitcnt vmcnt(6)
; __device__ __forceinline__ float shfl_xor_f(float v, int mask, int lane) { return __int_as_float(__builtin_amdgcn_ds_bpermute((lane ^ mask) << 2, __float_as_int(v))); }
; __device__ __forceinline__ void quant_rows(unsigned char* ws, size_t xq_off, size_t sar_off, int gw, int NGW, int lane) {
;     ...
;         if (lane < 32) { const f32x4 s4 = *(const f32x4*)(ssp + (size_t)(m + (lane >> 2) * NGW) * 16 + 4 * (lane & 3)); ssv = (s4[0] + s4[1]) + (s4[2] + s4[3]); }
;         ssv += shfl_xor_f(ssv, 1, lane); ssv += shfl_xor_f(ssv, 2, lane);
; #pragma unroll
;         for (int q = 0; q < 8; ++q) { float t = 0.f;
; #pragma unroll
;             for (int i = 0; i < 8; ++i) { const unsigned wd = a[q][i >> 2][i & 3]; t = __builtin_fmaxf(t, __builtin_fmaxf(__builtin_fabsf(__uint_as_float(wd << 16)), __builtin_fabsf(__uint_as_float(wd & 0xFFFF0000u)))); }
;             mx[q] = t; }
; #pragma unroll
;         for (int o = 1; o < 64; o <<= 1) {
; #pragma unroll
;             for (int q = 0; q < 8; ++q) mx[q] = __builtin_fmaxf(mx[q], shfl_xor_f(mx[q], o, lane)); }
	v_lshlrev_b32_e32 v82, 16, v30
	v_and_b32_e32 v80, 0xffff0000, v30
	v_max3_f32 v85, v34, v35, v36
	v_max_f32_e64 v30, |v80|, |v80|
	v_max_f32_e64 v34, |v82|, |v82|
	v_lshlrev_b32_e32 v81, 16, v31
	v_and_b32_e32 v65, 0xffff0000, v31
	v_max_f32_e32 v30, v34, v30
	v_max_f32_e64 v31, |v65|, |v65|
	v_max_f32_e64 v34, |v81|, |v81|
	v_max_f32_e32 v31, v34, v31
	v_lshlrev_b32_e32 v63, 16, v32
	v_and_b32_e32 v60, 0xffff0000, v32
	v_max3_f32 v30, v30, 0, v31
	v_max_f32_e64 v31, |v60|, |v60|
	v_max_f32_e64 v32, |v63|, |v63|
	v_lshlrev_b32_e32 v61, 16, v33
	v_and_b32_e32 v59, 0xffff0000, v33
	v_max_f32_e32 v31, v32, v31
	v_max_f32_e64 v32, |v59|, |v59|
	v_max_f32_e64 v33, |v61|, |v61|
	v_max_f32_e32 v32, v33, v32
	v_lshlrev_b32_e32 v58, 16, v26
	v_and_b32_e32 v56, 0xffff0000, v26
	v_max3_f32 v30, v30, v31, v32
	v_max_f32_e64 v26, |v56|, |v56|
	v_max_f32_e64 v31, |v58|, |v58|
	v_lshlrev_b32_e32 v57, 16, v27
	v_and_b32_e32 v55, 0xffff0000, v27
	v_max_f32_e32 v26, v31, v26
	v_max_f32_e64 v27, |v55|, |v55|
	v_max_f32_e64 v31, |v57|, |v57|
	v_max_f32_e32 v27, v31, v27
	v_lshlrev_b32_e32 v54, 16, v28
	v_and_b32_e32 v52, 0xffff0000, v28
	v_max3_f32 v26, v30, v26, v27
	v_max_f32_e64 v27, |v52|, |v52|
	v_max_f32_e64 v28, |v54|, |v54|
	v_lshlrev_b32_e32 v53, 16, v29
	v_and_b32_e32 v51, 0xffff0000, v29
	v_max_f32_e32 v27, v28, v27
	v_max_f32_e64 v28, |v51|, |v51|
	v_max_f32_e64 v29, |v53|, |v53|
	v_max_f32_e32 v28, v29, v28
	s_waitcnt vmcnt(4)
	v_lshlrev_b32_e32 v50, 16, v22
	v_and_b32_e32 v48, 0xffff0000, v22
	v_max3_f32 v86, v26, v27, v28
	v_max_f32_e64 v22, |v48|, |v48|
	v_max_f32_e64 v26, |v50|, |v50|
	v_lshlrev_b32_e32 v49, 16, v23
	v_and_b32_e32 v47, 0xffff0000, v23
	v_max_f32_e32 v22, v26, v22
	v_max_f32_e64 v23, |v47|, |v47|
	v_max_f32_e64 v26, |v49|, |v49|
	v_max_f32_e32 v23, v26, v23
	v_lshlrev_b32_e32 v46, 16, v24
	v_and_b32_e32 v44, 0xffff0000, v24
	v_max3_f32 v22, v22, 0, v23
	v_max_f32_e64 v23, |v44|, |v44|
	v_max_f32_e64 v24, |v46|, |v46|
	v_lshlrev_b32_e32 v45, 16, v25
	v_and_b32_e32 v43, 0xffff0000, v25
	v_max_f32_e32 v23, v24, v23
	v_max_f32_e64 v24, |v43|, |v43|
	v_max_f32_e64 v25, |v45|, |v45|
	v_max_f32_e32 v24, v25, v24
	v_lshlrev_b32_e32 v42, 16, v18
	v_and_b32_e32 v40, 0xffff0000, v18
	v_max3_f32 v22, v22, v23, v24
	v_max_f32_e64 v18, |v40|, |v40|
	v_max_f32_e64 v23, |v42|, |v42|
	v_lshlrev_b32_e32 v41, 16, v19
	v_and_b32_e32 v39, 0xffff0000, v19
	v_max_f32_e32 v18, v23, v18
	v_max_f32_e64 v19, |v39|, |v39|
	v_max_f32_e64 v23, |v41|, |v41|
	v_max_f32_e32 v19, v23, v19
	v_lshlrev_b32_e32 v38, 16, v20
	v_and_b32_e32 v36, 0xffff0000, v20
	v_max3_f32 v18, v22, v18, v19
	v_max_f32_e64 v19, |v36|, |v36|
	v_max_f32_e64 v20, |v38|, |v38|
	v_lshlrev_b32_e32 v37, 16, v21
	v_and_b32_e32 v35, 0xffff0000, v21
	v_max_f32_e32 v19, v20, v19
	v_max_f32_e64 v20, |v35|, |v35|
	v_max_f32_e64 v21, |v37|, |v37|
	v_max_f32_e32 v20, v21, v20
	s_waitcnt vmcnt(2)
	v_lshlrev_b32_e32 v34, 16, v14
	v_and_b32_e32 v32, 0xffff0000, v14
	v_max3_f32 v93, v18, v19, v20
	v_max_f32_e64 v14, |v32|, |v32|
	v_max_f32_e64 v18, |v34|, |v34|
	v_lshlrev_b32_e32 v33, 16, v15
	v_and_b32_e32 v31, 0xffff0000, v15
	v_max_f32_e32 v14, v18, v14
	v_max_f32_e64 v15, |v31|, |v31|
	v_max_f32_e64 v18, |v33|, |v33|
	v_max_f32_e32 v15, v18, v15
	v_lshlrev_b32_e32 v30, 16, v16
	v_and_b32_e32 v28, 0xffff0000, v16
	v_max3_f32 v14, v14, 0, v15
	v_max_f32_e64 v15, |v28|, |v28|
	v_max_f32_e64 v16, |v30|, |v30|
	v_lshlrev_b32_e32 v29, 16, v17
	v_and_b32_e32 v27, 0xffff0000, v17
	v_max_f32_e32 v15, v16, v15
	v_max_f32_e64 v16, |v27|, |v27|
	v_max_f32_e64 v17, |v29|, |v29|
	v_max_f32_e32 v16, v17, v16
	v_lshlrev_b32_e32 v26, 16, v10
	v_and_b32_e32 v24, 0xffff0000, v10
	v_max3_f32 v14, v14, v15, v16
	v_max_f32_e64 v10, |v24|, |v24|
	v_max_f32_e64 v15, |v26|, |v26|
	v_lshlrev_b32_e32 v25, 16, v11
	v_and_b32_e32 v23, 0xffff0000, v11
	v_max_f32_e32 v10, v15, v10
	v_max_f32_e64 v11, |v23|, |v23|
	v_max_f32_e64 v15, |v25|, |v25|
	v_max_f32_e32 v11, v15, v11
	v_lshlrev_b32_e32 v22, 16, v12
	v_and_b32_e32 v20, 0xffff0000, v12
	v_max3_f32 v10, v14, v10, v11
	v_max_f32_e64 v11, |v20|, |v20|
	v_max_f32_e64 v12, |v22|, |v22|
	v_lshlrev_b32_e32 v21, 16, v13
	v_and_b32_e32 v19, 0xffff0000, v13
	v_max_f32_e32 v11, v12, v11
	v_max_f32_e64 v12, |v19|, |v19|
	v_max_f32_e64 v13, |v21|, |v21|
	v_max_f32_e32 v12, v13, v12
	s_waitcnt vmcnt(0)
	v_lshlrev_b32_e32 v18, 16, v6
	v_and_b32_e32 v16, 0xffff0000, v6
	v_max3_f32 v99, v10, v11, v12
	v_max_f32_e64 v6, |v16|, |v16|
	v_max_f32_e64 v10, |v18|, |v18|
	v_lshlrev_b32_e32 v17, 16, v7
	v_and_b32_e32 v15, 0xffff0000, v7
	v_max_f32_e32 v6, v10, v6
	v_max_f32_e64 v7, |v15|, |v15|
	v_max_f32_e64 v10, |v17|, |v17|
	v_max_f32_e32 v7, v10, v7
	v_lshlrev_b32_e32 v14, 16, v8
	v_and_b32_e32 v12, 0xffff0000, v8
	v_max3_f32 v6, v6, 0, v7
	v_max_f32_e64 v7, |v12|, |v12|
	v_max_f32_e64 v8, |v14|, |v14|
	v_lshlrev_b32_e32 v13, 16, v9
	v_and_b32_e32 v11, 0xffff0000, v9
	v_max_f32_e32 v7, v8, v7
	v_max_f32_e64 v8, |v11|, |v11|
	v_max_f32_e64 v9, |v13|, |v13|
	v_max_f32_e32 v8, v9, v8
	v_max3_f32 v6, v6, v7, v8
	v_lshlrev_b32_e32 v10, 16, v2
	v_and_b32_e32 v8, 0xffff0000, v2
	v_max_f32_e64 v2, |v8|, |v8|
	v_max_f32_e64 v7, |v10|, |v10|
	v_max_f32_e32 v2, v7, v2
	v_lshlrev_b32_e32 v9, 16, v3
	v_and_b32_e32 v7, 0xffff0000, v3
	v_max_f32_e64 v3, |v7|, |v7|
	v_max_f32_e64 v153, |v9|, |v9|
	v_max_f32_e32 v3, v153, v3
	v_max3_f32 v153, v6, v2, v3
	v_lshlrev_b32_e32 v6, 16, v4
	v_and_b32_e32 v3, 0xffff0000, v4
	v_max_f32_e64 v2, |v3|, |v3|
	v_max_f32_e64 v4, |v6|, |v6|
	ds_bpermute_b32 v155, v75, v64
	v_max_f32_e32 v154, v4, v2
	v_lshlrev_b32_e32 v4, 16, v5
	v_and_b32_e32 v2, 0xffff0000, v5
	v_max_f32_e64 v5, |v2|, |v2|
	v_max_f32_e64 v156, |v4|, |v4|
	v_max_f32_e32 v5, v156, v5
	ds_bpermute_b32 v156, v75, v83
	v_max3_f32 v5, v153, v154, v5
	ds_bpermute_b32 v154, v75, v84
	s_waitcnt lgkmcnt(2)
; __device__ __forceinline__ float shfl_xor_f(float v, int mask, int lane) { return __int_as_float(__builtin_amdgcn_ds_bpermute((lane ^ mask) << 2, __float_as_int(v))); }
; __device__ __forceinline__ void quant_rows(unsigned char* ws, size_t xq_off, size_t sar_off, int gw, int NGW, int lane) {
;     ...
; #pragma unroll
;         for (int o = 1; o < 64; o <<= 1) {
; #pragma unroll
;             for (int q = 0; q < 8; ++q) mx[q] = __builtin_fmaxf(mx[q], shfl_xor_f(mx[q], o, lane)); }
;         float mysar = 0.f;
; #pragma unroll
;         for (int q = 0; q < 8; ++q) { const int row = m + q * NGW;
;             const float inv = mx[q] > 0.f ? 127.0f / mx[q] : 0.f, step = mx[q] > 0.f ? mx[q] * (1.0f / 127.0f) : 1.0f;
	v_max_f32_e32 v153, v155, v155
	ds_bpermute_b32 v155, v75, v85
	v_max_f32_e32 v64, v64, v153
	s_waitcnt lgkmcnt(2)
	v_max_f32_e32 v153, v156, v156
	v_max_f32_e32 v83, v83, v153
	s_waitcnt lgkmcnt(1)
	v_max_f32_e32 v153, v154, v154
	ds_bpermute_b32 v154, v75, v86
	v_max_f32_e32 v84, v84, v153
	s_waitcnt lgkmcnt(1)
	v_max_f32_e32 v153, v155, v155
	ds_bpermute_b32 v155, v75, v93
	v_max_f32_e32 v85, v85, v153
	s_waitcnt lgkmcnt(1)
	v_max_f32_e32 v153, v154, v154
	ds_bpermute_b32 v154, v75, v99
	v_max_f32_e32 v86, v86, v153
	s_waitcnt lgkmcnt(1)
	v_max_f32_e32 v153, v155, v155
	ds_bpermute_b32 v155, v75, v5
	v_max_f32_e32 v93, v93, v153
	s_waitcnt lgkmcnt(1)
	v_max_f32_e32 v153, v154, v154
	ds_bpermute_b32 v154, v76, v64
	v_max_f32_e32 v99, v99, v153
	s_waitcnt lgkmcnt(1)
	v_max_f32_e32 v153, v155, v155
	ds_bpermute_b32 v155, v76, v83
	v_max_f32_e32 v5, v5, v153
	s_waitcnt lgkmcnt(1)
	v_max_f32_e32 v153, v154, v154
	ds_bpermute_b32 v154, v76, v84
	v_max_f32_e32 v64, v64, v153
	s_waitcnt lgkmcnt(1)
	v_max_f32_e32 v153, v155, v155
	ds_bpermute_b32 v155, v76, v85
	v_max_f32_e32 v83, v83, v153
	s_waitcnt lgkmcnt(1)
	v_max_f32_e32 v153, v154, v154
	ds_bpermute_b32 v154, v76, v86
	v_max_f32_e32 v84, v84, v153
	s_waitcnt lgkmcnt(1)
	v_max_f32_e32 v153, v155, v155
	ds_bpermute_b32 v155, v76, v93
	v_max_f32_e32 v85, v85, v153
	s_waitcnt lgkmcnt(1)
	v_max_f32_e32 v153, v154, v154
	ds_bpermute_b32 v154, v76, v99
	v_max_f32_e32 v86, v86, v153
	s_waitcnt lgkmcnt(1)
	v_max_f32_e32 v153, v155, v155
	ds_bpermute_b32 v155, v76, v5
	v_max_f32_e32 v93, v93, v153
	s_waitcnt lgkmcnt(1)
	v_max_f32_e32 v153, v154, v154
	ds_bpermute_b32 v154, v0, v64
	v_max_f32_e32 v99, v99, v153
	s_waitcnt lgkmcnt(1)
	v_max_f32_e32 v153, v155, v155
	ds_bpermute_b32 v155, v0, v83
	v_max_f32_e32 v5, v5, v153
	s_waitcnt lgkmcnt(1)
	v_max_f32_e32 v153, v154, v154
	ds_bpermute_b32 v154, v0, v84
	v_max_f32_e32 v64, v64, v153
	s_waitcnt lgkmcnt(1)
	v_max_f32_e32 v153, v155, v155
	ds_bpermute_b32 v155, v0, v85
	v_max_f32_e32 v83, v83, v153
	s_waitcnt lgkmcnt(1)
	v_max_f32_e32 v153, v154, v154
	ds_bpermute_b32 v154, v0, v86
	v_max_f32_e32 v84, v84, v153
	s_waitcnt lgkmcnt(1)
	v_max_f32_e32 v153, v155, v155
	ds_bpermute_b32 v155, v0, v93
	v_max_f32_e32 v85, v85, v153
	s_waitcnt lgkmcnt(1)
	v_max_f32_e32 v153, v154, v154
	ds_bpermute_b32 v154, v0, v99
	v_max_f32_e32 v86, v86, v153
	s_waitcnt lgkmcnt(1)
	v_max_f32_e32 v153, v155, v155
	ds_bpermute_b32 v155, v0, v5
	v_max_f32_e32 v93, v93, v153
	s_waitcnt lgkmcnt(1)
	v_max_f32_e32 v153, v154, v154
	ds_bpermute_b32 v154, v77, v64
	v_max_f32_e32 v99, v99, v153
	s_waitcnt lgkmcnt(1)
	v_max_f32_e32 v153, v155, v155
	ds_bpermute_b32 v155, v77, v83
	v_max_f32_e32 v5, v5, v153
	s_waitcnt lgkmcnt(1)
	v_max_f32_e32 v153, v154, v154
	ds_bpermute_b32 v154, v77, v84
	v_max_f32_e32 v64, v64, v153
	s_waitcnt lgkmcnt(1)
	v_max_f32_e32 v153, v155, v155
	ds_bpermute_b32 v155, v77, v85
	v_max_f32_e32 v83, v83, v153
	s_waitcnt lgkmcnt(1)
	v_max_f32_e32 v153, v154, v154
	ds_bpermute_b32 v154, v77, v86
	v_max_f32_e32 v84, v84, v153
	s_waitcnt lgkmcnt(1)
	v_max_f32_e32 v153, v155, v155
	ds_bpermute_b32 v155, v77, v93
	v_max_f32_e32 v85, v85, v153
	s_waitcnt lgkmcnt(1)
	v_max_f32_e32 v153, v154, v154
	ds_bpermute_b32 v154, v77, v99
	v_max_f32_e32 v86, v86, v153
	s_waitcnt lgkmcnt(1)
	v_max_f32_e32 v153, v155, v155
	ds_bpermute_b32 v155, v77, v5
	v_max_f32_e32 v93, v93, v153
	s_waitcnt lgkmcnt(1)
	v_max_f32_e32 v153, v154, v154
	ds_bpermute_b32 v154, v78, v64
	v_max_f32_e32 v99, v99, v153
	s_waitcnt lgkmcnt(1)
	v_max_f32_e32 v153, v155, v155
	ds_bpermute_b32 v155, v78, v83
	v_max_f32_e32 v5, v5, v153
	s_waitcnt lgkmcnt(1)
	v_max_f32_e32 v153, v154, v154
	ds_bpermute_b32 v154, v78, v84
	v_max_f32_e32 v64, v64, v153
	s_waitcnt lgkmcnt(1)
	v_max_f32_e32 v153, v155, v155
	ds_bpermute_b32 v155, v78, v85
	v_max_f32_e32 v83, v83, v153
	s_waitcnt lgkmcnt(1)
	v_max_f32_e32 v153, v154, v154
	ds_bpermute_b32 v154, v78, v86
	v_max_f32_e32 v84, v84, v153
	s_waitcnt lgkmcnt(1)
	v_max_f32_e32 v153, v155, v155
	ds_bpermute_b32 v155, v78, v93
	v_max_f32_e32 v85, v85, v153
	s_waitcnt lgkmcnt(1)
	v_max_f32_e32 v153, v154, v154
	ds_bpermute_b32 v154, v78, v99
	v_max_f32_e32 v86, v86, v153
	s_waitcnt lgkmcnt(1)
	v_max_f32_e32 v153, v155, v155
	ds_bpermute_b32 v155, v78, v5
	v_max_f32_e32 v93, v93, v153
	s_waitcnt lgkmcnt(1)
	v_max_f32_e32 v153, v154, v154
	ds_bpermute_b32 v154, v79, v64
	v_max_f32_e32 v99, v99, v153
	s_waitcnt lgkmcnt(1)
	v_max_f32_e32 v153, v155, v155
	ds_bpermute_b32 v155, v79, v83
	v_max_f32_e32 v153, v5, v153
	s_waitcnt lgkmcnt(1)
	v_max_f32_e32 v5, v154, v154
	ds_bpermute_b32 v154, v79, v84
	v_max_f32_e32 v5, v64, v5
	s_waitcnt lgkmcnt(1)
	v_max_f32_e32 v64, v155, v155
	ds_bpermute_b32 v155, v79, v85
	v_max_f32_e32 v64, v83, v64
	s_waitcnt lgkmcnt(1)
	v_max_f32_e32 v83, v154, v154
	ds_bpermute_b32 v154, v79, v86
	v_max_f32_e32 v83, v84, v83
	s_waitcnt lgkmcnt(1)
	v_max_f32_e32 v84, v155, v155
	ds_bpermute_b32 v155, v79, v93
	ds_bpermute_b32 v156, v79, v99
	v_max_f32_e32 v84, v85, v84
	s_waitcnt lgkmcnt(2)
	v_max_f32_e32 v85, v154, v154
	ds_bpermute_b32 v154, v79, v153
	v_max_f32_e32 v85, v86, v85
	s_waitcnt lgkmcnt(2)
	v_max_f32_e32 v86, v155, v155
	v_div_scale_f32 v155, s[24:25], v5, v5, s67
	v_max_f32_e32 v86, v93, v86
	s_waitcnt lgkmcnt(1)
	v_max_f32_e32 v93, v156, v156
	v_rcp_f32_e32 v156, v155
	v_max_f32_e32 v93, v99, v93
	s_waitcnt lgkmcnt(0)
; __device__ __forceinline__ void st16_wt(void* p, u32x4 v) { asm volatile("global_store_dwordx4 %0, %1, off sc1\n\ts_nop 1" :: "v"(p), "v"(v) : "memory"); }
; __device__ __forceinline__ void quant_rows(unsigned char* ws, size_t xq_off, size_t sar_off, int gw, int NGW, int lane) {
;     ...
;         for (int q = 0; q < 8; ++q) { const int row = m + q * NGW;
;             const float inv = mx[q] > 0.f ? 127.0f / mx[q] : 0.f, step = mx[q] > 0.f ? mx[q] * (1.0f / 127.0f) : 1.0f;
;             if (lane == 4 * q) mysar = rsqrtf(ssv * (1.0f / D) + EPS) * step;
;             u32x4 o4;
; #pragma unroll
;             for (int w4 = 0; w4 < 4; ++w4) { const unsigned w0 = a[q][w4 >> 1][2 * (w4 & 1)], w1 = a[q][w4 >> 1][2 * (w4 & 1) + 1];
;                 const int q0 = (int)__builtin_rintf(__uint_as_float(w0 << 16) * inv), q1 = (int)__builtin_rintf(__uint_as_float(w0 & 0xFFFF0000u) * inv);
;                 const int q2 = (int)__builtin_rintf(__uint_as_float(w1 << 16) * inv), q3 = (int)__builtin_rintf(__uint_as_float(w1 & 0xFFFF0000u) * inv);
;                 o4[w4] = ((unsigned)q0 & 0xFFu) | (((unsigned)q1 & 0xFFu) << 8) | (((unsigned)q2 & 0xFFu) << 16) | (((unsigned)q3 & 0xFFu) << 24); }
;             st16_wt(xq + (size_t)row * D + 16 * lane, o4);
	v_max_f32_e32 v99, v154, v154
	v_max_f32_e32 v99, v153, v99
	v_fma_f32 v153, -v155, v156, 1.0
	v_fmac_f32_e32 v156, v153, v156
	v_div_scale_f32 v153, vcc, s67, v5, s67
	v_mul_f32_e32 v154, v153, v156
	v_fma_f32 v157, -v155, v154, v153
	v_fmac_f32_e32 v154, v157, v156
	v_fma_f32 v153, -v155, v154, v153
	v_div_fmas_f32 v153, v153, v156, v154
	v_div_fixup_f32 v153, v153, v5, s67
	v_cmp_lt_f32_e64 s[24:25], 0, v5
	s_lshl_b64 s[26:27], s[26:27], 10
	s_lshl_b64 s[30:31], s[30:31], 10
	v_cndmask_b32_e64 v153, 0, v153, s[24:25]
	v_mul_f32_e32 v138, v153, v138
	v_mul_f32_e32 v140, v153, v140
	v_rndne_f32_e32 v138, v138
	v_mul_f32_e32 v139, v153, v139
	v_mul_f32_e32 v137, v153, v137
	v_rndne_f32_e32 v140, v140
	v_cvt_i32_f32_e32 v138, v138
	v_rndne_f32_e32 v139, v139
	v_rndne_f32_e32 v137, v137
	v_cvt_i32_f32_e32 v140, v140
	v_cvt_i32_f32_sdwa v139, v139 dst_sel:WORD_1 dst_unused:UNUSED_PAD src0_sel:DWORD
	v_cvt_i32_f32_e32 v137, v137
	v_mul_f32_e32 v149, v153, v149
	v_mul_f32_e32 v146, v153, v146
	v_mul_f32_e32 v142, v153, v142
	v_mul_f32_e32 v151, v153, v151
	v_rndne_f32_e32 v149, v149
	v_mul_f32_e32 v152, v153, v152
	v_mul_f32_e32 v150, v153, v150
	v_mul_f32_e32 v148, v153, v148
	v_rndne_f32_e32 v146, v146
	v_mul_f32_e32 v147, v153, v147
	v_mul_f32_e32 v145, v153, v145
	v_mul_f32_e32 v144, v153, v144
	v_rndne_f32_e32 v142, v142
	v_mul_f32_e32 v143, v153, v143
	v_mul_f32_e32 v141, v153, v141
	v_lshlrev_b32_e32 v138, 8, v138
	v_rndne_f32_e32 v151, v151
	v_cvt_i32_f32_e32 v149, v149
	v_rndne_f32_e32 v152, v152
	v_rndne_f32_e32 v150, v150
	v_rndne_f32_e32 v148, v148
	v_cvt_i32_f32_e32 v146, v146
	v_rndne_f32_e32 v147, v147
	v_rndne_f32_e32 v145, v145
	v_rndne_f32_e32 v144, v144
	v_cvt_i32_f32_e32 v142, v142
	v_rndne_f32_e32 v143, v143
	v_rndne_f32_e32 v141, v141
	v_and_b32_e32 v138, 0xff00, v138
	v_and_b32_e32 v139, 0xff0000, v139
	v_perm_b32 v137, v137, v140, s68
	v_cvt_i32_f32_e32 v151, v151
	v_cvt_i32_f32_sdwa v152, v152 dst_sel:WORD_1 dst_unused:UNUSED_PAD src0_sel:DWORD
	v_cvt_i32_f32_e32 v150, v150
	v_cvt_i32_f32_e32 v148, v148
	v_cvt_i32_f32_sdwa v147, v147 dst_sel:WORD_1 dst_unused:UNUSED_PAD src0_sel:DWORD
	v_cvt_i32_f32_e32 v145, v145
	v_cvt_i32_f32_e32 v144, v144
	v_cvt_i32_f32_sdwa v143, v143 dst_sel:WORD_1 dst_unused:UNUSED_PAD src0_sel:DWORD
	v_cvt_i32_f32_e32 v141, v141
	v_or3_b32 v153, v137, v138, v139
	v_div_scale_f32 v137, s[28:29], v64, v64, s67
	v_rcp_f32_e32 v140, v137
	v_lshlrev_b32_e32 v149, 8, v149
	v_lshlrev_b32_e32 v146, 8, v146
	v_lshlrev_b32_e32 v142, 8, v142
	v_and_b32_e32 v149, 0xff00, v149
	v_and_b32_e32 v152, 0xff0000, v152
	v_perm_b32 v150, v150, v151, s68
	v_and_b32_e32 v146, 0xff00, v146
	v_and_b32_e32 v147, 0xff0000, v147
	v_perm_b32 v145, v145, v148, s68
	v_and_b32_e32 v142, 0xff00, v142
	v_and_b32_e32 v143, 0xff0000, v143
	v_perm_b32 v141, v141, v144, s68
	v_lshl_add_u64 v[138:139], v[70:71], 0, s[26:27]
	v_or3_b32 v150, v150, v149, v152
	v_or3_b32 v151, v145, v146, v147
	v_or3_b32 v152, v141, v142, v143
	global_store_dwordx4 v[138:139], v[150:153], off sc1
	s_nop 1
	v_fma_f32 v138, -v137, v140, 1.0
	v_fmac_f32_e32 v140, v138, v140
	v_div_scale_f32 v138, vcc, s67, v64, s67
	v_mul_f32_e32 v139, v138, v140
	v_fma_f32 v141, -v137, v139, v138
	v_fmac_f32_e32 v139, v141, v140
	v_fma_f32 v137, -v137, v139, v138
	v_div_fmas_f32 v137, v137, v140, v139
	v_div_fixup_f32 v137, v137, v64, s67
	v_cmp_lt_f32_e64 s[26:27], 0, v64
	s_lshl_b64 s[34:35], s[34:35], 10
	s_lshl_b64 s[36:37], s[36:37], 10
	v_cndmask_b32_e64 v137, 0, v137, s[26:27]
	v_mul_f32_e32 v122, v137, v122
	v_mul_f32_e32 v124, v137, v124
	v_rndne_f32_e32 v122, v122
	v_mul_f32_e32 v123, v137, v123
	v_mul_f32_e32 v121, v137, v121
	v_rndne_f32_e32 v124, v124
	v_cvt_i32_f32_e32 v122, v122
	v_rndne_f32_e32 v123, v123
	v_rndne_f32_e32 v121, v121
	v_cvt_i32_f32_e32 v124, v124
	v_cvt_i32_f32_sdwa v123, v123 dst_sel:WORD_1 dst_unused:UNUSED_PAD src0_sel:DWORD
	v_cvt_i32_f32_e32 v121, v121
	v_mul_f32_e32 v134, v137, v134
	v_mul_f32_e32 v130, v137, v130
	v_mul_f32_e32 v126, v137, v126
	v_mul_f32_e32 v136, v137, v136
	v_rndne_f32_e32 v134, v134
	v_mul_f32_e32 v135, v137, v135
	v_mul_f32_e32 v133, v137, v133
	v_mul_f32_e32 v132, v137, v132
	v_rndne_f32_e32 v130, v130
	v_mul_f32_e32 v131, v137, v131
	v_mul_f32_e32 v129, v137, v129
	v_mul_f32_e32 v128, v137, v128
	v_rndne_f32_e32 v126, v126
	v_mul_f32_e32 v127, v137, v127
	v_mul_f32_e32 v125, v137, v125
	v_lshlrev_b32_e32 v122, 8, v122
	v_rndne_f32_e32 v136, v136
	v_cvt_i32_f32_e32 v134, v134
	v_rndne_f32_e32 v135, v135
	v_rndne_f32_e32 v133, v133
	v_rndne_f32_e32 v132, v132
	v_cvt_i32_f32_e32 v130, v130
	v_rndne_f32_e32 v131, v131
	v_rndne_f32_e32 v129, v129
	v_rndne_f32_e32 v128, v128
	v_cvt_i32_f32_e32 v126, v126
	v_rndne_f32_e32 v127, v127
	v_rndne_f32_e32 v125, v125
	v_and_b32_e32 v122, 0xff00, v122
	v_and_b32_e32 v123, 0xff0000, v123
	v_perm_b32 v121, v121, v124, s68
	v_cvt_i32_f32_e32 v136, v136
	v_cvt_i32_f32_sdwa v135, v135 dst_sel:WORD_1 dst_unused:UNUSED_PAD src0_sel:DWORD
	v_cvt_i32_f32_e32 v133, v133
	v_cvt_i32_f32_e32 v132, v132
	v_cvt_i32_f32_sdwa v131, v131 dst_sel:WORD_1 dst_unused:UNUSED_PAD src0_sel:DWORD
	v_cvt_i32_f32_e32 v129, v129
	v_cvt_i32_f32_e32 v128, v128
	v_cvt_i32_f32_sdwa v127, v127 dst_sel:WORD_1 dst_unused:UNUSED_PAD src0_sel:DWORD
	v_cvt_i32_f32_e32 v125, v125
	v_or3_b32 v137, v121, v122, v123
	v_div_scale_f32 v121, s[28:29], v83, v83, s67
	v_rcp_f32_e32 v124, v121
	v_lshlrev_b32_e32 v134, 8, v134
	v_lshlrev_b32_e32 v130, 8, v130
	v_lshlrev_b32_e32 v126, 8, v126
	s_lshl_b64 s[28:29], s[46:47], 10
	v_and_b32_e32 v134, 0xff00, v134
	v_and_b32_e32 v135, 0xff0000, v135
	v_perm_b32 v133, v133, v136, s68
; __device__ __forceinline__ void st16_wt(void* p, u32x4 v) { asm volatile("global_store_dwordx4 %0, %1, off sc1\n\ts_nop 1" :: "v"(p), "v"(v) : "memory"); }
; __device__ __forceinline__ void quant_rows(unsigned char* ws, size_t xq_off, size_t sar_off, int gw, int NGW, int lane) {
;     ...
;         for (int q = 0; q < 8; ++q) { const int row = m + q * NGW;
;             const float inv = mx[q] > 0.f ? 127.0f / mx[q] : 0.f, step = mx[q] > 0.f ? mx[q] * (1.0f / 127.0f) : 1.0f;
;             if (lane == 4 * q) mysar = rsqrtf(ssv * (1.0f / D) + EPS) * step;
;             u32x4 o4;
; #pragma unroll
;             for (int w4 = 0; w4 < 4; ++w4) { const unsigned w0 = a[q][w4 >> 1][2 * (w4 & 1)], w1 = a[q][w4 >> 1][2 * (w4 & 1) + 1];
;                 const int q0 = (int)__builtin_rintf(__uint_as_float(w0 << 16) * inv), q1 = (int)__builtin_rintf(__uint_as_float(w0 & 0xFFFF0000u) * inv);
;                 const int q2 = (int)__builtin_rintf(__uint_as_float(w1 << 16) * inv), q3 = (int)__builtin_rintf(__uint_as_float(w1 & 0xFFFF0000u) * inv);
;                 o4[w4] = ((unsigned)q0 & 0xFFu) | (((unsigned)q1 & 0xFFu) << 8) | (((unsigned)q2 & 0xFFu) << 16) | (((unsigned)q3 & 0xFFu) << 24); }
;             st16_wt(xq + (size_t)row * D + 16 * lane, o4);
	v_and_b32_e32 v130, 0xff00, v130
	v_and_b32_e32 v131, 0xff0000, v131
	v_perm_b32 v129, v129, v132, s68
	v_and_b32_e32 v126, 0xff00, v126
	v_and_b32_e32 v127, 0xff0000, v127
	v_perm_b32 v125, v125, v128, s68
	v_lshl_add_u64 v[122:123], v[70:71], 0, s[28:29]
	v_or3_b32 v134, v133, v134, v135
	v_or3_b32 v135, v129, v130, v131
	v_or3_b32 v136, v125, v126, v127
	global_store_dwordx4 v[122:123], v[134:137], off sc1
	s_nop 1
	v_fma_f32 v122, -v121, v124, 1.0
	v_fmac_f32_e32 v124, v122, v124
	v_div_scale_f32 v122, vcc, s67, v83, s67
	v_mul_f32_e32 v123, v122, v124
	v_fma_f32 v125, -v121, v123, v122
	v_fmac_f32_e32 v123, v125, v124
	v_fma_f32 v121, -v121, v123, v122
	v_div_fmas_f32 v121, v121, v124, v123
	v_div_fixup_f32 v121, v121, v83, s67
	v_cmp_lt_f32_e64 s[28:29], 0, v83
	s_lshl_b64 s[38:39], s[38:39], 10
	s_lshl_b64 s[48:49], s[48:49], 10
	v_cndmask_b32_e64 v121, 0, v121, s[28:29]
	v_mul_f32_e32 v106, v121, v106
	v_mul_f32_e32 v108, v121, v108
	v_rndne_f32_e32 v106, v106
	v_mul_f32_e32 v107, v121, v107
	v_mul_f32_e32 v105, v121, v105
	v_rndne_f32_e32 v108, v108
	v_cvt_i32_f32_e32 v106, v106
	v_rndne_f32_e32 v107, v107
	v_rndne_f32_e32 v105, v105
	v_cvt_i32_f32_e32 v108, v108
	v_cvt_i32_f32_sdwa v107, v107 dst_sel:WORD_1 dst_unused:UNUSED_PAD src0_sel:DWORD
	v_cvt_i32_f32_e32 v105, v105
	v_mul_f32_e32 v118, v121, v118
	v_mul_f32_e32 v114, v121, v114
	v_mul_f32_e32 v110, v121, v110
	v_mul_f32_e32 v120, v121, v120
	v_rndne_f32_e32 v118, v118
	v_mul_f32_e32 v119, v121, v119
	v_mul_f32_e32 v117, v121, v117
	v_mul_f32_e32 v116, v121, v116
	v_rndne_f32_e32 v114, v114
	v_mul_f32_e32 v115, v121, v115
	v_mul_f32_e32 v113, v121, v113
	v_mul_f32_e32 v112, v121, v112
	v_rndne_f32_e32 v110, v110
	v_mul_f32_e32 v111, v121, v111
	v_mul_f32_e32 v109, v121, v109
	v_lshlrev_b32_e32 v106, 8, v106
	v_rndne_f32_e32 v120, v120
	v_cvt_i32_f32_e32 v118, v118
	v_rndne_f32_e32 v119, v119
	v_rndne_f32_e32 v117, v117
	v_rndne_f32_e32 v116, v116
	v_cvt_i32_f32_e32 v114, v114
	v_rndne_f32_e32 v115, v115
	v_rndne_f32_e32 v113, v113
	v_rndne_f32_e32 v112, v112
	v_cvt_i32_f32_e32 v110, v110
	v_rndne_f32_e32 v111, v111
	v_rndne_f32_e32 v109, v109
	v_and_b32_e32 v106, 0xff00, v106
	v_and_b32_e32 v107, 0xff0000, v107
	v_perm_b32 v105, v105, v108, s68
	v_cvt_i32_f32_e32 v120, v120
	v_cvt_i32_f32_sdwa v119, v119 dst_sel:WORD_1 dst_unused:UNUSED_PAD src0_sel:DWORD
	v_cvt_i32_f32_e32 v117, v117
	v_cvt_i32_f32_e32 v116, v116
	v_cvt_i32_f32_sdwa v115, v115 dst_sel:WORD_1 dst_unused:UNUSED_PAD src0_sel:DWORD
	v_cvt_i32_f32_e32 v113, v113
	v_cvt_i32_f32_e32 v112, v112
	v_cvt_i32_f32_sdwa v111, v111 dst_sel:WORD_1 dst_unused:UNUSED_PAD src0_sel:DWORD
	v_cvt_i32_f32_e32 v109, v109
	v_or3_b32 v121, v105, v106, v107
	v_div_scale_f32 v105, s[50:51], v84, v84, s67
	v_rcp_f32_e32 v108, v105
	v_lshlrev_b32_e32 v118, 8, v118
	v_lshlrev_b32_e32 v114, 8, v114
	v_lshlrev_b32_e32 v110, 8, v110
	v_and_b32_e32 v118, 0xff00, v118
	v_and_b32_e32 v119, 0xff0000, v119
	v_perm_b32 v117, v117, v120, s68
	v_and_b32_e32 v114, 0xff00, v114
	v_and_b32_e32 v115, 0xff0000, v115
	v_perm_b32 v113, v113, v116, s68
	v_and_b32_e32 v110, 0xff00, v110
	v_and_b32_e32 v111, 0xff0000, v111
	v_perm_b32 v109, v109, v112, s68
	v_lshl_add_u64 v[106:107], v[70:71], 0, s[30:31]
	v_or3_b32 v118, v117, v118, v119
	v_or3_b32 v119, v113, v114, v115
	v_or3_b32 v120, v109, v110, v111
	global_store_dwordx4 v[106:107], v[118:121], off sc1
	s_nop 1
	v_fma_f32 v106, -v105, v108, 1.0
	v_fmac_f32_e32 v108, v106, v108
	v_div_scale_f32 v106, vcc, s67, v84, s67
	v_mul_f32_e32 v107, v106, v108
	v_fma_f32 v109, -v105, v107, v106
	v_fmac_f32_e32 v107, v109, v108
	v_fma_f32 v105, -v105, v107, v106
	v_div_fmas_f32 v105, v105, v108, v107
	v_div_fixup_f32 v105, v105, v84, s67
	v_cmp_lt_f32_e64 s[30:31], 0, v84
	ds_bpermute_b32 v73, v76, v62
	s_lshl_b64 s[40:41], s[40:41], 10
	v_cndmask_b32_e64 v105, 0, v105, s[30:31]
	v_mul_f32_e32 v88, v105, v88
	v_mul_f32_e32 v90, v105, v90
	v_rndne_f32_e32 v88, v88
	v_mul_f32_e32 v89, v105, v89
	v_mul_f32_e32 v87, v105, v87
	v_rndne_f32_e32 v90, v90
	v_cvt_i32_f32_e32 v88, v88
	v_rndne_f32_e32 v89, v89
	v_rndne_f32_e32 v87, v87
	v_cvt_i32_f32_e32 v90, v90
	v_cvt_i32_f32_sdwa v89, v89 dst_sel:WORD_1 dst_unused:UNUSED_PAD src0_sel:DWORD
	v_cvt_i32_f32_e32 v87, v87
	v_mul_f32_e32 v102, v105, v102
	v_mul_f32_e32 v97, v105, v97
	v_mul_f32_e32 v92, v105, v92
	v_mul_f32_e32 v104, v105, v104
	v_rndne_f32_e32 v102, v102
	v_mul_f32_e32 v103, v105, v103
	v_mul_f32_e32 v101, v105, v101
	v_mul_f32_e32 v100, v105, v100
	v_rndne_f32_e32 v97, v97
	v_mul_f32_e32 v98, v105, v98
	v_mul_f32_e32 v96, v105, v96
	v_mul_f32_e32 v95, v105, v95
	v_rndne_f32_e32 v92, v92
	v_mul_f32_e32 v94, v105, v94
	v_mul_f32_e32 v91, v105, v91
	v_lshlrev_b32_e32 v88, 8, v88
	v_rndne_f32_e32 v104, v104
	v_cvt_i32_f32_e32 v102, v102
	v_rndne_f32_e32 v103, v103
	v_rndne_f32_e32 v101, v101
	v_rndne_f32_e32 v100, v100
	v_cvt_i32_f32_e32 v97, v97
	v_rndne_f32_e32 v98, v98
	v_rndne_f32_e32 v96, v96
	v_rndne_f32_e32 v95, v95
	v_cvt_i32_f32_e32 v92, v92
	v_rndne_f32_e32 v94, v94
	v_rndne_f32_e32 v91, v91
	v_and_b32_e32 v88, 0xff00, v88
	v_and_b32_e32 v89, 0xff0000, v89
	v_perm_b32 v87, v87, v90, s68
	v_cvt_i32_f32_e32 v104, v104
	v_cvt_i32_f32_sdwa v103, v103 dst_sel:WORD_1 dst_unused:UNUSED_PAD src0_sel:DWORD
	v_cvt_i32_f32_e32 v101, v101
	v_cvt_i32_f32_e32 v100, v100
	v_cvt_i32_f32_sdwa v98, v98 dst_sel:WORD_1 dst_unused:UNUSED_PAD src0_sel:DWORD
	v_cvt_i32_f32_e32 v96, v96
	v_cvt_i32_f32_e32 v95, v95
	v_cvt_i32_f32_sdwa v94, v94 dst_sel:WORD_1 dst_unused:UNUSED_PAD src0_sel:DWORD
	v_cvt_i32_f32_e32 v91, v91
	v_or3_b32 v105, v87, v88, v89
; __device__ __forceinline__ void st16_wt(void* p, u32x4 v) { asm volatile("global_store_dwordx4 %0, %1, off sc1\n\ts_nop 1" :: "v"(p), "v"(v) : "memory"); }
; __device__ __forceinline__ void quant_rows(unsigned char* ws, size_t xq_off, size_t sar_off, int gw, int NGW, int lane) {
;     ...
;         for (int q = 0; q < 8; ++q) { const int row = m + q * NGW;
;             const float inv = mx[q] > 0.f ? 127.0f / mx[q] : 0.f, step = mx[q] > 0.f ? mx[q] * (1.0f / 127.0f) : 1.0f;
;             if (lane == 4 * q) mysar = rsqrtf(ssv * (1.0f / D) + EPS) * step;
;             u32x4 o4;
; #pragma unroll
;             for (int w4 = 0; w4 < 4; ++w4) { const unsigned w0 = a[q][w4 >> 1][2 * (w4 & 1)], w1 = a[q][w4 >> 1][2 * (w4 & 1) + 1];
;                 const int q0 = (int)__builtin_rintf(__uint_as_float(w0 << 16) * inv), q1 = (int)__builtin_rintf(__uint_as_float(w0 & 0xFFFF0000u) * inv);
;                 const int q2 = (int)__builtin_rintf(__uint_as_float(w1 << 16) * inv), q3 = (int)__builtin_rintf(__uint_as_float(w1 & 0xFFFF0000u) * inv);
;                 o4[w4] = ((unsigned)q0 & 0xFFu) | (((unsigned)q1 & 0xFFu) << 8) | (((unsigned)q2 & 0xFFu) << 16) | (((unsigned)q3 & 0xFFu) << 24); }
;             st16_wt(xq + (size_t)row * D + 16 * lane, o4);
	v_div_scale_f32 v87, s[50:51], v85, v85, s67
	v_rcp_f32_e32 v90, v87
	v_lshlrev_b32_e32 v102, 8, v102
	v_lshlrev_b32_e32 v97, 8, v97
	v_lshlrev_b32_e32 v92, 8, v92
	v_and_b32_e32 v102, 0xff00, v102
	v_and_b32_e32 v103, 0xff0000, v103
	v_perm_b32 v101, v101, v104, s68
	v_and_b32_e32 v97, 0xff00, v97
	v_and_b32_e32 v98, 0xff0000, v98
	v_perm_b32 v96, v96, v100, s68
	v_and_b32_e32 v92, 0xff00, v92
	v_and_b32_e32 v94, 0xff0000, v94
	v_perm_b32 v91, v91, v95, s68
	v_lshl_add_u64 v[88:89], v[70:71], 0, s[34:35]
	v_or3_b32 v102, v101, v102, v103
	v_or3_b32 v103, v96, v97, v98
	v_or3_b32 v104, v91, v92, v94
	global_store_dwordx4 v[88:89], v[102:105], off sc1
	s_nop 1
	v_fma_f32 v88, -v87, v90, 1.0
	v_fmac_f32_e32 v90, v88, v90
	v_div_scale_f32 v88, vcc, s67, v85, s67
	v_mul_f32_e32 v89, v88, v90
	v_fma_f32 v91, -v87, v89, v88
	v_fmac_f32_e32 v89, v91, v90
	v_fma_f32 v87, -v87, v89, v88
	v_div_fmas_f32 v87, v87, v90, v89
	v_div_fixup_f32 v87, v87, v85, s67
	v_cmp_lt_f32_e64 s[34:35], 0, v85
	s_nop 1
	v_cndmask_b32_e64 v87, 0, v87, s[34:35]
	v_mul_f32_e32 v52, v87, v52
	v_mul_f32_e32 v54, v87, v54
	v_rndne_f32_e32 v52, v52
	v_mul_f32_e32 v53, v87, v53
	v_mul_f32_e32 v51, v87, v51
	v_rndne_f32_e32 v54, v54
	v_cvt_i32_f32_e32 v52, v52
	v_rndne_f32_e32 v53, v53
	v_rndne_f32_e32 v51, v51
	v_cvt_i32_f32_e32 v54, v54
	v_cvt_i32_f32_sdwa v53, v53 dst_sel:WORD_1 dst_unused:UNUSED_PAD src0_sel:DWORD
	v_cvt_i32_f32_e32 v51, v51
	v_mul_f32_e32 v80, v87, v80
	v_mul_f32_e32 v60, v87, v60
	v_mul_f32_e32 v56, v87, v56
	v_mul_f32_e32 v82, v87, v82
	v_rndne_f32_e32 v80, v80
	v_mul_f32_e32 v81, v87, v81
	v_mul_f32_e32 v65, v87, v65
	v_mul_f32_e32 v63, v87, v63
	v_rndne_f32_e32 v60, v60
	v_mul_f32_e32 v61, v87, v61
	v_mul_f32_e32 v59, v87, v59
	v_mul_f32_e32 v58, v87, v58
	v_rndne_f32_e32 v56, v56
	v_mul_f32_e32 v57, v87, v57
	v_mul_f32_e32 v55, v87, v55
	v_lshlrev_b32_e32 v52, 8, v52
	v_rndne_f32_e32 v82, v82
	v_cvt_i32_f32_e32 v80, v80
	v_rndne_f32_e32 v81, v81
	v_rndne_f32_e32 v65, v65
	v_rndne_f32_e32 v63, v63
	v_cvt_i32_f32_e32 v60, v60
	v_rndne_f32_e32 v61, v61
	v_rndne_f32_e32 v59, v59
	v_rndne_f32_e32 v58, v58
	v_cvt_i32_f32_e32 v56, v56
	v_rndne_f32_e32 v57, v57
	v_rndne_f32_e32 v55, v55
	v_and_b32_e32 v52, 0xff00, v52
	v_and_b32_e32 v53, 0xff0000, v53
	v_perm_b32 v51, v51, v54, s68
	v_cvt_i32_f32_e32 v82, v82
	v_cvt_i32_f32_sdwa v81, v81 dst_sel:WORD_1 dst_unused:UNUSED_PAD src0_sel:DWORD
	v_cvt_i32_f32_e32 v65, v65
	v_cvt_i32_f32_e32 v63, v63
	v_cvt_i32_f32_sdwa v61, v61 dst_sel:WORD_1 dst_unused:UNUSED_PAD src0_sel:DWORD
	v_cvt_i32_f32_e32 v59, v59
	v_cvt_i32_f32_e32 v58, v58
	v_cvt_i32_f32_sdwa v57, v57 dst_sel:WORD_1 dst_unused:UNUSED_PAD src0_sel:DWORD
	v_cvt_i32_f32_e32 v55, v55
	v_or3_b32 v91, v51, v52, v53
	v_div_scale_f32 v51, s[50:51], v86, v86, s67
	v_rcp_f32_e32 v54, v51
	v_lshlrev_b32_e32 v80, 8, v80
	v_lshlrev_b32_e32 v60, 8, v60
	v_lshlrev_b32_e32 v56, 8, v56
	v_and_b32_e32 v80, 0xff00, v80
	v_and_b32_e32 v81, 0xff0000, v81
	v_perm_b32 v65, v65, v82, s68
	v_and_b32_e32 v60, 0xff00, v60
	v_and_b32_e32 v61, 0xff0000, v61
	v_perm_b32 v59, v59, v63, s68
	v_and_b32_e32 v56, 0xff00, v56
	v_and_b32_e32 v57, 0xff0000, v57
	v_perm_b32 v55, v55, v58, s68
	v_lshl_add_u64 v[52:53], v[70:71], 0, s[36:37]
	v_or3_b32 v88, v65, v80, v81
	v_or3_b32 v89, v59, v60, v61
	v_or3_b32 v90, v55, v56, v57
	global_store_dwordx4 v[52:53], v[88:91], off sc1
	s_nop 1
	v_fma_f32 v52, -v51, v54, 1.0
	v_fmac_f32_e32 v54, v52, v54
	v_div_scale_f32 v52, vcc, s67, v86, s67
	v_mul_f32_e32 v53, v52, v54
	v_fma_f32 v55, -v51, v53, v52
	v_fmac_f32_e32 v53, v55, v54
	v_fma_f32 v51, -v51, v53, v52
	v_div_fmas_f32 v51, v51, v54, v53
	v_div_fixup_f32 v51, v51, v86, s67
	v_cmp_lt_f32_e64 s[36:37], 0, v86
	s_nop 1
	v_cndmask_b32_e64 v51, 0, v51, s[36:37]
	v_mul_f32_e32 v36, v51, v36
	v_mul_f32_e32 v38, v51, v38
	v_rndne_f32_e32 v36, v36
	v_mul_f32_e32 v37, v51, v37
	v_mul_f32_e32 v35, v51, v35
	v_rndne_f32_e32 v38, v38
	v_cvt_i32_f32_e32 v36, v36
	v_rndne_f32_e32 v37, v37
	v_rndne_f32_e32 v35, v35
	v_cvt_i32_f32_e32 v38, v38
	v_cvt_i32_f32_sdwa v37, v37 dst_sel:WORD_1 dst_unused:UNUSED_PAD src0_sel:DWORD
	v_cvt_i32_f32_e32 v35, v35
	v_mul_f32_e32 v48, v51, v48
	v_mul_f32_e32 v44, v51, v44
	v_mul_f32_e32 v40, v51, v40
	v_mul_f32_e32 v50, v51, v50
	v_rndne_f32_e32 v48, v48
	v_mul_f32_e32 v49, v51, v49
	v_mul_f32_e32 v47, v51, v47
	v_mul_f32_e32 v46, v51, v46
	v_rndne_f32_e32 v44, v44
	v_mul_f32_e32 v45, v51, v45
	v_mul_f32_e32 v43, v51, v43
	v_mul_f32_e32 v42, v51, v42
	v_rndne_f32_e32 v40, v40
	v_mul_f32_e32 v41, v51, v41
	v_mul_f32_e32 v39, v51, v39
	v_lshlrev_b32_e32 v36, 8, v36
	v_rndne_f32_e32 v50, v50
	v_cvt_i32_f32_e32 v48, v48
	v_rndne_f32_e32 v49, v49
	v_rndne_f32_e32 v47, v47
	v_rndne_f32_e32 v46, v46
	v_cvt_i32_f32_e32 v44, v44
	v_rndne_f32_e32 v45, v45
	v_rndne_f32_e32 v43, v43
	v_rndne_f32_e32 v42, v42
	v_cvt_i32_f32_e32 v40, v40
	v_rndne_f32_e32 v41, v41
	v_rndne_f32_e32 v39, v39
	v_and_b32_e32 v36, 0xff00, v36
	v_and_b32_e32 v37, 0xff0000, v37
	v_perm_b32 v35, v35, v38, s68
	v_cvt_i32_f32_e32 v50, v50
	v_cvt_i32_f32_sdwa v49, v49 dst_sel:WORD_1 dst_unused:UNUSED_PAD src0_sel:DWORD
	v_cvt_i32_f32_e32 v47, v47
	v_cvt_i32_f32_e32 v46, v46
	v_cvt_i32_f32_sdwa v45, v45 dst_sel:WORD_1 dst_unused:UNUSED_PAD src0_sel:DWORD
	v_cvt_i32_f32_e32 v43, v43
	v_cvt_i32_f32_e32 v42, v42
	v_cvt_i32_f32_sdwa v41, v41 dst_sel:WORD_1 dst_unused:UNUSED_PAD src0_sel:DWORD
	v_cvt_i32_f32_e32 v39, v39
	v_or3_b32 v51, v35, v36, v37
	v_div_scale_f32 v35, s[50:51], v93, v93, s67
	v_rcp_f32_e32 v38, v35
	v_lshlrev_b32_e32 v48, 8, v48
	v_lshlrev_b32_e32 v44, 8, v44
	v_lshlrev_b32_e32 v40, 8, v40
; __device__ __forceinline__ void st16_wt(void* p, u32x4 v) { asm volatile("global_store_dwordx4 %0, %1, off sc1\n\ts_nop 1" :: "v"(p), "v"(v) : "memory"); }
; __device__ __forceinline__ void quant_rows(unsigned char* ws, size_t xq_off, size_t sar_off, int gw, int NGW, int lane) {
;     ...
;         for (int q = 0; q < 8; ++q) { const int row = m + q * NGW;
;             const float inv = mx[q] > 0.f ? 127.0f / mx[q] : 0.f, step = mx[q] > 0.f ? mx[q] * (1.0f / 127.0f) : 1.0f;
;             if (lane == 4 * q) mysar = rsqrtf(ssv * (1.0f / D) + EPS) * step;
;             u32x4 o4;
; #pragma unroll
;             for (int w4 = 0; w4 < 4; ++w4) { const unsigned w0 = a[q][w4 >> 1][2 * (w4 & 1)], w1 = a[q][w4 >> 1][2 * (w4 & 1) + 1];
;                 const int q0 = (int)__builtin_rintf(__uint_as_float(w0 << 16) * inv), q1 = (int)__builtin_rintf(__uint_as_float(w0 & 0xFFFF0000u) * inv);
;                 const int q2 = (int)__builtin_rintf(__uint_as_float(w1 << 16) * inv), q3 = (int)__builtin_rintf(__uint_as_float(w1 & 0xFFFF0000u) * inv);
;                 o4[w4] = ((unsigned)q0 & 0xFFu) | (((unsigned)q1 & 0xFFu) << 8) | (((unsigned)q2 & 0xFFu) << 16) | (((unsigned)q3 & 0xFFu) << 24); }
;             st16_wt(xq + (size_t)row * D + 16 * lane, o4);
;         }
;         if (lane < 32 && (lane & 3) == 0) sar[m + (lane >> 2) * NGW] = mysar;
	v_and_b32_e32 v48, 0xff00, v48
	v_and_b32_e32 v49, 0xff0000, v49
	v_perm_b32 v47, v47, v50, s68
	v_and_b32_e32 v44, 0xff00, v44
	v_and_b32_e32 v45, 0xff0000, v45
	v_perm_b32 v43, v43, v46, s68
	v_and_b32_e32 v40, 0xff00, v40
	v_and_b32_e32 v41, 0xff0000, v41
	v_perm_b32 v39, v39, v42, s68
	v_lshl_add_u64 v[36:37], v[70:71], 0, s[38:39]
	v_or3_b32 v48, v47, v48, v49
	v_or3_b32 v49, v43, v44, v45
	v_or3_b32 v50, v39, v40, v41
	global_store_dwordx4 v[36:37], v[48:51], off sc1
	s_nop 1
	v_fma_f32 v36, -v35, v38, 1.0
	v_fmac_f32_e32 v38, v36, v38
	v_div_scale_f32 v36, vcc, s67, v93, s67
	v_mul_f32_e32 v37, v36, v38
	v_fma_f32 v39, -v35, v37, v36
	v_fmac_f32_e32 v37, v39, v38
	v_fma_f32 v35, -v35, v37, v36
	v_div_fmas_f32 v35, v35, v38, v37
	v_div_fixup_f32 v35, v35, v93, s67
	v_cmp_lt_f32_e64 s[38:39], 0, v93
	s_nop 1
	v_cndmask_b32_e64 v35, 0, v35, s[38:39]
	v_mul_f32_e32 v20, v35, v20
	v_mul_f32_e32 v22, v35, v22
	v_rndne_f32_e32 v20, v20
	v_mul_f32_e32 v21, v35, v21
	v_mul_f32_e32 v19, v35, v19
	v_rndne_f32_e32 v22, v22
	v_cvt_i32_f32_e32 v20, v20
	v_rndne_f32_e32 v21, v21
	v_rndne_f32_e32 v19, v19
	v_cvt_i32_f32_e32 v22, v22
	v_cvt_i32_f32_sdwa v21, v21 dst_sel:WORD_1 dst_unused:UNUSED_PAD src0_sel:DWORD
	v_cvt_i32_f32_e32 v19, v19
	v_mul_f32_e32 v32, v35, v32
	v_mul_f32_e32 v28, v35, v28
	v_mul_f32_e32 v24, v35, v24
	v_mul_f32_e32 v34, v35, v34
	v_rndne_f32_e32 v32, v32
	v_mul_f32_e32 v33, v35, v33
	v_mul_f32_e32 v31, v35, v31
	v_mul_f32_e32 v30, v35, v30
	v_rndne_f32_e32 v28, v28
	v_mul_f32_e32 v29, v35, v29
	v_mul_f32_e32 v27, v35, v27
	v_mul_f32_e32 v26, v35, v26
	v_rndne_f32_e32 v24, v24
	v_mul_f32_e32 v25, v35, v25
	v_mul_f32_e32 v23, v35, v23
	v_lshlrev_b32_e32 v20, 8, v20
	v_rndne_f32_e32 v34, v34
	v_cvt_i32_f32_e32 v32, v32
	v_rndne_f32_e32 v33, v33
	v_rndne_f32_e32 v31, v31
	v_rndne_f32_e32 v30, v30
	v_cvt_i32_f32_e32 v28, v28
	v_rndne_f32_e32 v29, v29
	v_rndne_f32_e32 v27, v27
	v_rndne_f32_e32 v26, v26
	v_cvt_i32_f32_e32 v24, v24
	v_rndne_f32_e32 v25, v25
	v_rndne_f32_e32 v23, v23
	v_and_b32_e32 v20, 0xff00, v20
	v_and_b32_e32 v21, 0xff0000, v21
	v_perm_b32 v19, v19, v22, s68
	v_cvt_i32_f32_e32 v34, v34
	v_cvt_i32_f32_sdwa v33, v33 dst_sel:WORD_1 dst_unused:UNUSED_PAD src0_sel:DWORD
	v_cvt_i32_f32_e32 v31, v31
	v_cvt_i32_f32_e32 v30, v30
	v_cvt_i32_f32_sdwa v29, v29 dst_sel:WORD_1 dst_unused:UNUSED_PAD src0_sel:DWORD
	v_cvt_i32_f32_e32 v27, v27
	v_cvt_i32_f32_e32 v26, v26
	v_cvt_i32_f32_sdwa v25, v25 dst_sel:WORD_1 dst_unused:UNUSED_PAD src0_sel:DWORD
	v_cvt_i32_f32_e32 v23, v23
	v_or3_b32 v35, v19, v20, v21
	v_div_scale_f32 v19, s[50:51], v99, v99, s67
	v_rcp_f32_e32 v22, v19
	v_lshlrev_b32_e32 v32, 8, v32
	v_lshlrev_b32_e32 v28, 8, v28
	v_lshlrev_b32_e32 v24, 8, v24
	v_and_b32_e32 v32, 0xff00, v32
	v_and_b32_e32 v33, 0xff0000, v33
	v_perm_b32 v31, v31, v34, s68
	v_and_b32_e32 v28, 0xff00, v28
	v_and_b32_e32 v29, 0xff0000, v29
	v_perm_b32 v27, v27, v30, s68
	v_and_b32_e32 v24, 0xff00, v24
	v_and_b32_e32 v25, 0xff0000, v25
	v_perm_b32 v23, v23, v26, s68
	v_lshl_add_u64 v[20:21], v[70:71], 0, s[48:49]
	v_or3_b32 v32, v31, v32, v33
	v_or3_b32 v33, v27, v28, v29
	v_or3_b32 v34, v23, v24, v25
	global_store_dwordx4 v[20:21], v[32:35], off sc1
	s_nop 1
	v_fma_f32 v20, -v19, v22, 1.0
	v_fmac_f32_e32 v22, v20, v22
	v_div_scale_f32 v20, vcc, s67, v99, s67
	v_mul_f32_e32 v21, v20, v22
	v_fma_f32 v23, -v19, v21, v20
	v_fmac_f32_e32 v21, v23, v22
	v_fma_f32 v19, -v19, v21, v20
	v_div_fmas_f32 v19, v19, v22, v21
	v_div_fixup_f32 v19, v19, v99, s67
	v_cmp_lt_f32_e32 vcc, 0, v99
	s_nop 1
	v_cndmask_b32_e32 v19, 0, v19, vcc
	v_mul_f32_e32 v16, v19, v16
	v_mul_f32_e32 v12, v19, v12
	v_mul_f32_e32 v8, v19, v8
	v_mul_f32_e32 v3, v19, v3
	v_mul_f32_e32 v18, v19, v18
	v_rndne_f32_e32 v16, v16
	v_mul_f32_e32 v17, v19, v17
	v_mul_f32_e32 v15, v19, v15
	v_mul_f32_e32 v14, v19, v14
	v_rndne_f32_e32 v12, v12
	v_mul_f32_e32 v13, v19, v13
	v_mul_f32_e32 v11, v19, v11
	v_mul_f32_e32 v10, v19, v10
	v_rndne_f32_e32 v8, v8
	v_mul_f32_e32 v9, v19, v9
	v_mul_f32_e32 v7, v19, v7
	v_mul_f32_e32 v6, v19, v6
	v_rndne_f32_e32 v3, v3
	v_mul_f32_e32 v4, v19, v4
	v_mul_f32_e32 v2, v19, v2
	v_rndne_f32_e32 v18, v18
	v_cvt_i32_f32_e32 v16, v16
	v_rndne_f32_e32 v17, v17
	v_rndne_f32_e32 v15, v15
	v_rndne_f32_e32 v14, v14
	v_cvt_i32_f32_e32 v12, v12
	v_rndne_f32_e32 v13, v13
	v_rndne_f32_e32 v11, v11
	v_rndne_f32_e32 v10, v10
	v_cvt_i32_f32_e32 v8, v8
	v_rndne_f32_e32 v9, v9
	v_rndne_f32_e32 v7, v7
	v_rndne_f32_e32 v6, v6
	v_cvt_i32_f32_e32 v3, v3
	v_rndne_f32_e32 v4, v4
	v_rndne_f32_e32 v2, v2
	v_cvt_i32_f32_e32 v18, v18
	v_cvt_i32_f32_sdwa v17, v17 dst_sel:WORD_1 dst_unused:UNUSED_PAD src0_sel:DWORD
	v_cvt_i32_f32_e32 v15, v15
	v_cvt_i32_f32_e32 v14, v14
	v_cvt_i32_f32_sdwa v13, v13 dst_sel:WORD_1 dst_unused:UNUSED_PAD src0_sel:DWORD
	v_cvt_i32_f32_e32 v11, v11
	v_cvt_i32_f32_e32 v10, v10
	v_cvt_i32_f32_sdwa v9, v9 dst_sel:WORD_1 dst_unused:UNUSED_PAD src0_sel:DWORD
	v_cvt_i32_f32_e32 v7, v7
	v_cvt_i32_f32_e32 v6, v6
	v_cvt_i32_f32_sdwa v4, v4 dst_sel:WORD_1 dst_unused:UNUSED_PAD src0_sel:DWORD
	v_cvt_i32_f32_e32 v2, v2
	v_lshlrev_b32_e32 v16, 8, v16
	v_lshlrev_b32_e32 v12, 8, v12
	v_lshlrev_b32_e32 v8, 8, v8
	v_lshlrev_b32_e32 v3, 8, v3
	v_and_b32_e32 v16, 0xff00, v16
	v_and_b32_e32 v17, 0xff0000, v17
	v_perm_b32 v15, v15, v18, s68
	v_and_b32_e32 v12, 0xff00, v12
	v_and_b32_e32 v13, 0xff0000, v13
	v_perm_b32 v11, v11, v14, s68
	v_and_b32_e32 v8, 0xff00, v8
	v_and_b32_e32 v9, 0xff0000, v9
	v_perm_b32 v7, v7, v10, s68
	v_and_b32_e32 v3, 0xff00, v3
	v_and_b32_e32 v4, 0xff0000, v4
	v_perm_b32 v2, v2, v6, s68
	v_or3_b32 v16, v15, v16, v17
	v_or3_b32 v17, v11, v12, v13
	v_or3_b32 v18, v7, v8, v9
	v_or3_b32 v19, v2, v3, v4
	v_lshl_add_u64 v[2:3], v[70:71], 0, s[40:41]
	global_store_dwordx4 v[2:3], v[16:19], off sc1
	s_nop 1
	s_and_saveexec_b64 s[48:49], s[6:7]
	s_cbranch_execz .LBB0_221
; __device__ __forceinline__ float shfl_xor_f(float v, int mask, int lane) { return __int_as_float(__builtin_amdgcn_ds_bpermute((lane ^ mask) << 2, __float_as_int(v))); }
; __device__ __forceinline__ void st16_wt(void* p, u32x4 v) { asm volatile("global_store_dwordx4 %0, %1, off sc1\n\ts_nop 1" :: "v"(p), "v"(v) : "memory"); }
; __device__ __forceinline__ void quant_rows(unsigned char* ws, size_t xq_off, size_t sar_off, int gw, int NGW, int lane) {
;     ...
;         float ssv = 0.f;
;         if (lane < 32) { const f32x4 s4 = *(const f32x4*)(ssp + (size_t)(m + (lane >> 2) * NGW) * 16 + 4 * (lane & 3)); ssv = (s4[0] + s4[1]) + (s4[2] + s4[3]); }
;         ssv += shfl_xor_f(ssv, 1, lane); ssv += shfl_xor_f(ssv, 2, lane);
;     ...
;         float mysar = 0.f;
; #pragma unroll
;         for (int q = 0; q < 8; ++q) { const int row = m + q * NGW;
;             const float inv = mx[q] > 0.f ? 127.0f / mx[q] : 0.f, step = mx[q] > 0.f ? mx[q] * (1.0f / 127.0f) : 1.0f;
;             if (lane == 4 * q) mysar = rsqrtf(ssv * (1.0f / D) + EPS) * step;
;             u32x4 o4;
; #pragma unroll
;             for (int w4 = 0; w4 < 4; ++w4) { const unsigned w0 = a[q][w4 >> 1][2 * (w4 & 1)], w1 = a[q][w4 >> 1][2 * (w4 & 1) + 1];
;                 const int q0 = (int)__builtin_rintf(__uint_as_float(w0 << 16) * inv), q1 = (int)__builtin_rintf(__uint_as_float(w0 & 0xFFFF0000u) * inv);
;                 const int q2 = (int)__builtin_rintf(__uint_as_float(w1 << 16) * inv), q3 = (int)__builtin_rintf(__uint_as_float(w1 & 0xFFFF0000u) * inv);
;                 o4[w4] = ((unsigned)q0 & 0xFFu) | (((unsigned)q1 & 0xFFu) << 8) | (((unsigned)q2 & 0xFFu) << 16) | (((unsigned)q3 & 0xFFu) << 24); }
;             st16_wt(xq + (size_t)row * D + 16 * lane, o4);
;         }
;         if (lane < 32 && (lane & 3) == 0) sar[m + (lane >> 2) * NGW] = mysar;
	s_waitcnt lgkmcnt(0)
	v_add_f32_e32 v2, v62, v73
	v_fmamk_f32 v2, v2, 0x3a800000, v228
	v_mul_f32_e32 v3, 0x4b800000, v2
	v_cmp_gt_f32_e64 s[40:41], s84, v2
	v_mul_f32_e32 v6, 0x3c010204, v86
	v_mul_f32_e32 v7, 0x3c010204, v85
	v_cndmask_b32_e64 v2, v2, v3, s[40:41]
	v_rsq_f32_e32 v2, v2
	v_mul_f32_e32 v3, 0x3c010204, v99
	v_mul_f32_e32 v8, 0x3c010204, v84
	v_mul_f32_e32 v9, 0x3c010204, v83
	v_mul_f32_e32 v4, 0x45800000, v2
	v_cndmask_b32_e64 v2, v2, v4, s[40:41]
	v_mul_f32_e32 v4, 0x3c010204, v93
	v_mul_f32_e32 v10, 0x3c010204, v64
	v_mul_f32_e32 v5, 0x3c010204, v5
	v_cndmask_b32_e32 v3, 1.0, v3, vcc
	v_cndmask_b32_e64 v4, 1.0, v4, s[38:39]
	v_cndmask_b32_e64 v6, 1.0, v6, s[36:37]
	v_cndmask_b32_e64 v7, 1.0, v7, s[34:35]
	v_cndmask_b32_e64 v8, 1.0, v8, s[30:31]
	v_cndmask_b32_e64 v9, 1.0, v9, s[28:29]
	v_cndmask_b32_e64 v10, 1.0, v10, s[26:27]
	v_cndmask_b32_e64 v5, 1.0, v5, s[24:25]
	v_mul_f32_e32 v3, v2, v3
	v_mul_f32_e32 v4, v2, v4
	v_mul_f32_e32 v6, v2, v6
	v_mul_f32_e32 v7, v2, v7
	v_mul_f32_e32 v8, v2, v8
	v_mul_f32_e32 v9, v2, v9
	v_mul_f32_e32 v10, v2, v10
	v_mul_f32_e32 v2, v2, v5
	v_cndmask_b32_e64 v2, 0, v2, s[22:23]
	v_cndmask_b32_e64 v2, v2, v10, s[20:21]
	v_cndmask_b32_e64 v2, v2, v9, s[18:19]
	v_cndmask_b32_e64 v2, v2, v8, s[16:17]
	v_cndmask_b32_e64 v2, v2, v7, s[14:15]
	v_cndmask_b32_e64 v2, v2, v6, s[12:13]
	v_cndmask_b32_e64 v2, v2, v4, s[10:11]
	v_ashrrev_i32_e32 v73, 31, v72
	v_cndmask_b32_e64 v4, v2, v3, s[8:9]
	v_lshl_add_u64 v[2:3], v[72:73], 2, s[44:45]
	global_store_dword v[2:3], v4, off sc1
	s_branch .LBB0_221

; __device__ __forceinline__ float relu_i(float p) { const int i = __float_as_int(p); return __int_as_float(i > 0 ? i : 0); }
; __device__ __forceinline__ void idx_scores_k(f32x16& sc, const bf16x8 (&kf)[4], const bf16x8 (&qf)[16], const f32x4& w) {
;     f32x16 p0 = f32x16{}, p1 = f32x16{};
; #pragma unroll
;     for (int d0 = 0; d0 < 4; ++d0) p0 = __builtin_amdgcn_mfma_f32_32x32x16_bf16(kf[d0], qf[d0], p0, 0, 0, 0);
; #pragma unroll
;     for (int d0 = 0; d0 < 4; ++d0) p1 = __builtin_amdgcn_mfma_f32_32x32x16_bf16(kf[d0], qf[4 + d0], p1, 0, 0, 0);
; #pragma unroll
;     for (int r = 0; r < 16; ++r) sc[r] = w[0] * relu_i(p0[r]);
;     p0 = f32x16{};
; #pragma unroll
;     for (int d0 = 0; d0 < 4; ++d0) p0 = __builtin_amdgcn_mfma_f32_32x32x16_bf16(kf[d0], qf[8 + d0], p0, 0, 0, 0);
; #pragma unroll
;     for (int r = 0; r < 16; ++r) sc[r] = fmaf(w[1], relu_i(p1[r]), sc[r]);
;     p1 = f32x16{};
; #pragma unroll
;     for (int d0 = 0; d0 < 4; ++d0) p1 = __builtin_amdgcn_mfma_f32_32x32x16_bf16(kf[d0], qf[12 + d0], p1, 0, 0, 0);
; #pragma unroll
;     for (int r = 0; r < 16; ++r) sc[r] = fmaf(w[2], relu_i(p0[r]), sc[r]);
; #pragma unroll
;     for (int r = 0; r < 16; ++r) sc[r] = fmaf(w[3], relu_i(p1[r]), sc[r]);
; }
; template <int PASS> __device__ __forceinline__ void idx_pass(const bf16_t* KIb, const bf16x8 (&qf)[16], const f32x4& w, int jd, int tq, int wid, int r32, int hi, unsigned khi, unsigned klo, bool cand, LAS unsigned char* L) {
;     ...
;     for (; j <= jd; j += 8) {
;         const bool diag = (j == jd);
;         idx_loadk(kB, KIb + (size_t)(j * 64 + 32) * 64, r32, hi);
;         f32x16 sc; idx_scores_k(sc, kA, qf, w);
;         unsigned lo, elo, hw, ehw;
;         if (diag) idx_half<PASS, true>(lo, elo, sc, j * 64, tq, r32, hi, khi, klo, cand, L); else idx_half<PASS, false>(lo, elo, sc, j * 64, tq, r32, hi, khi, klo, cand, L);
;         if (j + 8 <= jd) idx_loadk(kA, KIb + (size_t)((j + 8) * 64) * 64, r32, hi);
.LBB0_712:
	s_add_i32 s0, s21, s20
	s_cmp_lg_u32 s0, 8
	s_cselect_b64 s[14:15], -1, 0
	s_add_i32 s0, s10, 0xfffffe20
	s_ashr_i32 s1, s0, 31
	s_lshl_b64 s[0:1], s[0:1], 7
	v_lshl_add_u64 v[2:3], v[50:51], 0, s[0:1]
	global_load_dwordx4 v[46:49], v[2:3], off
	global_load_dwordx4 v[42:45], v[2:3], off offset:32
	global_load_dwordx4 v[38:41], v[2:3], off offset:64
	global_load_dwordx4 v[34:37], v[2:3], off offset:96
	s_and_b64 vcc, exec, s[14:15]
	s_waitcnt vmcnt(7) lgkmcnt(14)
	v_mfma_f32_32x32x16_bf16 v[2:17], v[18:21], v[70:73], 0
	s_waitcnt vmcnt(6)
	v_mfma_f32_32x32x16_bf16 v[2:17], v[22:25], v[74:77], v[2:17]
	s_waitcnt vmcnt(5) lgkmcnt(13)
	v_mfma_f32_32x32x16_bf16 v[2:17], v[26:29], v[78:81], v[2:17]
	s_waitcnt vmcnt(4) lgkmcnt(12)
	v_mfma_f32_32x32x16_bf16 v[2:17], v[30:33], v[82:85], v[2:17]
	s_waitcnt lgkmcnt(11)
	v_mfma_f32_32x32x16_bf16 v[180:195], v[18:21], v[86:89], 0
	s_waitcnt lgkmcnt(10)
	v_mfma_f32_32x32x16_bf16 v[180:195], v[22:25], v[90:93], v[180:195]
	s_waitcnt lgkmcnt(9)
	v_mfma_f32_32x32x16_bf16 v[180:195], v[26:29], v[94:97], v[180:195]
	s_waitcnt lgkmcnt(8)
	v_mfma_f32_32x32x16_bf16 v[180:195], v[30:33], v[98:101], v[180:195]
	s_nop 3
	v_max_i32_e32 v200, 0, v2
	v_fma_f32 v136, v66, v200, 0
	v_max_i32_e32 v200, 0, v3
	v_fma_f32 v135, v66, v200, 0
	v_max_i32_e32 v200, 0, v4
	v_fma_f32 v134, v66, v200, 0
	v_max_i32_e32 v200, 0, v5
	v_fma_f32 v65, v66, v200, 0
	v_max_i32_e32 v200, 0, v6
	v_fma_f32 v64, v66, v200, 0
	v_max_i32_e32 v200, 0, v7
	v_fma_f32 v63, v66, v200, 0
	v_max_i32_e32 v200, 0, v8
	v_fma_f32 v62, v66, v200, 0
	v_max_i32_e32 v200, 0, v9
	v_fma_f32 v61, v66, v200, 0
	v_max_i32_e32 v200, 0, v10
	v_fma_f32 v60, v66, v200, 0
	v_max_i32_e32 v200, 0, v11
	v_fma_f32 v59, v66, v200, 0
	v_max_i32_e32 v200, 0, v12
	v_fma_f32 v58, v66, v200, 0
	v_max_i32_e32 v200, 0, v13
	v_fma_f32 v57, v66, v200, 0
	v_max_i32_e32 v200, 0, v14
	v_fma_f32 v56, v66, v200, 0
	v_max_i32_e32 v200, 0, v15
	v_fma_f32 v55, v66, v200, 0
	v_max_i32_e32 v200, 0, v16
	v_fma_f32 v54, v66, v200, 0
	v_max_i32_e32 v200, 0, v17
	v_fma_f32 v53, v66, v200, 0
	s_waitcnt lgkmcnt(7)
	v_mfma_f32_32x32x16_bf16 v[2:17], v[18:21], v[102:105], 0
	s_waitcnt lgkmcnt(6)
	v_mfma_f32_32x32x16_bf16 v[2:17], v[22:25], v[106:109], v[2:17]
	s_waitcnt lgkmcnt(5)
	v_mfma_f32_32x32x16_bf16 v[2:17], v[26:29], v[110:113], v[2:17]
	s_waitcnt lgkmcnt(4)
	v_mfma_f32_32x32x16_bf16 v[2:17], v[30:33], v[114:117], v[2:17]
	v_max_i32_e32 v200, 0, v180
	v_fmac_f32_e32 v136, v67, v200
	v_max_i32_e32 v200, 0, v181
	v_fmac_f32_e32 v135, v67, v200
	v_max_i32_e32 v200, 0, v182
	v_fmac_f32_e32 v134, v67, v200
	v_max_i32_e32 v200, 0, v183
	v_fmac_f32_e32 v65, v67, v200
	v_max_i32_e32 v200, 0, v184
	v_fmac_f32_e32 v64, v67, v200
	v_max_i32_e32 v200, 0, v185
	v_fmac_f32_e32 v63, v67, v200
	v_max_i32_e32 v200, 0, v186
	v_fmac_f32_e32 v62, v67, v200
	v_max_i32_e32 v200, 0, v187
	v_fmac_f32_e32 v61, v67, v200
	v_max_i32_e32 v200, 0, v188
	v_fmac_f32_e32 v60, v67, v200
	v_max_i32_e32 v200, 0, v189
	v_fmac_f32_e32 v59, v67, v200
	v_max_i32_e32 v200, 0, v190
	v_fmac_f32_e32 v58, v67, v200
	v_max_i32_e32 v200, 0, v191
	v_fmac_f32_e32 v57, v67, v200
	v_max_i32_e32 v200, 0, v192
	v_fmac_f32_e32 v56, v67, v200
	v_max_i32_e32 v200, 0, v193
	v_fmac_f32_e32 v55, v67, v200
	v_max_i32_e32 v200, 0, v194
	v_fmac_f32_e32 v54, v67, v200
	v_max_i32_e32 v200, 0, v195
	v_fmac_f32_e32 v53, v67, v200
	s_waitcnt lgkmcnt(3)
	v_mfma_f32_32x32x16_bf16 v[180:195], v[18:21], v[118:121], 0
	s_waitcnt lgkmcnt(2)
	v_mfma_f32_32x32x16_bf16 v[180:195], v[22:25], v[122:125], v[180:195]
	s_waitcnt lgkmcnt(1)
	v_mfma_f32_32x32x16_bf16 v[180:195], v[26:29], v[126:129], v[180:195]
	s_waitcnt lgkmcnt(0)
	v_mfma_f32_32x32x16_bf16 v[180:195], v[30:33], v[130:133], v[180:195]
	v_max_i32_e32 v200, 0, v2
	v_fmac_f32_e32 v136, v68, v200
	v_max_i32_e32 v200, 0, v3
	v_fmac_f32_e32 v135, v68, v200
	v_max_i32_e32 v200, 0, v4
	v_fmac_f32_e32 v134, v68, v200
	v_max_i32_e32 v200, 0, v5
	v_fmac_f32_e32 v65, v68, v200
	v_max_i32_e32 v200, 0, v6
	v_fmac_f32_e32 v64, v68, v200
	v_max_i32_e32 v200, 0, v7
	v_fmac_f32_e32 v63, v68, v200
	v_max_i32_e32 v200, 0, v8
	v_fmac_f32_e32 v62, v68, v200
	v_max_i32_e32 v200, 0, v9
	v_fmac_f32_e32 v61, v68, v200
	v_max_i32_e32 v200, 0, v10
	v_fmac_f32_e32 v60, v68, v200
	v_max_i32_e32 v200, 0, v11
	v_fmac_f32_e32 v59, v68, v200
	v_max_i32_e32 v200, 0, v12
	v_fmac_f32_e32 v58, v68, v200
	v_max_i32_e32 v200, 0, v13
	v_fmac_f32_e32 v57, v68, v200
	v_max_i32_e32 v200, 0, v14
	v_fmac_f32_e32 v56, v68, v200
	v_max_i32_e32 v200, 0, v15
	v_fmac_f32_e32 v55, v68, v200
	v_max_i32_e32 v200, 0, v16
	v_fmac_f32_e32 v54, v68, v200
	v_max_i32_e32 v200, 0, v17
	v_fmac_f32_e32 v53, v68, v200
	v_max_i32_e32 v200, 0, v180
	v_fmac_f32_e32 v136, v69, v200
	v_max_i32_e32 v200, 0, v181
	v_fmac_f32_e32 v135, v69, v200
	v_max_i32_e32 v200, 0, v182
	v_fmac_f32_e32 v134, v69, v200
	v_max_i32_e32 v200, 0, v183
	v_fmac_f32_e32 v65, v69, v200
	v_max_i32_e32 v200, 0, v184
	v_fmac_f32_e32 v64, v69, v200
	v_max_i32_e32 v200, 0, v185
	v_fmac_f32_e32 v63, v69, v200
	v_max_i32_e32 v200, 0, v186
	v_fmac_f32_e32 v62, v69, v200
	v_max_i32_e32 v200, 0, v187
	v_fmac_f32_e32 v61, v69, v200
	v_max_i32_e32 v200, 0, v188
	v_fmac_f32_e32 v60, v69, v200
	v_max_i32_e32 v200, 0, v189
	v_fmac_f32_e32 v59, v69, v200
	v_max_i32_e32 v200, 0, v190
	v_fmac_f32_e32 v58, v69, v200
	v_max_i32_e32 v200, 0, v191
	v_fmac_f32_e32 v57, v69, v200
	v_max_i32_e32 v200, 0, v192
	v_fmac_f32_e32 v56, v69, v200
	v_max_i32_e32 v200, 0, v193
	v_fmac_f32_e32 v55, v69, v200
	v_max_i32_e32 v200, 0, v194
	v_fmac_f32_e32 v54, v69, v200
	v_max_i32_e32 v200, 0, v195
	v_fmac_f32_e32 v53, v69, v200
	s_cbranch_vccz .LBB0_714
; #define LAS __attribute__((address_space(3)))
; __device__ __forceinline__ int crow(int r, int hi) { return (r & 3) + 8 * (r >> 2) + 4 * hi; }
; __device__ __forceinline__ int ibin_u_m160(unsigned u) {
;     const int a = (int)u >> 20;
;     return imed3(-953 - a, 0, 159) + imed3(a - 936, 0, 158) + imed3((int)u, -160, 1);
; }
; template <int PASS, bool DIAG> __device__ __forceinline__ void idx_half(unsigned& bits, unsigned& ebits, const f32x16& sc, int sbase, int tq, int r32, int hi, unsigned khi, unsigned klo, bool cand, LAS unsigned char* L) {
;     ...
;     if (PASS == 1) {
;         LAS unsigned* H = (LAS unsigned*)(L + IL_HIST) + r32 * HSTR + 160;
; #pragma unroll
;         for (int r = 0; r < 16; ++r) { int b = ibin_u_m160(__float_as_uint(sc[r] + 0.0f)); asm("" : "+v"(b));
;             if (!DIAG || crow(r, 0) <= d) __hip_atomic_fetch_add(H + b, 1u, __ATOMIC_RELAXED, __HIP_MEMORY_SCOPE_WORKGROUP); }
	v_ashrrev_i32_e32 v3, 20, v136
	v_sub_u32_e32 v4, 0xfffffc47, v3
	v_med3_i32 v3, v3, s88, v233
	v_med3_i32 v2, v136, s89, 1
	v_med3_i32 v4, v4, 0, v232
	v_add_u32_e32 v2, v2, v3
	v_add3_u32 v2, v2, v4, s92
	v_lshl_add_u32 v2, v2, 2, v0
	ds_add_u32 v2, v229 offset:1152
	v_ashrrev_i32_e32 v3, 20, v135
	v_sub_u32_e32 v4, 0xfffffc47, v3
	v_med3_i32 v3, v3, s88, v233
	v_med3_i32 v2, v135, s89, 1
	v_med3_i32 v4, v4, 0, v232
	v_add_u32_e32 v2, v2, v3
	v_add3_u32 v2, v2, v4, s92
	s_mov_b64 s[16:17], -1
	v_lshl_add_u32 v2, v2, 2, v0
	ds_add_u32 v2, v229 offset:1152
	v_ashrrev_i32_e32 v3, 20, v134
	v_sub_u32_e32 v4, 0xfffffc47, v3
	v_med3_i32 v3, v3, s88, v233
	v_med3_i32 v2, v134, s89, 1
	v_med3_i32 v4, v4, 0, v232
	v_add_u32_e32 v2, v2, v3
	v_add3_u32 v2, v2, v4, s92
	v_lshl_add_u32 v2, v2, 2, v0
	ds_add_u32 v2, v229 offset:1152
	v_ashrrev_i32_e32 v3, 20, v65
	v_sub_u32_e32 v4, 0xfffffc47, v3
	v_med3_i32 v3, v3, s88, v233
	v_med3_i32 v2, v65, s89, 1
	v_med3_i32 v4, v4, 0, v232
	v_add_u32_e32 v2, v2, v3
	v_add3_u32 v2, v2, v4, s92
	v_lshl_add_u32 v2, v2, 2, v0
	ds_add_u32 v2, v229 offset:1152
	v_ashrrev_i32_e32 v3, 20, v64
	v_sub_u32_e32 v4, 0xfffffc47, v3
	v_med3_i32 v3, v3, s88, v233
	v_med3_i32 v2, v64, s89, 1
	v_med3_i32 v4, v4, 0, v232
	v_add_u32_e32 v2, v2, v3
	v_add3_u32 v2, v2, v4, s92
	v_lshl_add_u32 v2, v2, 2, v0
	ds_add_u32 v2, v229 offset:1152
	v_ashrrev_i32_e32 v3, 20, v63
	v_sub_u32_e32 v4, 0xfffffc47, v3
	v_med3_i32 v3, v3, s88, v233
	v_med3_i32 v2, v63, s89, 1
	v_med3_i32 v4, v4, 0, v232
	v_add_u32_e32 v2, v2, v3
	v_add3_u32 v2, v2, v4, s92
	v_lshl_add_u32 v2, v2, 2, v0
	ds_add_u32 v2, v229 offset:1152
	v_ashrrev_i32_e32 v3, 20, v62
	v_sub_u32_e32 v4, 0xfffffc47, v3
	v_med3_i32 v3, v3, s88, v233
	v_med3_i32 v2, v62, s89, 1
	v_med3_i32 v4, v4, 0, v232
	v_add_u32_e32 v2, v2, v3
	v_add3_u32 v2, v2, v4, s92
	v_lshl_add_u32 v2, v2, 2, v0
	ds_add_u32 v2, v229 offset:1152
	v_ashrrev_i32_e32 v3, 20, v61
	v_sub_u32_e32 v4, 0xfffffc47, v3
	v_med3_i32 v3, v3, s88, v233
	v_med3_i32 v2, v61, s89, 1
	v_med3_i32 v4, v4, 0, v232
	v_add_u32_e32 v2, v2, v3
	v_add3_u32 v2, v2, v4, s92
	v_lshl_add_u32 v2, v2, 2, v0
	ds_add_u32 v2, v229 offset:1152
	v_ashrrev_i32_e32 v3, 20, v60
	v_sub_u32_e32 v4, 0xfffffc47, v3
	v_med3_i32 v3, v3, s88, v233
	v_med3_i32 v2, v60, s89, 1
	v_med3_i32 v4, v4, 0, v232
	v_add_u32_e32 v2, v2, v3
	v_add3_u32 v2, v2, v4, s92
	v_lshl_add_u32 v2, v2, 2, v0
	ds_add_u32 v2, v229 offset:1152
	v_ashrrev_i32_e32 v3, 20, v59
	v_sub_u32_e32 v4, 0xfffffc47, v3
	v_med3_i32 v3, v3, s88, v233
	v_med3_i32 v2, v59, s89, 1
	v_med3_i32 v4, v4, 0, v232
	v_add_u32_e32 v2, v2, v3
	v_add3_u32 v2, v2, v4, s92
	v_lshl_add_u32 v2, v2, 2, v0
	ds_add_u32 v2, v229 offset:1152
	v_ashrrev_i32_e32 v3, 20, v58
	v_sub_u32_e32 v4, 0xfffffc47, v3
	v_med3_i32 v3, v3, s88, v233
	v_med3_i32 v2, v58, s89, 1
	v_med3_i32 v4, v4, 0, v232
	v_add_u32_e32 v2, v2, v3
	v_add3_u32 v2, v2, v4, s92
	v_lshl_add_u32 v2, v2, 2, v0
	ds_add_u32 v2, v229 offset:1152
	v_ashrrev_i32_e32 v3, 20, v57
	v_sub_u32_e32 v4, 0xfffffc47, v3
	v_med3_i32 v3, v3, s88, v233
	v_med3_i32 v2, v57, s89, 1
	v_med3_i32 v4, v4, 0, v232
	v_add_u32_e32 v2, v2, v3
	v_add3_u32 v2, v2, v4, s92
	v_lshl_add_u32 v2, v2, 2, v0
	ds_add_u32 v2, v229 offset:1152
	v_ashrrev_i32_e32 v3, 20, v56
	v_sub_u32_e32 v4, 0xfffffc47, v3
	v_med3_i32 v3, v3, s88, v233
	v_med3_i32 v2, v56, s89, 1
	v_med3_i32 v4, v4, 0, v232
	v_add_u32_e32 v2, v2, v3
	v_add3_u32 v2, v2, v4, s92
	v_lshl_add_u32 v2, v2, 2, v0
	ds_add_u32 v2, v229 offset:1152
	v_ashrrev_i32_e32 v3, 20, v55
	v_sub_u32_e32 v4, 0xfffffc47, v3
	v_med3_i32 v3, v3, s88, v233
	v_med3_i32 v2, v55, s89, 1
	v_med3_i32 v4, v4, 0, v232
	v_add_u32_e32 v2, v2, v3
	v_add3_u32 v2, v2, v4, s92
	v_lshl_add_u32 v2, v2, 2, v0
	ds_add_u32 v2, v229 offset:1152
	v_ashrrev_i32_e32 v3, 20, v54
	v_sub_u32_e32 v4, 0xfffffc47, v3
	v_med3_i32 v3, v3, s88, v233
	v_med3_i32 v2, v54, s89, 1
	v_med3_i32 v4, v4, 0, v232
	v_add_u32_e32 v2, v2, v3
	v_add3_u32 v2, v2, v4, s92
	v_lshl_add_u32 v2, v2, 2, v0
	ds_add_u32 v2, v229 offset:1152
	v_ashrrev_i32_e32 v3, 20, v53
	v_sub_u32_e32 v4, 0xfffffc47, v3
	v_med3_i32 v3, v3, s88, v233
	v_med3_i32 v2, v53, s89, 1
	v_med3_i32 v4, v4, 0, v232
	v_add_u32_e32 v2, v2, v3
	v_add3_u32 v2, v2, v4, s92
	s_cbranch_execz .LBB0_715
	s_branch .LBB0_746

; __device__ __forceinline__ float relu_i(float p) { const int i = __float_as_int(p); return __int_as_float(i > 0 ? i : 0); }
; __device__ __forceinline__ void idx_scores_k(f32x16& sc, const bf16x8 (&kf)[4], const bf16x8 (&qf)[16], const f32x4& w) {
;     f32x16 p0 = f32x16{}, p1 = f32x16{};
; #pragma unroll
;     for (int d0 = 0; d0 < 4; ++d0) p0 = __builtin_amdgcn_mfma_f32_32x32x16_bf16(kf[d0], qf[d0], p0, 0, 0, 0);
; #pragma unroll
;     for (int d0 = 0; d0 < 4; ++d0) p1 = __builtin_amdgcn_mfma_f32_32x32x16_bf16(kf[d0], qf[4 + d0], p1, 0, 0, 0);
; #pragma unroll
;     for (int r = 0; r < 16; ++r) sc[r] = w[0] * relu_i(p0[r]);
;     p0 = f32x16{};
; #pragma unroll
;     for (int d0 = 0; d0 < 4; ++d0) p0 = __builtin_amdgcn_mfma_f32_32x32x16_bf16(kf[d0], qf[8 + d0], p0, 0, 0, 0);
; #pragma unroll
;     for (int r = 0; r < 16; ++r) sc[r] = fmaf(w[1], relu_i(p1[r]), sc[r]);
;     p1 = f32x16{};
; #pragma unroll
;     for (int d0 = 0; d0 < 4; ++d0) p1 = __builtin_amdgcn_mfma_f32_32x32x16_bf16(kf[d0], qf[12 + d0], p1, 0, 0, 0);
; #pragma unroll
;     for (int r = 0; r < 16; ++r) sc[r] = fmaf(w[2], relu_i(p0[r]), sc[r]);
; #pragma unroll
;     for (int r = 0; r < 16; ++r) sc[r] = fmaf(w[3], relu_i(p1[r]), sc[r]);
; }
.LBB0_750:
	s_and_b64 vcc, exec, s[14:15]
	s_waitcnt vmcnt(3)
	v_mfma_f32_32x32x16_bf16 v[2:17], v[46:49], v[70:73], 0
	s_waitcnt vmcnt(2)
	v_mfma_f32_32x32x16_bf16 v[2:17], v[42:45], v[74:77], v[2:17]
	s_waitcnt vmcnt(1)
	v_mfma_f32_32x32x16_bf16 v[2:17], v[38:41], v[78:81], v[2:17]
	s_waitcnt vmcnt(0)
	v_mfma_f32_32x32x16_bf16 v[2:17], v[34:37], v[82:85], v[2:17]
	v_mfma_f32_32x32x16_bf16 v[180:195], v[46:49], v[86:89], 0
	v_mfma_f32_32x32x16_bf16 v[180:195], v[42:45], v[90:93], v[180:195]
	v_mfma_f32_32x32x16_bf16 v[180:195], v[38:41], v[94:97], v[180:195]
	v_mfma_f32_32x32x16_bf16 v[180:195], v[34:37], v[98:101], v[180:195]
	s_nop 7
	v_max_i32_e32 v200, 0, v2
	v_fma_f32 v136, v66, v200, 0
	v_max_i32_e32 v200, 0, v3
	v_fma_f32 v135, v66, v200, 0
	v_max_i32_e32 v200, 0, v4
	v_fma_f32 v134, v66, v200, 0
	v_max_i32_e32 v200, 0, v5
	v_fma_f32 v65, v66, v200, 0
	v_max_i32_e32 v200, 0, v6
	v_fma_f32 v64, v66, v200, 0
	v_max_i32_e32 v200, 0, v7
	v_fma_f32 v63, v66, v200, 0
	v_max_i32_e32 v200, 0, v8
	v_fma_f32 v62, v66, v200, 0
	v_max_i32_e32 v200, 0, v9
	v_fma_f32 v61, v66, v200, 0
	v_max_i32_e32 v200, 0, v10
	v_fma_f32 v60, v66, v200, 0
	v_max_i32_e32 v200, 0, v11
	v_fma_f32 v59, v66, v200, 0
	v_max_i32_e32 v200, 0, v12
	v_fma_f32 v58, v66, v200, 0
	v_max_i32_e32 v200, 0, v13
	v_fma_f32 v57, v66, v200, 0
	v_max_i32_e32 v200, 0, v14
	v_fma_f32 v56, v66, v200, 0
	v_max_i32_e32 v200, 0, v15
	v_fma_f32 v55, v66, v200, 0
	v_max_i32_e32 v200, 0, v16
	v_fma_f32 v54, v66, v200, 0
	v_max_i32_e32 v200, 0, v17
	v_fma_f32 v53, v66, v200, 0
	v_mfma_f32_32x32x16_bf16 v[2:17], v[46:49], v[102:105], 0
	v_mfma_f32_32x32x16_bf16 v[2:17], v[42:45], v[106:109], v[2:17]
	v_mfma_f32_32x32x16_bf16 v[2:17], v[38:41], v[110:113], v[2:17]
	v_mfma_f32_32x32x16_bf16 v[2:17], v[34:37], v[114:117], v[2:17]
	v_max_i32_e32 v200, 0, v180
	v_fmac_f32_e32 v136, v67, v200
	v_max_i32_e32 v200, 0, v181
	v_fmac_f32_e32 v135, v67, v200
	v_max_i32_e32 v200, 0, v182
	v_fmac_f32_e32 v134, v67, v200
	v_max_i32_e32 v200, 0, v183
	v_fmac_f32_e32 v65, v67, v200
	v_max_i32_e32 v200, 0, v184
	v_fmac_f32_e32 v64, v67, v200
	v_max_i32_e32 v200, 0, v185
	v_fmac_f32_e32 v63, v67, v200
	v_max_i32_e32 v200, 0, v186
	v_fmac_f32_e32 v62, v67, v200
	v_max_i32_e32 v200, 0, v187
	v_fmac_f32_e32 v61, v67, v200
	v_max_i32_e32 v200, 0, v188
	v_fmac_f32_e32 v60, v67, v200
	v_max_i32_e32 v200, 0, v189
	v_fmac_f32_e32 v59, v67, v200
	v_max_i32_e32 v200, 0, v190
	v_fmac_f32_e32 v58, v67, v200
	v_max_i32_e32 v200, 0, v191
	v_fmac_f32_e32 v57, v67, v200
	v_max_i32_e32 v200, 0, v192
	v_fmac_f32_e32 v56, v67, v200
	v_max_i32_e32 v200, 0, v193
	v_fmac_f32_e32 v55, v67, v200
	v_max_i32_e32 v200, 0, v194
	v_fmac_f32_e32 v54, v67, v200
	v_max_i32_e32 v200, 0, v195
	v_fmac_f32_e32 v53, v67, v200
	v_mfma_f32_32x32x16_bf16 v[180:195], v[46:49], v[118:121], 0
	v_mfma_f32_32x32x16_bf16 v[180:195], v[42:45], v[122:125], v[180:195]
	v_mfma_f32_32x32x16_bf16 v[180:195], v[38:41], v[126:129], v[180:195]
	v_mfma_f32_32x32x16_bf16 v[180:195], v[34:37], v[130:133], v[180:195]
	v_max_i32_e32 v200, 0, v2
	v_fmac_f32_e32 v136, v68, v200
	v_max_i32_e32 v200, 0, v3
	v_fmac_f32_e32 v135, v68, v200
	v_max_i32_e32 v200, 0, v4
	v_fmac_f32_e32 v134, v68, v200
	v_max_i32_e32 v200, 0, v5
	v_fmac_f32_e32 v65, v68, v200
	v_max_i32_e32 v200, 0, v6
	v_fmac_f32_e32 v64, v68, v200
	v_max_i32_e32 v200, 0, v7
	v_fmac_f32_e32 v63, v68, v200
	v_max_i32_e32 v200, 0, v8
	v_fmac_f32_e32 v62, v68, v200
	v_max_i32_e32 v200, 0, v9
	v_fmac_f32_e32 v61, v68, v200
	v_max_i32_e32 v200, 0, v10
	v_fmac_f32_e32 v60, v68, v200
	v_max_i32_e32 v200, 0, v11
	v_fmac_f32_e32 v59, v68, v200
	v_max_i32_e32 v200, 0, v12
	v_fmac_f32_e32 v58, v68, v200
	v_max_i32_e32 v200, 0, v13
	v_fmac_f32_e32 v57, v68, v200
	v_max_i32_e32 v200, 0, v14
	v_fmac_f32_e32 v56, v68, v200
	v_max_i32_e32 v200, 0, v15
	v_fmac_f32_e32 v55, v68, v200
	v_max_i32_e32 v200, 0, v16
	v_fmac_f32_e32 v54, v68, v200
	v_max_i32_e32 v200, 0, v17
	v_fmac_f32_e32 v53, v68, v200
	v_max_i32_e32 v200, 0, v180
	v_fmac_f32_e32 v136, v69, v200
	v_max_i32_e32 v200, 0, v181
	v_fmac_f32_e32 v135, v69, v200
	v_max_i32_e32 v200, 0, v182
	v_fmac_f32_e32 v134, v69, v200
	v_max_i32_e32 v200, 0, v183
	v_fmac_f32_e32 v65, v69, v200
	v_max_i32_e32 v200, 0, v184
	v_fmac_f32_e32 v64, v69, v200
	v_max_i32_e32 v200, 0, v185
	v_fmac_f32_e32 v63, v69, v200
	v_max_i32_e32 v200, 0, v186
	v_fmac_f32_e32 v62, v69, v200
	v_max_i32_e32 v200, 0, v187
	v_fmac_f32_e32 v61, v69, v200
	v_max_i32_e32 v200, 0, v188
	v_fmac_f32_e32 v60, v69, v200
	v_max_i32_e32 v200, 0, v189
	v_fmac_f32_e32 v59, v69, v200
	v_max_i32_e32 v200, 0, v190
	v_fmac_f32_e32 v58, v69, v200
	v_max_i32_e32 v200, 0, v191
	v_fmac_f32_e32 v57, v69, v200
	v_max_i32_e32 v200, 0, v192
	v_fmac_f32_e32 v56, v69, v200
	v_max_i32_e32 v200, 0, v193
	v_fmac_f32_e32 v55, v69, v200
	v_max_i32_e32 v200, 0, v194
	v_fmac_f32_e32 v54, v69, v200
	v_max_i32_e32 v200, 0, v195
	v_fmac_f32_e32 v53, v69, v200
	s_cbranch_vccz .LBB0_752
; #define LAS __attribute__((address_space(3)))
; __device__ __forceinline__ int crow(int r, int hi) { return (r & 3) + 8 * (r >> 2) + 4 * hi; }
; __device__ __forceinline__ int ibin_u_m160(unsigned u) {
;     const int a = (int)u >> 20;
;     return imed3(-953 - a, 0, 159) + imed3(a - 936, 0, 158) + imed3((int)u, -160, 1);
; }
; template <int PASS, bool DIAG> __device__ __forceinline__ void idx_half(unsigned& bits, unsigned& ebits, const f32x16& sc, int sbase, int tq, int r32, int hi, unsigned khi, unsigned klo, bool cand, LAS unsigned char* L) {
;     bits = 0u; ebits = 0u;
;     const int d = tq - sbase - 4 * hi;
;     if (PASS == 1) {
;         LAS unsigned* H = (LAS unsigned*)(L + IL_HIST) + r32 * HSTR + 160;
; #pragma unroll
;         for (int r = 0; r < 16; ++r) { int b = ibin_u_m160(__float_as_uint(sc[r] + 0.0f)); asm("" : "+v"(b));
;             if (!DIAG || crow(r, 0) <= d) __hip_atomic_fetch_add(H + b, 1u, __ATOMIC_RELAXED, __HIP_MEMORY_SCOPE_WORKGROUP); }
	v_ashrrev_i32_e32 v3, 20, v136
	v_sub_u32_e32 v4, 0xfffffc47, v3
	v_med3_i32 v3, v3, s88, v233
	v_med3_i32 v2, v136, s89, 1
	v_med3_i32 v4, v4, 0, v232
	v_add_u32_e32 v2, v2, v3
	v_add3_u32 v2, v2, v4, s92
	v_lshl_add_u32 v2, v2, 2, v0
	ds_add_u32 v2, v229 offset:1152
	v_ashrrev_i32_e32 v3, 20, v135
	v_sub_u32_e32 v4, 0xfffffc47, v3
	v_med3_i32 v3, v3, s88, v233
	v_med3_i32 v2, v135, s89, 1
	v_med3_i32 v4, v4, 0, v232
	v_add_u32_e32 v2, v2, v3
	v_add3_u32 v2, v2, v4, s92
	s_mov_b64 s[14:15], -1
	v_lshl_add_u32 v2, v2, 2, v0
	ds_add_u32 v2, v229 offset:1152
	v_ashrrev_i32_e32 v3, 20, v134
	v_sub_u32_e32 v4, 0xfffffc47, v3
	v_med3_i32 v3, v3, s88, v233
	v_med3_i32 v2, v134, s89, 1
	v_med3_i32 v4, v4, 0, v232
	v_add_u32_e32 v2, v2, v3
	v_add3_u32 v2, v2, v4, s92
	v_lshl_add_u32 v2, v2, 2, v0
	ds_add_u32 v2, v229 offset:1152
	v_ashrrev_i32_e32 v3, 20, v65
	v_sub_u32_e32 v4, 0xfffffc47, v3
	v_med3_i32 v3, v3, s88, v233
	v_med3_i32 v2, v65, s89, 1
	v_med3_i32 v4, v4, 0, v232
	v_add_u32_e32 v2, v2, v3
	v_add3_u32 v2, v2, v4, s92
	v_lshl_add_u32 v2, v2, 2, v0
	ds_add_u32 v2, v229 offset:1152
	v_ashrrev_i32_e32 v3, 20, v64
	v_sub_u32_e32 v4, 0xfffffc47, v3
	v_med3_i32 v3, v3, s88, v233
	v_med3_i32 v2, v64, s89, 1
	v_med3_i32 v4, v4, 0, v232
	v_add_u32_e32 v2, v2, v3
	v_add3_u32 v2, v2, v4, s92
	v_lshl_add_u32 v2, v2, 2, v0
	ds_add_u32 v2, v229 offset:1152
	v_ashrrev_i32_e32 v3, 20, v63
	v_sub_u32_e32 v4, 0xfffffc47, v3
	v_med3_i32 v3, v3, s88, v233
	v_med3_i32 v2, v63, s89, 1
	v_med3_i32 v4, v4, 0, v232
	v_add_u32_e32 v2, v2, v3
	v_add3_u32 v2, v2, v4, s92
	v_lshl_add_u32 v2, v2, 2, v0
	ds_add_u32 v2, v229 offset:1152
	v_ashrrev_i32_e32 v3, 20, v62
	v_sub_u32_e32 v4, 0xfffffc47, v3
	v_med3_i32 v3, v3, s88, v233
	v_med3_i32 v2, v62, s89, 1
	v_med3_i32 v4, v4, 0, v232
	v_add_u32_e32 v2, v2, v3
	v_add3_u32 v2, v2, v4, s92
	v_lshl_add_u32 v2, v2, 2, v0
	ds_add_u32 v2, v229 offset:1152
	v_ashrrev_i32_e32 v3, 20, v61
	v_sub_u32_e32 v4, 0xfffffc47, v3
	v_med3_i32 v3, v3, s88, v233
	v_med3_i32 v2, v61, s89, 1
	v_med3_i32 v4, v4, 0, v232
	v_add_u32_e32 v2, v2, v3
	v_add3_u32 v2, v2, v4, s92
	v_lshl_add_u32 v2, v2, 2, v0
	ds_add_u32 v2, v229 offset:1152
	v_ashrrev_i32_e32 v3, 20, v60
	v_sub_u32_e32 v4, 0xfffffc47, v3
	v_med3_i32 v3, v3, s88, v233
	v_med3_i32 v2, v60, s89, 1
	v_med3_i32 v4, v4, 0, v232
	v_add_u32_e32 v2, v2, v3
	v_add3_u32 v2, v2, v4, s92
	v_lshl_add_u32 v2, v2, 2, v0
	ds_add_u32 v2, v229 offset:1152
	v_ashrrev_i32_e32 v3, 20, v59
	v_sub_u32_e32 v4, 0xfffffc47, v3
	v_med3_i32 v3, v3, s88, v233
	v_med3_i32 v2, v59, s89, 1
	v_med3_i32 v4, v4, 0, v232
	v_add_u32_e32 v2, v2, v3
	v_add3_u32 v2, v2, v4, s92
	v_lshl_add_u32 v2, v2, 2, v0
	ds_add_u32 v2, v229 offset:1152
	v_ashrrev_i32_e32 v3, 20, v58
	v_sub_u32_e32 v4, 0xfffffc47, v3
	v_med3_i32 v3, v3, s88, v233
	v_med3_i32 v2, v58, s89, 1
	v_med3_i32 v4, v4, 0, v232
	v_add_u32_e32 v2, v2, v3
	v_add3_u32 v2, v2, v4, s92
	v_lshl_add_u32 v2, v2, 2, v0
	ds_add_u32 v2, v229 offset:1152
	v_ashrrev_i32_e32 v3, 20, v57
	v_sub_u32_e32 v4, 0xfffffc47, v3
	v_med3_i32 v3, v3, s88, v233
	v_med3_i32 v2, v57, s89, 1
	v_med3_i32 v4, v4, 0, v232
	v_add_u32_e32 v2, v2, v3
	v_add3_u32 v2, v2, v4, s92
	v_lshl_add_u32 v2, v2, 2, v0
	ds_add_u32 v2, v229 offset:1152
	v_ashrrev_i32_e32 v3, 20, v56
	v_sub_u32_e32 v4, 0xfffffc47, v3
	v_med3_i32 v3, v3, s88, v233
	v_med3_i32 v2, v56, s89, 1
	v_med3_i32 v4, v4, 0, v232
	v_add_u32_e32 v2, v2, v3
	v_add3_u32 v2, v2, v4, s92
	v_lshl_add_u32 v2, v2, 2, v0
	ds_add_u32 v2, v229 offset:1152
	v_ashrrev_i32_e32 v3, 20, v55
	v_sub_u32_e32 v4, 0xfffffc47, v3
	v_med3_i32 v3, v3, s88, v233
	v_med3_i32 v2, v55, s89, 1
	v_med3_i32 v4, v4, 0, v232
	v_add_u32_e32 v2, v2, v3
	v_add3_u32 v2, v2, v4, s92
	v_lshl_add_u32 v2, v2, 2, v0
	ds_add_u32 v2, v229 offset:1152
	v_ashrrev_i32_e32 v3, 20, v54
	v_sub_u32_e32 v4, 0xfffffc47, v3
	v_med3_i32 v3, v3, s88, v233
	v_med3_i32 v2, v54, s89, 1
	v_med3_i32 v4, v4, 0, v232
	v_add_u32_e32 v2, v2, v3
	v_add3_u32 v2, v2, v4, s92
	v_lshl_add_u32 v2, v2, 2, v0
	ds_add_u32 v2, v229 offset:1152
	v_ashrrev_i32_e32 v3, 20, v53
	v_sub_u32_e32 v4, 0xfffffc47, v3
	v_med3_i32 v3, v3, s88, v233
	v_med3_i32 v2, v53, s89, 1
	v_med3_i32 v4, v4, 0, v232
	v_add_u32_e32 v2, v2, v3
	v_add3_u32 v3, v2, v4, s92
	s_cbranch_execz .LBB0_753
	s_branch .LBB0_784

; __device__ __forceinline__ float relu_i(float p) { const int i = __float_as_int(p); return __int_as_float(i > 0 ? i : 0); }
; __device__ __forceinline__ void idx_scores_k(f32x16& sc, const bf16x8 (&kf)[4], const bf16x8 (&qf)[16], const f32x4& w) {
;     f32x16 p0 = f32x16{}, p1 = f32x16{};
; #pragma unroll
;     for (int d0 = 0; d0 < 4; ++d0) p0 = __builtin_amdgcn_mfma_f32_32x32x16_bf16(kf[d0], qf[d0], p0, 0, 0, 0);
; #pragma unroll
;     for (int d0 = 0; d0 < 4; ++d0) p1 = __builtin_amdgcn_mfma_f32_32x32x16_bf16(kf[d0], qf[4 + d0], p1, 0, 0, 0);
; #pragma unroll
;     for (int r = 0; r < 16; ++r) sc[r] = w[0] * relu_i(p0[r]);
;     p0 = f32x16{};
; #pragma unroll
;     for (int d0 = 0; d0 < 4; ++d0) p0 = __builtin_amdgcn_mfma_f32_32x32x16_bf16(kf[d0], qf[8 + d0], p0, 0, 0, 0);
; #pragma unroll
;     for (int r = 0; r < 16; ++r) sc[r] = fmaf(w[1], relu_i(p1[r]), sc[r]);
;     p1 = f32x16{};
; #pragma unroll
;     for (int d0 = 0; d0 < 4; ++d0) p1 = __builtin_amdgcn_mfma_f32_32x32x16_bf16(kf[d0], qf[12 + d0], p1, 0, 0, 0);
; #pragma unroll
;     for (int r = 0; r < 16; ++r) sc[r] = fmaf(w[2], relu_i(p0[r]), sc[r]);
; #pragma unroll
;     for (int r = 0; r < 16; ++r) sc[r] = fmaf(w[3], relu_i(p1[r]), sc[r]);
; }
; template <int PASS> __device__ __forceinline__ void idx_pass(const bf16_t* KIb, const bf16x8 (&qf)[16], const f32x4& w, int jd, int tq, int wid, int r32, int hi, unsigned khi, unsigned klo, bool cand, LAS unsigned char* L) {
;     ...
;     for (; j <= jd; j += 8) {
;         const bool diag = (j == jd);
;         idx_loadk(kB, KIb + (size_t)(j * 64 + 32) * 64, r32, hi);
;         f32x16 sc; idx_scores_k(sc, kA, qf, w);
;         unsigned lo, elo, hw, ehw;
;         if (diag) idx_half<PASS, true>(lo, elo, sc, j * 64, tq, r32, hi, khi, klo, cand, L); else idx_half<PASS, false>(lo, elo, sc, j * 64, tq, r32, hi, khi, klo, cand, L);
;         if (j + 8 <= jd) idx_loadk(kA, KIb + (size_t)((j + 8) * 64) * 64, r32, hi);
;         idx_scores_k(sc, kB, qf, w);
;         if (diag) idx_half<PASS, true>(hw, ehw, sc, j * 64 + 32, tq, r32, hi, khi, klo, cand, L); else idx_half<PASS, false>(hw, ehw, sc, j * 64 + 32, tq, r32, hi, khi, klo, cand, L);
.LBB0_1064:
	s_add_i32 s0, s46, s44
	s_cmp_lg_u32 s0, 8
	s_cselect_b64 s[18:19], -1, 0
	s_add_i32 s0, s16, 0xfffffe20
	s_ashr_i32 s1, s0, 31
	s_lshl_b64 s[0:1], s[0:1], 7
	v_lshl_add_u64 v[2:3], v[50:51], 0, s[0:1]
	global_load_dwordx4 v[46:49], v[2:3], off
	global_load_dwordx4 v[42:45], v[2:3], off offset:32
	global_load_dwordx4 v[38:41], v[2:3], off offset:64
	global_load_dwordx4 v[34:37], v[2:3], off offset:96
	s_mov_b64 s[14:15], -1
	s_and_b64 vcc, exec, s[18:19]
	s_waitcnt vmcnt(7)
	v_mfma_f32_32x32x16_bf16 v[2:17], v[18:21], v[70:73], 0
	s_waitcnt vmcnt(6)
	v_mfma_f32_32x32x16_bf16 v[2:17], v[22:25], v[74:77], v[2:17]
	s_waitcnt vmcnt(5)
	v_mfma_f32_32x32x16_bf16 v[2:17], v[26:29], v[78:81], v[2:17]
	s_waitcnt vmcnt(4)
	v_mfma_f32_32x32x16_bf16 v[2:17], v[30:33], v[82:85], v[2:17]
	v_mfma_f32_32x32x16_bf16 v[180:195], v[18:21], v[86:89], 0
	v_mfma_f32_32x32x16_bf16 v[180:195], v[22:25], v[90:93], v[180:195]
	v_mfma_f32_32x32x16_bf16 v[180:195], v[26:29], v[94:97], v[180:195]
	v_mfma_f32_32x32x16_bf16 v[180:195], v[30:33], v[98:101], v[180:195]
	s_nop 7
	v_max_i32_e32 v200, 0, v2
	v_fma_f32 v144, v66, v200, 0
	v_max_i32_e32 v200, 0, v3
	v_fma_f32 v145, v66, v200, 0
	v_max_i32_e32 v200, 0, v4
	v_fma_f32 v146, v66, v200, 0
	v_max_i32_e32 v200, 0, v5
	v_fma_f32 v147, v66, v200, 0
	v_max_i32_e32 v200, 0, v6
	v_fma_f32 v148, v66, v200, 0
	v_max_i32_e32 v200, 0, v7
	v_fma_f32 v149, v66, v200, 0
	v_max_i32_e32 v200, 0, v8
	v_fma_f32 v150, v66, v200, 0
	v_max_i32_e32 v200, 0, v9
	v_fma_f32 v151, v66, v200, 0
	v_max_i32_e32 v200, 0, v10
	v_fma_f32 v152, v66, v200, 0
	v_max_i32_e32 v200, 0, v11
	v_fma_f32 v153, v66, v200, 0
	v_max_i32_e32 v200, 0, v12
	v_fma_f32 v154, v66, v200, 0
	v_max_i32_e32 v200, 0, v13
	v_fma_f32 v155, v66, v200, 0
	v_max_i32_e32 v200, 0, v14
	v_fma_f32 v156, v66, v200, 0
	v_max_i32_e32 v200, 0, v15
	v_fma_f32 v157, v66, v200, 0
	v_max_i32_e32 v200, 0, v16
	v_fma_f32 v158, v66, v200, 0
	v_max_i32_e32 v200, 0, v17
	v_fma_f32 v159, v66, v200, 0
	v_mfma_f32_32x32x16_bf16 v[2:17], v[18:21], v[102:105], 0
	v_mfma_f32_32x32x16_bf16 v[2:17], v[22:25], v[106:109], v[2:17]
	v_mfma_f32_32x32x16_bf16 v[2:17], v[26:29], v[110:113], v[2:17]
	v_mfma_f32_32x32x16_bf16 v[2:17], v[30:33], v[114:117], v[2:17]
	v_max_i32_e32 v200, 0, v180
	v_fmac_f32_e32 v144, v67, v200
	v_max_i32_e32 v200, 0, v181
	v_fmac_f32_e32 v145, v67, v200
	v_max_i32_e32 v200, 0, v182
	v_fmac_f32_e32 v146, v67, v200
	v_max_i32_e32 v200, 0, v183
	v_fmac_f32_e32 v147, v67, v200
	v_max_i32_e32 v200, 0, v184
	v_fmac_f32_e32 v148, v67, v200
	v_max_i32_e32 v200, 0, v185
	v_fmac_f32_e32 v149, v67, v200
	v_max_i32_e32 v200, 0, v186
	v_fmac_f32_e32 v150, v67, v200
	v_max_i32_e32 v200, 0, v187
	v_fmac_f32_e32 v151, v67, v200
	v_max_i32_e32 v200, 0, v188
	v_fmac_f32_e32 v152, v67, v200
	v_max_i32_e32 v200, 0, v189
	v_fmac_f32_e32 v153, v67, v200
	v_max_i32_e32 v200, 0, v190
	v_fmac_f32_e32 v154, v67, v200
	v_max_i32_e32 v200, 0, v191
	v_fmac_f32_e32 v155, v67, v200
	v_max_i32_e32 v200, 0, v192
	v_fmac_f32_e32 v156, v67, v200
	v_max_i32_e32 v200, 0, v193
	v_fmac_f32_e32 v157, v67, v200
	v_max_i32_e32 v200, 0, v194
	v_fmac_f32_e32 v158, v67, v200
	v_max_i32_e32 v200, 0, v195
	v_fmac_f32_e32 v159, v67, v200
	v_mfma_f32_32x32x16_bf16 v[180:195], v[18:21], v[118:121], 0
	v_mfma_f32_32x32x16_bf16 v[180:195], v[22:25], v[122:125], v[180:195]
	v_mfma_f32_32x32x16_bf16 v[180:195], v[26:29], v[126:129], v[180:195]
	v_mfma_f32_32x32x16_bf16 v[180:195], v[30:33], v[130:133], v[180:195]
	v_max_i32_e32 v200, 0, v2
	v_fmac_f32_e32 v144, v68, v200
	v_max_i32_e32 v200, 0, v3
	v_fmac_f32_e32 v145, v68, v200
	v_max_i32_e32 v200, 0, v4
	v_fmac_f32_e32 v146, v68, v200
	v_max_i32_e32 v200, 0, v5
	v_fmac_f32_e32 v147, v68, v200
	v_max_i32_e32 v200, 0, v6
	v_fmac_f32_e32 v148, v68, v200
	v_max_i32_e32 v200, 0, v7
	v_fmac_f32_e32 v149, v68, v200
	v_max_i32_e32 v200, 0, v8
	v_fmac_f32_e32 v150, v68, v200
	v_max_i32_e32 v200, 0, v9
	v_fmac_f32_e32 v151, v68, v200
	v_max_i32_e32 v200, 0, v10
	v_fmac_f32_e32 v152, v68, v200
	v_max_i32_e32 v200, 0, v11
	v_fmac_f32_e32 v153, v68, v200
	v_max_i32_e32 v200, 0, v12
	v_fmac_f32_e32 v154, v68, v200
	v_max_i32_e32 v200, 0, v13
	v_fmac_f32_e32 v155, v68, v200
	v_max_i32_e32 v200, 0, v14
	v_fmac_f32_e32 v156, v68, v200
	v_max_i32_e32 v200, 0, v15
	v_fmac_f32_e32 v157, v68, v200
	v_max_i32_e32 v200, 0, v16
	v_fmac_f32_e32 v158, v68, v200
	v_max_i32_e32 v200, 0, v17
	v_fmac_f32_e32 v159, v68, v200
	v_max_i32_e32 v200, 0, v180
	v_fmac_f32_e32 v144, v69, v200
	v_max_i32_e32 v200, 0, v181
	v_fmac_f32_e32 v145, v69, v200
	v_max_i32_e32 v200, 0, v182
	v_fmac_f32_e32 v146, v69, v200
	v_max_i32_e32 v200, 0, v183
	v_fmac_f32_e32 v147, v69, v200
	v_max_i32_e32 v200, 0, v184
	v_fmac_f32_e32 v148, v69, v200
	v_max_i32_e32 v200, 0, v185
	v_fmac_f32_e32 v149, v69, v200
	v_max_i32_e32 v200, 0, v186
	v_fmac_f32_e32 v150, v69, v200
	v_max_i32_e32 v200, 0, v187
	v_fmac_f32_e32 v151, v69, v200
	v_max_i32_e32 v200, 0, v188
	v_fmac_f32_e32 v152, v69, v200
	v_max_i32_e32 v200, 0, v189
	v_fmac_f32_e32 v153, v69, v200
	v_max_i32_e32 v200, 0, v190
	v_fmac_f32_e32 v154, v69, v200
	v_max_i32_e32 v200, 0, v191
	v_fmac_f32_e32 v155, v69, v200
	v_max_i32_e32 v200, 0, v192
	v_fmac_f32_e32 v156, v69, v200
	v_max_i32_e32 v200, 0, v193
	v_fmac_f32_e32 v157, v69, v200
	v_max_i32_e32 v200, 0, v194
	v_fmac_f32_e32 v158, v69, v200
	v_max_i32_e32 v200, 0, v195
	v_fmac_f32_e32 v159, v69, v200
	s_cbranch_vccz .LBB0_1263
; #define LAS __attribute__((address_space(3)))
; __device__ __forceinline__ int crow(int r, int hi) { return (r & 3) + 8 * (r >> 2) + 4 * hi; }
; __device__ __forceinline__ unsigned fkey2(float v) { const unsigned u = __float_as_uint(v + 0.0f); return u ^ ((unsigned)((int)u >> 31) | 0x80000000u); }
; __device__ __forceinline__ void shl_ge(unsigned& acc, unsigned key, unsigned thr) { asm("v_cmp_ge_u32 vcc, %1, %2\n\tv_addc_co_u32 %0, vcc, %0, %0, vcc" : "+v"(acc) : "v"(key), "v"(thr) : "vcc"); }
; __device__ __forceinline__ unsigned spread4(unsigned x) { return (x & 0xFu) | ((x & 0xF0u) << 4) | ((x & 0xF00u) << 8) | ((x & 0xF000u) << 12); }
; template <int PASS, bool DIAG> __device__ __forceinline__ void idx_half(unsigned& bits, unsigned& ebits, const f32x16& sc, int sbase, int tq, int r32, int hi, unsigned khi, unsigned klo, bool cand, LAS unsigned char* L) {
;     ...
;         unsigned hb = 0u, lb = 0u;
; #pragma unroll
;         for (int r = 15; r >= 0; --r) { const unsigned key = fkey2(sc[r]); shl_ge(hb, key, khi); shl_ge(lb, key, klo); }
;         bits = spread4(hb); ebits = spread4(lb & ~hb);
;         if (DIAG) { const unsigned vm = d < 0 ? 0u : (d >= 31 ? 0xFFFFFFFFu : ((2u << d) - 1u)); bits &= vm; ebits &= vm; }
;         if (cand && ebits != 0u) {
;             unsigned slot = __hip_atomic_fetch_add((LAS unsigned*)(L + IL_CNT) + r32, (unsigned)__builtin_popcount(ebits), __ATOMIC_RELAXED, __HIP_MEMORY_SCOPE_WORKGROUP);
; #pragma unroll
;             for (int r = 0; r < 16; ++r) if ((ebits >> crow(r, 0)) & 1u) { const int s = sbase + crow(r, hi);
;                 if (slot < (unsigned)IDX_CAP) ((LAS unsigned long long*)(L + IL_CAND))[r32 * IDX_CAP + slot] = ((unsigned long long)fkey2(sc[r]) << 16) | (unsigned long long)(0xFFFFu - (unsigned)s);
;                 ++slot; }
	v_mov_b32_e32 v160, 0
	v_mov_b32_e32 v5, 0
	v_cmp_ge_f32 vcc, v159, v165
	v_addc_co_u32 v160, vcc, v160, v160, vcc
	v_cmp_ge_f32 vcc, v159, v164
	v_addc_co_u32 v5, vcc, v5, v5, vcc
	v_cmp_ge_f32 vcc, v158, v165
	v_addc_co_u32 v160, vcc, v160, v160, vcc
	v_cmp_ge_f32 vcc, v158, v164
	v_addc_co_u32 v5, vcc, v5, v5, vcc
	v_cmp_ge_f32 vcc, v157, v165
	v_addc_co_u32 v160, vcc, v160, v160, vcc
	v_cmp_ge_f32 vcc, v157, v164
	v_addc_co_u32 v5, vcc, v5, v5, vcc
	v_cmp_ge_f32 vcc, v156, v165
	v_addc_co_u32 v160, vcc, v160, v160, vcc
	v_cmp_ge_f32 vcc, v156, v164
	v_addc_co_u32 v5, vcc, v5, v5, vcc
	v_cmp_ge_f32 vcc, v155, v165
	v_addc_co_u32 v160, vcc, v160, v160, vcc
	v_cmp_ge_f32 vcc, v155, v164
	v_addc_co_u32 v5, vcc, v5, v5, vcc
	v_cmp_ge_f32 vcc, v154, v165
	v_addc_co_u32 v160, vcc, v160, v160, vcc
	v_cmp_ge_f32 vcc, v154, v164
	v_addc_co_u32 v5, vcc, v5, v5, vcc
	v_cmp_ge_f32 vcc, v153, v165
	v_addc_co_u32 v160, vcc, v160, v160, vcc
	v_cmp_ge_f32 vcc, v153, v164
	v_addc_co_u32 v5, vcc, v5, v5, vcc
	v_cmp_ge_f32 vcc, v152, v165
	v_addc_co_u32 v160, vcc, v160, v160, vcc
	v_cmp_ge_f32 vcc, v152, v164
	v_addc_co_u32 v5, vcc, v5, v5, vcc
	v_cmp_ge_f32 vcc, v151, v165
	v_addc_co_u32 v160, vcc, v160, v160, vcc
	v_cmp_ge_f32 vcc, v151, v164
	v_addc_co_u32 v5, vcc, v5, v5, vcc
	v_cmp_ge_f32 vcc, v150, v165
	v_addc_co_u32 v160, vcc, v160, v160, vcc
	v_cmp_ge_f32 vcc, v150, v164
	v_addc_co_u32 v5, vcc, v5, v5, vcc
	v_cmp_ge_f32 vcc, v149, v165
	v_addc_co_u32 v160, vcc, v160, v160, vcc
	v_cmp_ge_f32 vcc, v149, v164
	v_addc_co_u32 v5, vcc, v5, v5, vcc
	v_cmp_ge_f32 vcc, v148, v165
	v_addc_co_u32 v160, vcc, v160, v160, vcc
	v_cmp_ge_f32 vcc, v148, v164
	v_addc_co_u32 v5, vcc, v5, v5, vcc
	s_nop 0
	v_cmp_ge_f32 vcc, v147, v165
	v_addc_co_u32 v160, vcc, v160, v160, vcc
	s_nop 0
	v_cmp_ge_f32 vcc, v147, v164
	v_addc_co_u32 v5, vcc, v5, v5, vcc
	s_nop 0
	v_cmp_ge_f32 vcc, v146, v165
	v_addc_co_u32 v160, vcc, v160, v160, vcc
	s_nop 0
	v_cmp_ge_f32 vcc, v146, v164
	v_addc_co_u32 v5, vcc, v5, v5, vcc
	s_nop 0
	v_cmp_ge_f32 vcc, v145, v165
	v_addc_co_u32 v160, vcc, v160, v160, vcc
	s_nop 0
	v_cmp_ge_f32 vcc, v145, v164
	v_addc_co_u32 v5, vcc, v5, v5, vcc
	s_nop 0
	v_cmp_ge_f32 vcc, v144, v165
	v_addc_co_u32 v160, vcc, v160, v160, vcc
	s_nop 0
	v_cmp_ge_f32 vcc, v144, v164
	v_addc_co_u32 v5, vcc, v5, v5, vcc
	s_nop 0
	v_bitop3_b32 v3, v5, v160, v5 bitop3:0x30
	v_bitop3_b32 v5, v5, 15, v160 bitop3:0x40
	v_lshlrev_b32_e32 v7, 4, v3
	v_and_or_b32 v5, v7, s93, v5
	v_lshlrev_b32_e32 v7, 8, v3
	v_lshlrev_b32_e32 v9, 12, v3
	v_and_b32_e32 v7, 0xf0000, v7
	v_and_b32_e32 v9, 0xf000000, v9
	v_or3_b32 v143, v5, v7, v9
	v_cmp_ne_u32_e32 vcc, 0, v143
	s_and_b64 s[0:1], s[10:11], vcc
	s_and_saveexec_b64 s[20:21], s[0:1]
	s_cbranch_execz .LBB0_1128
	v_bcnt_u32_b32 v5, v143, 0
	ds_add_rtn_u32 v161, v221, v5
	v_and_b32_e32 v5, 1, v3
	v_cmp_eq_u32_e32 vcc, 1, v5
	s_and_saveexec_b64 s[14:15], vcc
	s_cbranch_execz .LBB0_1070
	s_waitcnt lgkmcnt(0)
	v_cmp_gt_u32_e32 vcc, s87, v161
	s_and_saveexec_b64 s[42:43], vcc
	v_add_f32_e32 v0, 0, v144
	v_ashrrev_i32_e32 v252, 31, v0
	v_bitop3_b32 v0, v252, v0, s85 bitop3:0x36
	v_lshlrev_b64 v[162:163], 16, v[0:1]
	v_add_u32_e32 v0, s45, v142
	v_lshl_add_u32 v5, v161, 3, v136
	v_or_b32_e32 v162, v162, v0
	ds_write_b64 v5, v[162:163] offset:512
	s_or_b64 exec, exec, s[42:43]
	v_add_u32_e32 v161, 1, v161

; __device__ __forceinline__ float relu_i(float p) { const int i = __float_as_int(p); return __int_as_float(i > 0 ? i : 0); }
; __device__ __forceinline__ void idx_scores_k(f32x16& sc, const bf16x8 (&kf)[4], const bf16x8 (&qf)[16], const f32x4& w) {
;     f32x16 p0 = f32x16{}, p1 = f32x16{};
; #pragma unroll
;     for (int d0 = 0; d0 < 4; ++d0) p0 = __builtin_amdgcn_mfma_f32_32x32x16_bf16(kf[d0], qf[d0], p0, 0, 0, 0);
; #pragma unroll
;     for (int d0 = 0; d0 < 4; ++d0) p1 = __builtin_amdgcn_mfma_f32_32x32x16_bf16(kf[d0], qf[4 + d0], p1, 0, 0, 0);
; #pragma unroll
;     for (int r = 0; r < 16; ++r) sc[r] = w[0] * relu_i(p0[r]);
;     p0 = f32x16{};
; #pragma unroll
;     for (int d0 = 0; d0 < 4; ++d0) p0 = __builtin_amdgcn_mfma_f32_32x32x16_bf16(kf[d0], qf[8 + d0], p0, 0, 0, 0);
; #pragma unroll
;     for (int r = 0; r < 16; ++r) sc[r] = fmaf(w[1], relu_i(p1[r]), sc[r]);
;     p1 = f32x16{};
; #pragma unroll
;     for (int d0 = 0; d0 < 4; ++d0) p1 = __builtin_amdgcn_mfma_f32_32x32x16_bf16(kf[d0], qf[12 + d0], p1, 0, 0, 0);
; #pragma unroll
;     for (int r = 0; r < 16; ++r) sc[r] = fmaf(w[2], relu_i(p0[r]), sc[r]);
; #pragma unroll
;     for (int r = 0; r < 16; ++r) sc[r] = fmaf(w[3], relu_i(p1[r]), sc[r]);
; }
.LBB0_1131:
	s_mov_b64 s[14:15], -1
	s_and_b64 vcc, exec, s[18:19]
	s_waitcnt vmcnt(3)
	v_mfma_f32_32x32x16_bf16 v[2:17], v[46:49], v[70:73], 0
	s_waitcnt vmcnt(2)
	v_mfma_f32_32x32x16_bf16 v[2:17], v[42:45], v[74:77], v[2:17]
	s_waitcnt vmcnt(1)
	v_mfma_f32_32x32x16_bf16 v[2:17], v[38:41], v[78:81], v[2:17]
	s_waitcnt vmcnt(0)
	v_mfma_f32_32x32x16_bf16 v[2:17], v[34:37], v[82:85], v[2:17]
	v_mfma_f32_32x32x16_bf16 v[180:195], v[46:49], v[86:89], 0
	v_mfma_f32_32x32x16_bf16 v[180:195], v[42:45], v[90:93], v[180:195]
	v_mfma_f32_32x32x16_bf16 v[180:195], v[38:41], v[94:97], v[180:195]
	v_mfma_f32_32x32x16_bf16 v[180:195], v[34:37], v[98:101], v[180:195]
	s_nop 7
	v_max_i32_e32 v200, 0, v2
	v_fma_f32 v53, v66, v200, 0
	v_max_i32_e32 v200, 0, v3
	v_fma_f32 v54, v66, v200, 0
	v_max_i32_e32 v200, 0, v4
	v_fma_f32 v55, v66, v200, 0
	v_max_i32_e32 v200, 0, v5
	v_fma_f32 v56, v66, v200, 0
	v_max_i32_e32 v200, 0, v6
	v_fma_f32 v57, v66, v200, 0
	v_max_i32_e32 v200, 0, v7
	v_fma_f32 v58, v66, v200, 0
	v_max_i32_e32 v200, 0, v8
	v_fma_f32 v59, v66, v200, 0
	v_max_i32_e32 v200, 0, v9
	v_fma_f32 v60, v66, v200, 0
	v_max_i32_e32 v200, 0, v10
	v_fma_f32 v61, v66, v200, 0
	v_max_i32_e32 v200, 0, v11
	v_fma_f32 v62, v66, v200, 0
	v_max_i32_e32 v200, 0, v12
	v_fma_f32 v63, v66, v200, 0
	v_max_i32_e32 v200, 0, v13
	v_fma_f32 v64, v66, v200, 0
	v_max_i32_e32 v200, 0, v14
	v_fma_f32 v65, v66, v200, 0
	v_max_i32_e32 v200, 0, v15
	v_fma_f32 v144, v66, v200, 0
	v_max_i32_e32 v200, 0, v16
	v_fma_f32 v145, v66, v200, 0
	v_max_i32_e32 v200, 0, v17
	v_fma_f32 v146, v66, v200, 0
	v_mfma_f32_32x32x16_bf16 v[2:17], v[46:49], v[102:105], 0
	v_mfma_f32_32x32x16_bf16 v[2:17], v[42:45], v[106:109], v[2:17]
	v_mfma_f32_32x32x16_bf16 v[2:17], v[38:41], v[110:113], v[2:17]
	v_mfma_f32_32x32x16_bf16 v[2:17], v[34:37], v[114:117], v[2:17]
	v_max_i32_e32 v200, 0, v180
	v_fmac_f32_e32 v53, v67, v200
	v_max_i32_e32 v200, 0, v181
	v_fmac_f32_e32 v54, v67, v200
	v_max_i32_e32 v200, 0, v182
	v_fmac_f32_e32 v55, v67, v200
	v_max_i32_e32 v200, 0, v183
	v_fmac_f32_e32 v56, v67, v200
	v_max_i32_e32 v200, 0, v184
	v_fmac_f32_e32 v57, v67, v200
	v_max_i32_e32 v200, 0, v185
	v_fmac_f32_e32 v58, v67, v200
	v_max_i32_e32 v200, 0, v186
	v_fmac_f32_e32 v59, v67, v200
	v_max_i32_e32 v200, 0, v187
	v_fmac_f32_e32 v60, v67, v200
	v_max_i32_e32 v200, 0, v188
	v_fmac_f32_e32 v61, v67, v200
	v_max_i32_e32 v200, 0, v189
	v_fmac_f32_e32 v62, v67, v200
	v_max_i32_e32 v200, 0, v190
	v_fmac_f32_e32 v63, v67, v200
	v_max_i32_e32 v200, 0, v191
	v_fmac_f32_e32 v64, v67, v200
	v_max_i32_e32 v200, 0, v192
	v_fmac_f32_e32 v65, v67, v200
	v_max_i32_e32 v200, 0, v193
	v_fmac_f32_e32 v144, v67, v200
	v_max_i32_e32 v200, 0, v194
	v_fmac_f32_e32 v145, v67, v200
	v_max_i32_e32 v200, 0, v195
	v_fmac_f32_e32 v146, v67, v200
	v_mfma_f32_32x32x16_bf16 v[180:195], v[46:49], v[118:121], 0
	v_mfma_f32_32x32x16_bf16 v[180:195], v[42:45], v[122:125], v[180:195]
	v_mfma_f32_32x32x16_bf16 v[180:195], v[38:41], v[126:129], v[180:195]
	v_mfma_f32_32x32x16_bf16 v[180:195], v[34:37], v[130:133], v[180:195]
	v_max_i32_e32 v200, 0, v2
	v_fmac_f32_e32 v53, v68, v200
	v_max_i32_e32 v200, 0, v3
	v_fmac_f32_e32 v54, v68, v200
	v_max_i32_e32 v200, 0, v4
	v_fmac_f32_e32 v55, v68, v200
	v_max_i32_e32 v200, 0, v5
	v_fmac_f32_e32 v56, v68, v200
	v_max_i32_e32 v200, 0, v6
	v_fmac_f32_e32 v57, v68, v200
	v_max_i32_e32 v200, 0, v7
	v_fmac_f32_e32 v58, v68, v200
	v_max_i32_e32 v200, 0, v8
	v_fmac_f32_e32 v59, v68, v200
	v_max_i32_e32 v200, 0, v9
	v_fmac_f32_e32 v60, v68, v200
	v_max_i32_e32 v200, 0, v10
	v_fmac_f32_e32 v61, v68, v200
	v_max_i32_e32 v200, 0, v11
	v_fmac_f32_e32 v62, v68, v200
	v_max_i32_e32 v200, 0, v12
	v_fmac_f32_e32 v63, v68, v200
	v_max_i32_e32 v200, 0, v13
	v_fmac_f32_e32 v64, v68, v200
	v_max_i32_e32 v200, 0, v14
	v_fmac_f32_e32 v65, v68, v200
	v_max_i32_e32 v200, 0, v15
	v_fmac_f32_e32 v144, v68, v200
	v_max_i32_e32 v200, 0, v16
	v_fmac_f32_e32 v145, v68, v200
	v_max_i32_e32 v200, 0, v17
	v_fmac_f32_e32 v146, v68, v200
	v_max_i32_e32 v200, 0, v180
	v_fmac_f32_e32 v53, v69, v200
	v_max_i32_e32 v200, 0, v181
	v_fmac_f32_e32 v54, v69, v200
	v_max_i32_e32 v200, 0, v182
	v_fmac_f32_e32 v55, v69, v200
	v_max_i32_e32 v200, 0, v183
	v_fmac_f32_e32 v56, v69, v200
	v_max_i32_e32 v200, 0, v184
	v_fmac_f32_e32 v57, v69, v200
	v_max_i32_e32 v200, 0, v185
	v_fmac_f32_e32 v58, v69, v200
	v_max_i32_e32 v200, 0, v186
	v_fmac_f32_e32 v59, v69, v200
	v_max_i32_e32 v200, 0, v187
	v_fmac_f32_e32 v60, v69, v200
	v_max_i32_e32 v200, 0, v188
	v_fmac_f32_e32 v61, v69, v200
	v_max_i32_e32 v200, 0, v189
	v_fmac_f32_e32 v62, v69, v200
	v_max_i32_e32 v200, 0, v190
	v_fmac_f32_e32 v63, v69, v200
	v_max_i32_e32 v200, 0, v191
	v_fmac_f32_e32 v64, v69, v200
	v_max_i32_e32 v200, 0, v192
	v_fmac_f32_e32 v65, v69, v200
	v_max_i32_e32 v200, 0, v193
	v_fmac_f32_e32 v144, v69, v200
	v_max_i32_e32 v200, 0, v194
	v_fmac_f32_e32 v145, v69, v200
	v_max_i32_e32 v200, 0, v195
	v_fmac_f32_e32 v146, v69, v200
	s_cbranch_vccz .LBB0_1196
; #define LAS __attribute__((address_space(3)))
; __device__ __forceinline__ int crow(int r, int hi) { return (r & 3) + 8 * (r >> 2) + 4 * hi; }
; __device__ __forceinline__ unsigned fkey2(float v) { const unsigned u = __float_as_uint(v + 0.0f); return u ^ ((unsigned)((int)u >> 31) | 0x80000000u); }
; __device__ __forceinline__ void shl_ge(unsigned& acc, unsigned key, unsigned thr) { asm("v_cmp_ge_u32 vcc, %1, %2\n\tv_addc_co_u32 %0, vcc, %0, %0, vcc" : "+v"(acc) : "v"(key), "v"(thr) : "vcc"); }
; __device__ __forceinline__ unsigned spread4(unsigned x) { return (x & 0xFu) | ((x & 0xF0u) << 4) | ((x & 0xF00u) << 8) | ((x & 0xF000u) << 12); }
; template <int PASS, bool DIAG> __device__ __forceinline__ void idx_half(unsigned& bits, unsigned& ebits, const f32x16& sc, int sbase, int tq, int r32, int hi, unsigned khi, unsigned klo, bool cand, LAS unsigned char* L) {
;     ...
;         unsigned hb = 0u, lb = 0u;
; #pragma unroll
;         for (int r = 15; r >= 0; --r) { const unsigned key = fkey2(sc[r]); shl_ge(hb, key, khi); shl_ge(lb, key, klo); }
;         bits = spread4(hb); ebits = spread4(lb & ~hb);
;         if (DIAG) { const unsigned vm = d < 0 ? 0u : (d >= 31 ? 0xFFFFFFFFu : ((2u << d) - 1u)); bits &= vm; ebits &= vm; }
;         if (cand && ebits != 0u) {
;             unsigned slot = __hip_atomic_fetch_add((LAS unsigned*)(L + IL_CNT) + r32, (unsigned)__builtin_popcount(ebits), __ATOMIC_RELAXED, __HIP_MEMORY_SCOPE_WORKGROUP);
; #pragma unroll
;             for (int r = 0; r < 16; ++r) if ((ebits >> crow(r, 0)) & 1u) { const int s = sbase + crow(r, hi);
;                 if (slot < (unsigned)IDX_CAP) ((LAS unsigned long long*)(L + IL_CAND))[r32 * IDX_CAP + slot] = ((unsigned long long)fkey2(sc[r]) << 16) | (unsigned long long)(0xFFFFu - (unsigned)s);
;                 ++slot; }
	v_mov_b32_e32 v49, 0
	v_mov_b32_e32 v5, 0
	v_cmp_ge_f32 vcc, v146, v165
	v_addc_co_u32 v49, vcc, v49, v49, vcc
	v_cmp_ge_f32 vcc, v146, v164
	v_addc_co_u32 v5, vcc, v5, v5, vcc
	v_cmp_ge_f32 vcc, v145, v165
	v_addc_co_u32 v49, vcc, v49, v49, vcc
	v_cmp_ge_f32 vcc, v145, v164
	v_addc_co_u32 v5, vcc, v5, v5, vcc
	v_cmp_ge_f32 vcc, v144, v165
	v_addc_co_u32 v49, vcc, v49, v49, vcc
	v_cmp_ge_f32 vcc, v144, v164
	v_addc_co_u32 v5, vcc, v5, v5, vcc
	v_cmp_ge_f32 vcc, v65, v165
	v_addc_co_u32 v49, vcc, v49, v49, vcc
	v_cmp_ge_f32 vcc, v65, v164
	v_addc_co_u32 v5, vcc, v5, v5, vcc
	v_cmp_ge_f32 vcc, v64, v165
	v_addc_co_u32 v49, vcc, v49, v49, vcc
	v_cmp_ge_f32 vcc, v64, v164
	v_addc_co_u32 v5, vcc, v5, v5, vcc
	v_cmp_ge_f32 vcc, v63, v165
	v_addc_co_u32 v49, vcc, v49, v49, vcc
	v_cmp_ge_f32 vcc, v63, v164
	v_addc_co_u32 v5, vcc, v5, v5, vcc
	v_cmp_ge_f32 vcc, v62, v165
	v_addc_co_u32 v49, vcc, v49, v49, vcc
	v_cmp_ge_f32 vcc, v62, v164
	v_addc_co_u32 v5, vcc, v5, v5, vcc
	v_cmp_ge_f32 vcc, v61, v165
	v_addc_co_u32 v49, vcc, v49, v49, vcc
	v_cmp_ge_f32 vcc, v61, v164
	v_addc_co_u32 v5, vcc, v5, v5, vcc
	v_cmp_ge_f32 vcc, v60, v165
	v_addc_co_u32 v49, vcc, v49, v49, vcc
	v_cmp_ge_f32 vcc, v60, v164
	v_addc_co_u32 v5, vcc, v5, v5, vcc
	v_cmp_ge_f32 vcc, v59, v165
	v_addc_co_u32 v49, vcc, v49, v49, vcc
	v_cmp_ge_f32 vcc, v59, v164
	v_addc_co_u32 v5, vcc, v5, v5, vcc
	v_cmp_ge_f32 vcc, v58, v165
	v_addc_co_u32 v49, vcc, v49, v49, vcc
	v_cmp_ge_f32 vcc, v58, v164
	v_addc_co_u32 v5, vcc, v5, v5, vcc
	v_cmp_ge_f32 vcc, v57, v165
	v_addc_co_u32 v49, vcc, v49, v49, vcc
	v_cmp_ge_f32 vcc, v57, v164
	v_addc_co_u32 v5, vcc, v5, v5, vcc
	s_nop 0
	v_cmp_ge_f32 vcc, v56, v165
	v_addc_co_u32 v49, vcc, v49, v49, vcc
	s_nop 0
	v_cmp_ge_f32 vcc, v56, v164
	v_addc_co_u32 v5, vcc, v5, v5, vcc
	s_nop 0
	v_cmp_ge_f32 vcc, v55, v165
	v_addc_co_u32 v49, vcc, v49, v49, vcc
	s_nop 0
	v_cmp_ge_f32 vcc, v55, v164
	v_addc_co_u32 v5, vcc, v5, v5, vcc
	s_nop 0
	v_cmp_ge_f32 vcc, v54, v165
	v_addc_co_u32 v49, vcc, v49, v49, vcc
	s_nop 0
	v_cmp_ge_f32 vcc, v54, v164
	v_addc_co_u32 v5, vcc, v5, v5, vcc
	s_nop 0
	v_cmp_ge_f32 vcc, v53, v165
	v_addc_co_u32 v49, vcc, v49, v49, vcc
	s_nop 0
	v_cmp_ge_f32 vcc, v53, v164
	v_addc_co_u32 v5, vcc, v5, v5, vcc
	s_nop 0
	v_bitop3_b32 v3, v5, v49, v5 bitop3:0x30
	v_bitop3_b32 v5, v5, 15, v49 bitop3:0x40
	v_lshlrev_b32_e32 v7, 4, v3
	v_and_or_b32 v5, v7, s93, v5
	v_lshlrev_b32_e32 v7, 8, v3
	v_lshlrev_b32_e32 v9, 12, v3
	v_and_b32_e32 v7, 0xf0000, v7
	v_and_b32_e32 v9, 0xf000000, v9
	v_or3_b32 v48, v5, v7, v9
	v_cmp_ne_u32_e32 vcc, 0, v48
	s_and_b64 s[0:1], s[10:11], vcc
	s_and_saveexec_b64 s[18:19], s[0:1]
	s_cbranch_execz .LBB0_1195
	v_bcnt_u32_b32 v5, v48, 0
	ds_add_rtn_u32 v147, v221, v5
	v_and_b32_e32 v5, 1, v3
	v_cmp_eq_u32_e32 vcc, 1, v5
	s_and_saveexec_b64 s[14:15], vcc
	s_cbranch_execz .LBB0_1137
	s_waitcnt lgkmcnt(0)
	v_cmp_gt_u32_e32 vcc, s87, v147
	s_and_saveexec_b64 s[42:43], vcc
	s_cbranch_execz .LBB0_1136
	v_add_f32_e32 v0, 0, v53
	v_ashrrev_i32_e32 v252, 31, v0
	v_bitop3_b32 v0, v252, v0, s85 bitop3:0x36
	v_lshlrev_b64 v[148:149], 16, v[0:1]
	v_add_u32_e32 v0, s45, v142
	v_subrev_u32_e32 v0, 32, v0
	v_lshl_add_u32 v5, v147, 3, v136
	v_or_b32_e32 v148, v148, v0
	ds_write_b64 v5, v[148:149] offset:512

; __device__ __forceinline__ void dsa_qk(f32x16& p0, f32x16& p1, const LAS char* kp, const bf16x8 (&qr)[4], unsigned long long mw, int hi, float mref, const LAS char* tbl) {
;     ...
;     for (int d0 = 0; d0 < 4; ++d0) { kf[2 * d0] = *(const LAS bf16x8*)(kp + d0 * 2048); kf[2 * d0 + 1] = *(const LAS bf16x8*)(kp + d0 * 2048 + 512); }
; __device__ __forceinline__ void dsa_block_unit(int b, int g, int m  , const bf16_t* Q, const bf16_t* K, const bf16_t* V, const unsigned long long* mask, bf16_t* O, LAS char* L, int wid, int lane, float sbound  ) {
;     const int r32 = lane & 31, hi = lane >> 5; const int h = 4 * g + (wid & 3), t0 = 64 * m + 32 * (wid >> 2); const size_t rowbase = (size_t)b * T; const int jd = m;
;     const bf16_t* Qw = Q + (rowbase + t0) * 512 + h * 64; const bf16_t* Kg = K + rowbase * 128 + g * 64; const bf16_t* Vg = V + rowbase * 128 + g * 64;
;     const unsigned long long* mrow = mask + (rowbase + t0 + r32) * 64;
;     bf16x8 qr[4];
; #pragma unroll
;     for (int d0 = 0; d0 < 4; ++d0) qr[d0] = *(const bf16x8*)(Qw + (size_t)r32 * 512 + 16 * d0 + 8 * hi);
;     f32x16 o[2]; o[0] = f32x16{}; o[1] = f32x16{};
;     const bool fixed = sbound > 0.f;
;     float mref = fixed ? sbound : 0.f, lsum = 0.f;
;     LAS float* wsf = (LAS float*)(L + DL_F + wid * 256);
;     const unsigned kvoff = (unsigned)lane * 256u;
;     const unsigned vvoff = (unsigned)((lane >> 2) * 128 + (lane & 3) * 8) * 2u;
;     const bf16_t* Kw = Kg + wid * 8; const bf16_t* Vw = Vg + (size_t)(16 * (wid & 3)) * 128 + (wid >> 2) * 32;
;     const unsigned kdst = (unsigned)(size_t)(L + DL_K) + wid * 1024u, vdst = (unsigned)(size_t)(L + DL_V) + wid * 1024u;
;     const LAS char* kp0 = L + DL_K + hi * 1024 + r32 * 16;
;     const LAS char* vp0 = L + DL_V + ((lane >> 4) & 1) * 32 + (lane & 3) * 8 + (4 * hi + ((lane & 15) >> 2)) * 64;
;     glds16_s(Kw, kvoff, kdst); glds16_s(Vw, vvoff, vdst);
;     if (jd >= 1) { glds16_s(Kw + (size_t)64 * 128, kvoff, kdst + 8192); glds16_s(Vw + (size_t)64 * 128, vvoff, vdst + 8192); }
;     unsigned long long mwn = mrow[0];
;     unsigned long long mwn2 = (jd >= 1) ? mrow[1] : 0ull;
;     asm volatile("s_waitcnt vmcnt(0) lgkmcnt(0)\n\ts_barrier" ::: "memory");
;     const LAS char* tblp = L + DL_T;
;     f32x16 pa0, pa1, pb0, pb1; dsa_qk(pa0, pa1, kp0, qr, mwn, hi, mref, fixed ? tblp : (const LAS char*)nullptr);
.LBB0_1677:
	s_lshl_b32 s0, s54, 6
	s_ashr_i32 s21, s20, 31
	s_bfe_u32 s16, s42, 0x10005
	v_readlane_b32 s2, v254, 55
	s_add_i32 s0, s0, s61
	s_lshl_b64 s[22:23], s[20:21], 12
	v_readlane_b32 s3, v254, 56
	s_add_u32 s28, s22, s0
	s_mov_b32 s1, s3
	s_addc_u32 s29, s23, 0
	s_mov_b64 s[70:71], s[0:1]
	s_lshl_b64 s[0:1], s[28:29], 10
	s_add_u32 s0, s43, s0
	s_addc_u32 s1, s44, s1
	s_lshl_b32 s2, s16, 8
	v_readlane_b32 s3, v254, 24
	s_or_b32 s2, s2, s3
	s_lshl_b32 s52, s2, 1
	s_add_u32 s0, s0, s52
	s_addc_u32 s1, s1, 0
	s_lshl_b64 s[2:3], s[20:21], 20
	s_add_u32 s17, s47, s2
	s_addc_u32 s18, s48, s3
	v_lshl_add_u64 v[4:5], s[0:1], 0, v[152:153]
	s_add_u32 s0, s45, s2
	s_addc_u32 s1, s46, s3
	s_lshl_b32 s2, s16, 7
	s_add_u32 s0, s0, s2
	s_addc_u32 s1, s1, 0
	s_add_u32 s2, s17, s2
	s_addc_u32 s3, s18, 0
	v_readlane_b32 s16, v254, 51
	s_add_u32 s16, s0, s16
	s_addc_u32 s17, s1, 0
	v_readlane_b32 s0, v254, 52
	s_add_u32 s0, s2, s0
	s_addc_u32 s1, s3, 0
	s_lshl_b32 s2, s61, 1
	s_add_u32 s18, s0, s2
	v_lshlrev_b32_e32 v0, 1, v154
	s_addc_u32 s19, s1, 0
	v_lshl_add_u64 v[4:5], v[4:5], 0, v[0:1]
	s_add_u32 s24, s18, 0x4000
	s_barrier
	global_load_dwordx4 v[98:101], v[4:5], off
	global_load_dwordx4 v[102:105], v[4:5], off offset:32
	global_load_dwordx4 v[106:109], v[4:5], off offset:64
	global_load_dwordx4 v[110:113], v[4:5], off offset:96
	s_nop 4
	s_mov_b32 s0, m0
	s_mov_b32 m0, s63
	s_nop 0
	global_load_lds_dwordx4 v172, s[16:17]
	s_mov_b32 m0, s0
	s_addc_u32 s25, s19, 0
	v_mov_b32_e32 v3, s29
	v_or_b32_e32 v2, s28, v150
	s_nop 4
	s_mov_b32 s0, m0
	s_mov_b32 m0, s64
	s_nop 0
	global_load_lds_dwordx4 v173, s[18:19]
	s_mov_b32 m0, s0
	s_add_u32 s26, s16, 0x4000
	v_lshlrev_b64 v[2:3], 9, v[2:3]
	s_addc_u32 s27, s17, 0
	v_readlane_b32 s1, v254, 29
	s_nop 4
	s_mov_b32 s0, m0
	s_mov_b32 m0, s1
	s_nop 0
	global_load_lds_dwordx4 v172, s[26:27]
	s_mov_b32 m0, s0
	v_lshl_add_u64 v[2:3], s[12:13], 0, v[2:3]
	v_readlane_b32 s1, v254, 28
	s_nop 4
	s_mov_b32 s0, m0
	s_mov_b32 m0, s1
	s_nop 0
	global_load_lds_dwordx4 v173, s[24:25]
	s_mov_b32 m0, s0
	global_load_dwordx4 v[114:117], v[2:3], off sc1
	s_waitcnt vmcnt(0) lgkmcnt(0)
	s_barrier
	ds_read_b128 v[30:33], v174
	ds_read_b128 v[26:29], v174 offset:512
	ds_read_b128 v[22:25], v174 offset:2048
	ds_read_b128 v[2:5], v174 offset:2560
	ds_read_b128 v[6:9], v174 offset:4096
	ds_read_b128 v[10:13], v174 offset:4608
	ds_read_b128 v[14:17], v174 offset:6144
	ds_read_b128 v[18:21], v174 offset:6656
	s_waitcnt vmcnt(0)
	v_lshrrev_b32_e32 v67, v176, v114
	v_lshrrev_b32_e32 v66, v176, v115
	s_and_saveexec_b64 s[0:1], s[4:5]
	s_xor_b64 s[30:31], exec, s[0:1]
	s_cbranch_execz .LBB0_1679
	v_lshlrev_b32_e32 v34, 4, v67
	v_lshlrev_b32_e32 v35, 4, v66
	s_add_i32 s0, 0, 0x14800
	v_mov_b32_e32 v206, 0xf0
	v_and_or_b32 v34, v34, v206, s0
	v_and_or_b32 v38, v35, v206, s0
	ds_read_b128 v[34:37], v34
	ds_read_b128 v[50:53], v38
	v_lshrrev_b32_e32 v38, 4, v67
	v_lshrrev_b32_e32 v39, 4, v66
	v_and_or_b32 v38, v38, v206, s0
	v_and_or_b32 v42, v39, v206, s0
	ds_read_b128 v[38:41], v38
	ds_read_b128 v[54:57], v42
	v_lshrrev_b32_e32 v42, 12, v67
	v_lshrrev_b32_e32 v43, 12, v66
	v_and_or_b32 v42, v42, v206, s0
	v_and_or_b32 v46, v43, v206, s0
	ds_read_b128 v[42:45], v42
	ds_read_b128 v[58:61], v46
	v_lshrrev_b32_e32 v46, 20, v67
	v_lshrrev_b32_e32 v47, 20, v66
	v_and_or_b32 v46, v46, v206, s0
	v_and_or_b32 v62, v47, v206, s0
	ds_read_b128 v[46:49], v46
	ds_read_b128 v[62:65], v62

; #define LAS __attribute__((address_space(3)))
; __device__ __forceinline__ void dsa_qk(f32x16& p0, f32x16& p1, const LAS char* kp, const bf16x8 (&qr)[4], unsigned long long mw, int hi, float mref, const LAS char* tbl) {
;     bf16x8 kf[8];
; #pragma unroll
;     for (int d0 = 0; d0 < 4; ++d0) { kf[2 * d0] = *(const LAS bf16x8*)(kp + d0 * 2048); kf[2 * d0 + 1] = *(const LAS bf16x8*)(kp + d0 * 2048 + 512); }
;     const unsigned mlo = (unsigned)mw >> (4 * hi), mhi = (unsigned)(mw >> 32) >> (4 * hi), negm = __float_as_uint(-mref);
;     if (tbl) {
; #pragma unroll
;         for (int i = 0; i < 4; ++i) { const u32x4 a = *(const LAS u32x4*)(tbl + ((mlo >> (8 * i)) & 15u) * 16u), b = *(const LAS u32x4*)(tbl + ((mhi >> (8 * i)) & 15u) * 16u);
; #pragma unroll
;             for (int e = 0; e < 4; ++e) { p0[4 * i + e] = __uint_as_float(a[e]); p1[4 * i + e] = __uint_as_float(b[e]); } }
; __device__ __forceinline__ void dsa_step(f32x16& c0, f32x16& c1, f32x16& n0, f32x16& n1, const bool have_n, const LAS char* kpn, const LAS char* vpc, const bf16x8 (&qr)[4], unsigned long long mwn, ...
;     if (have_n) dsa_qk(n0, n1, kpn, qr, mwn, hi, mref, fixed ? tblp : (const LAS char*)nullptr);
;     bf16x8 vf[8]; pv_load(vf, vpc);
.LBB0_1686:
	s_add_i32 s0, s58, -3
	s_cmp_lt_u32 s0, s54
	s_cselect_b64 s[34:35], -1, 0
	s_cmp_ge_u32 s0, s54
	s_cbranch_scc1 .LBB0_1692
	v_add_u32_e32 v66, s57, v174
	ds_read_b128 v[146:149], v66
	ds_read_b128 v[142:145], v66 offset:512
	ds_read_b128 v[138:141], v66 offset:2048
	ds_read_b128 v[134:137], v66 offset:2560
	ds_read_b128 v[130:133], v66 offset:4096
	ds_read_b128 v[126:129], v66 offset:4608
	ds_read_b128 v[122:125], v66 offset:6144
	ds_read_b128 v[118:121], v66 offset:6656
	v_lshrrev_b32_e32 v115, v176, v116
	v_lshrrev_b32_e32 v114, v176, v117
	s_and_saveexec_b64 s[0:1], s[4:5]
	s_xor_b64 s[36:37], exec, s[0:1]
	s_cbranch_execz .LBB0_1689
	v_lshlrev_b32_e32 v66, 4, v115
	v_lshlrev_b32_e32 v67, 4, v114
	v_lshrrev_b32_e32 v70, 4, v115
	v_lshrrev_b32_e32 v71, 4, v114
	v_lshrrev_b32_e32 v74, 12, v115
	v_lshrrev_b32_e32 v75, 12, v114
	v_lshrrev_b32_e32 v78, 20, v115
	v_lshrrev_b32_e32 v79, 20, v114
	s_add_i32 s0, 0, 0x14800
	v_mov_b32_e32 v206, 0xf0
	v_and_or_b32 v66, v66, v206, s0
	v_and_or_b32 v67, v67, v206, s0
	v_and_or_b32 v70, v70, v206, s0
	v_and_or_b32 v71, v71, v206, s0
	v_and_or_b32 v74, v74, v206, s0
	v_and_or_b32 v75, v75, v206, s0
	v_and_or_b32 v78, v78, v206, s0
	v_and_or_b32 v79, v79, v206, s0
	ds_read_b128 v[82:85], v66
	ds_read_b128 v[66:69], v67
	ds_read_b128 v[86:89], v70
	ds_read_b128 v[70:73], v71
	ds_read_b128 v[90:93], v74
	ds_read_b128 v[74:77], v75
	ds_read_b128 v[94:97], v78
	ds_read_b128 v[78:81], v79

; #define LAS __attribute__((address_space(3)))
; __device__ __forceinline__ void dsa_qk(f32x16& p0, f32x16& p1, const LAS char* kp, const bf16x8 (&qr)[4], unsigned long long mw, int hi, float mref, const LAS char* tbl) {
;     bf16x8 kf[8];
; #pragma unroll
;     for (int d0 = 0; d0 < 4; ++d0) { kf[2 * d0] = *(const LAS bf16x8*)(kp + d0 * 2048); kf[2 * d0 + 1] = *(const LAS bf16x8*)(kp + d0 * 2048 + 512); }
;     const unsigned mlo = (unsigned)mw >> (4 * hi), mhi = (unsigned)(mw >> 32) >> (4 * hi), negm = __float_as_uint(-mref);
;     if (tbl) {
; #pragma unroll
;         for (int i = 0; i < 4; ++i) { const u32x4 a = *(const LAS u32x4*)(tbl + ((mlo >> (8 * i)) & 15u) * 16u), b = *(const LAS u32x4*)(tbl + ((mhi >> (8 * i)) & 15u) * 16u);
; #pragma unroll
;             for (int e = 0; e < 4; ++e) { p0[4 * i + e] = __uint_as_float(a[e]); p1[4 * i + e] = __uint_as_float(b[e]); } }
; __device__ __forceinline__ void dsa_step(f32x16& c0, f32x16& c1, f32x16& n0, f32x16& n1, const bool have_n, const LAS char* kpn, const LAS char* vpc, const bf16x8 (&qr)[4], unsigned long long mwn, ...
;     if (have_n) dsa_qk(n0, n1, kpn, qr, mwn, hi, mref, fixed ? tblp : (const LAS char*)nullptr);
;     bf16x8 vf[8]; pv_load(vf, vpc);
.LBB0_1699:
	s_add_i32 s0, s58, -2
	s_cmp_lt_u32 s0, s54
	s_cselect_b64 s[34:35], -1, 0
	s_cmp_ge_u32 s0, s54
	s_cbranch_scc1 .LBB0_1705
	v_add_u32_e32 v34, s59, v174
	ds_read_b128 v[146:149], v34
	ds_read_b128 v[142:145], v34 offset:512
	ds_read_b128 v[138:141], v34 offset:2048
	ds_read_b128 v[134:137], v34 offset:2560
	ds_read_b128 v[130:133], v34 offset:4096
	ds_read_b128 v[126:129], v34 offset:4608
	ds_read_b128 v[122:125], v34 offset:6144
	ds_read_b128 v[118:121], v34 offset:6656
	v_lshrrev_b32_e32 v115, v176, v170
	v_lshrrev_b32_e32 v114, v176, v171
	s_and_saveexec_b64 s[0:1], s[4:5]
	s_xor_b64 s[36:37], exec, s[0:1]
	s_cbranch_execz .LBB0_1702
	v_lshlrev_b32_e32 v34, 4, v115
	v_lshlrev_b32_e32 v35, 4, v114
	s_add_i32 s0, 0, 0x14800
	v_mov_b32_e32 v206, 0xf0
	v_and_or_b32 v34, v34, v206, s0
	v_and_or_b32 v38, v35, v206, s0
	ds_read_b128 v[34:37], v34
	ds_read_b128 v[50:53], v38
	v_lshrrev_b32_e32 v38, 4, v115
	v_lshrrev_b32_e32 v39, 4, v114
	v_and_or_b32 v38, v38, v206, s0
	v_and_or_b32 v42, v39, v206, s0
	ds_read_b128 v[38:41], v38
	ds_read_b128 v[54:57], v42
	v_lshrrev_b32_e32 v42, 12, v115
	v_lshrrev_b32_e32 v43, 12, v114
	v_and_or_b32 v42, v42, v206, s0
	v_and_or_b32 v46, v43, v206, s0
	ds_read_b128 v[42:45], v42
	ds_read_b128 v[58:61], v46
	v_lshrrev_b32_e32 v46, 20, v115
	v_lshrrev_b32_e32 v47, 20, v114
	v_and_or_b32 v46, v46, v206, s0
	v_and_or_b32 v62, v47, v206, s0
	ds_read_b128 v[46:49], v46
	ds_read_b128 v[62:65], v62

; #define LAS __attribute__((address_space(3)))
; __device__ __forceinline__ void dsa_qk(f32x16& p0, f32x16& p1, const LAS char* kp, const bf16x8 (&qr)[4], unsigned long long mw, int hi, float mref, const LAS char* tbl) {
;     bf16x8 kf[8];
; #pragma unroll
;     for (int d0 = 0; d0 < 4; ++d0) { kf[2 * d0] = *(const LAS bf16x8*)(kp + d0 * 2048); kf[2 * d0 + 1] = *(const LAS bf16x8*)(kp + d0 * 2048 + 512); }
;     const unsigned mlo = (unsigned)mw >> (4 * hi), mhi = (unsigned)(mw >> 32) >> (4 * hi), negm = __float_as_uint(-mref);
;     if (tbl) {
; #pragma unroll
;         for (int i = 0; i < 4; ++i) { const u32x4 a = *(const LAS u32x4*)(tbl + ((mlo >> (8 * i)) & 15u) * 16u), b = *(const LAS u32x4*)(tbl + ((mhi >> (8 * i)) & 15u) * 16u);
; #pragma unroll
;             for (int e = 0; e < 4; ++e) { p0[4 * i + e] = __uint_as_float(a[e]); p1[4 * i + e] = __uint_as_float(b[e]); } }
; __device__ __forceinline__ void dsa_block_unit(int b, int g, int m  , const bf16_t* Q, const bf16_t* K, const bf16_t* V, const unsigned long long* mask, bf16_t* O, LAS char* L, int wid, int lane, float sbound  ) {
;     ...
;     asm volatile("s_waitcnt vmcnt(0) lgkmcnt(0)\n\ts_barrier" ::: "memory");
;     const LAS char* tblp = L + DL_T;
;     f32x16 pa0, pa1, pb0, pb1; dsa_qk(pa0, pa1, kp0, qr, mwn, hi, mref, fixed ? tblp : (const LAS char*)nullptr);
.LBB0_1748:
	s_waitcnt vmcnt(0) lgkmcnt(0)
	s_barrier
	ds_read_b128 v[30:33], v174
	ds_read_b128 v[26:29], v174 offset:512
	ds_read_b128 v[22:25], v174 offset:2048
	ds_read_b128 v[2:5], v174 offset:2560
	ds_read_b128 v[6:9], v174 offset:4096
	ds_read_b128 v[10:13], v174 offset:4608
	ds_read_b128 v[14:17], v174 offset:6144
	ds_read_b128 v[18:21], v174 offset:6656
	s_waitcnt vmcnt(0)
	v_lshrrev_b32_e32 v66, v176, v34
	v_lshrrev_b32_e32 v0, v176, v35
	s_and_saveexec_b64 s[0:1], s[4:5]
	s_xor_b64 s[20:21], exec, s[0:1]
	s_cbranch_execz .LBB0_1750
	v_lshlrev_b32_e32 v34, 4, v66
	v_lshlrev_b32_e32 v35, 4, v0
	s_add_i32 s0, 0, 0x14800
	v_mov_b32_e32 v206, 0xf0
	v_and_or_b32 v34, v34, v206, s0
	v_and_or_b32 v38, v35, v206, s0
	ds_read_b128 v[34:37], v34
	ds_read_b128 v[50:53], v38
	v_lshrrev_b32_e32 v38, 4, v66
	v_lshrrev_b32_e32 v39, 4, v0
	v_and_or_b32 v38, v38, v206, s0
	v_and_or_b32 v42, v39, v206, s0
	ds_read_b128 v[38:41], v38
	ds_read_b128 v[54:57], v42
	v_lshrrev_b32_e32 v42, 12, v66
	v_lshrrev_b32_e32 v43, 12, v0
	v_and_or_b32 v42, v42, v206, s0
	v_and_or_b32 v46, v43, v206, s0
	ds_read_b128 v[42:45], v42
	ds_read_b128 v[58:61], v46
	v_lshrrev_b32_e32 v46, 20, v66
	v_lshrrev_b32_e32 v0, 20, v0
	v_and_or_b32 v46, v46, v206, s0
	v_and_or_b32 v0, v0, v206, s0
	ds_read_b128 v[46:49], v46
	ds_read_b128 v[62:65], v0

; #define LAS __attribute__((address_space(3)))
; __device__ __forceinline__ void dsa_qk(f32x16& p0, f32x16& p1, const LAS char* kp, const bf16x8 (&qr)[4], unsigned long long mw, int hi, float mref, const LAS char* tbl) {
;     bf16x8 kf[8];
; #pragma unroll
;     for (int d0 = 0; d0 < 4; ++d0) { kf[2 * d0] = *(const LAS bf16x8*)(kp + d0 * 2048); kf[2 * d0 + 1] = *(const LAS bf16x8*)(kp + d0 * 2048 + 512); }
;     const unsigned mlo = (unsigned)mw >> (4 * hi), mhi = (unsigned)(mw >> 32) >> (4 * hi), negm = __float_as_uint(-mref);
;     if (tbl) {
; #pragma unroll
;         for (int i = 0; i < 4; ++i) { const u32x4 a = *(const LAS u32x4*)(tbl + ((mlo >> (8 * i)) & 15u) * 16u), b = *(const LAS u32x4*)(tbl + ((mhi >> (8 * i)) & 15u) * 16u);
; #pragma unroll
;             for (int e = 0; e < 4; ++e) { p0[4 * i + e] = __uint_as_float(a[e]); p1[4 * i + e] = __uint_as_float(b[e]); } }
; __device__ __forceinline__ void dsa_step(f32x16& c0, f32x16& c1, f32x16& n0, f32x16& n1, const bool have_n, const LAS char* kpn, const LAS char* vpc, const bf16x8 (&qr)[4], unsigned long long mwn, ...
;     if (have_n) dsa_qk(n0, n1, kpn, qr, mwn, hi, mref, fixed ? tblp : (const LAS char*)nullptr);
;     bf16x8 vf[8]; pv_load(vf, vpc);
.LBB0_1757:
	s_add_i32 s0, s35, -3
	s_cmp_lt_u32 s0, s53
	s_cselect_b64 s[22:23], -1, 0
	s_cmp_ge_u32 s0, s53
	s_cbranch_scc1 .LBB0_1763
	v_add_u32_e32 v0, s34, v174
	ds_read_b128 v[142:145], v0
	ds_read_b128 v[138:141], v0 offset:512
	ds_read_b128 v[134:137], v0 offset:2048
	ds_read_b128 v[130:133], v0 offset:2560
	ds_read_b128 v[126:129], v0 offset:4096
	ds_read_b128 v[122:125], v0 offset:4608
	ds_read_b128 v[118:121], v0 offset:6144
	ds_read_b128 v[114:117], v0 offset:6656
	v_lshrrev_b32_e32 v148, v176, v148
	v_lshrrev_b32_e32 v0, v176, v149
	s_and_saveexec_b64 s[0:1], s[4:5]
	s_xor_b64 s[24:25], exec, s[0:1]
	s_cbranch_execz .LBB0_1760
	v_lshlrev_b32_e32 v66, 4, v148
	v_lshlrev_b32_e32 v67, 4, v0
	v_lshrrev_b32_e32 v70, 4, v148
	v_lshrrev_b32_e32 v71, 4, v0
	v_lshrrev_b32_e32 v74, 12, v148
	v_lshrrev_b32_e32 v75, 12, v0
	v_lshrrev_b32_e32 v78, 20, v148
	s_add_i32 s0, 0, 0x14800
	v_mov_b32_e32 v206, 0xf0
	v_lshrrev_b32_e32 v0, 20, v0
	v_and_or_b32 v66, v66, v206, s0
	v_and_or_b32 v67, v67, v206, s0
	v_and_or_b32 v70, v70, v206, s0
	v_and_or_b32 v71, v71, v206, s0
	v_and_or_b32 v74, v74, v206, s0
	v_and_or_b32 v75, v75, v206, s0
	v_and_or_b32 v78, v78, v206, s0
	ds_read_b128 v[82:85], v66
	ds_read_b128 v[66:69], v67
	ds_read_b128 v[86:89], v70
	ds_read_b128 v[70:73], v71
	ds_read_b128 v[90:93], v74
	ds_read_b128 v[74:77], v75
	v_and_or_b32 v0, v0, v206, s0
	ds_read_b128 v[94:97], v78
	ds_read_b128 v[78:81], v0

; #define LAS __attribute__((address_space(3)))
; __device__ __forceinline__ void dsa_qk(f32x16& p0, f32x16& p1, const LAS char* kp, const bf16x8 (&qr)[4], unsigned long long mw, int hi, float mref, const LAS char* tbl) {
;     bf16x8 kf[8];
; #pragma unroll
;     for (int d0 = 0; d0 < 4; ++d0) { kf[2 * d0] = *(const LAS bf16x8*)(kp + d0 * 2048); kf[2 * d0 + 1] = *(const LAS bf16x8*)(kp + d0 * 2048 + 512); }
;     const unsigned mlo = (unsigned)mw >> (4 * hi), mhi = (unsigned)(mw >> 32) >> (4 * hi), negm = __float_as_uint(-mref);
;     if (tbl) {
; #pragma unroll
;         for (int i = 0; i < 4; ++i) { const u32x4 a = *(const LAS u32x4*)(tbl + ((mlo >> (8 * i)) & 15u) * 16u), b = *(const LAS u32x4*)(tbl + ((mhi >> (8 * i)) & 15u) * 16u);
; #pragma unroll
;             for (int e = 0; e < 4; ++e) { p0[4 * i + e] = __uint_as_float(a[e]); p1[4 * i + e] = __uint_as_float(b[e]); } }
; __device__ __forceinline__ void dsa_step(f32x16& c0, f32x16& c1, f32x16& n0, f32x16& n1, const bool have_n, const LAS char* kpn, const LAS char* vpc, const bf16x8 (&qr)[4], unsigned long long mwn, ...
;     if (have_n) dsa_qk(n0, n1, kpn, qr, mwn, hi, mref, fixed ? tblp : (const LAS char*)nullptr);
;     bf16x8 vf[8]; pv_load(vf, vpc);
.LBB0_1770:
	s_add_i32 s0, s35, -2
	s_cmp_lt_u32 s0, s53
	s_cselect_b64 s[22:23], -1, 0
	s_cmp_ge_u32 s0, s53
	s_cbranch_scc1 .LBB0_1776
	v_add_u32_e32 v0, s36, v174
	ds_read_b128 v[142:145], v0
	ds_read_b128 v[138:141], v0 offset:512
	ds_read_b128 v[134:137], v0 offset:2048
	ds_read_b128 v[130:133], v0 offset:2560
	ds_read_b128 v[126:129], v0 offset:4096
	ds_read_b128 v[122:125], v0 offset:4608
	ds_read_b128 v[118:121], v0 offset:6144
	ds_read_b128 v[114:117], v0 offset:6656
	v_lshrrev_b32_e32 v161, v176, v166
	v_lshrrev_b32_e32 v0, v176, v167
	s_and_saveexec_b64 s[0:1], s[4:5]
	s_xor_b64 s[24:25], exec, s[0:1]
	s_cbranch_execz .LBB0_1773
	v_lshlrev_b32_e32 v34, 4, v161
	v_lshlrev_b32_e32 v35, 4, v0
	s_add_i32 s0, 0, 0x14800
	v_mov_b32_e32 v206, 0xf0
	v_and_or_b32 v34, v34, v206, s0
	v_and_or_b32 v38, v35, v206, s0
	ds_read_b128 v[34:37], v34
	ds_read_b128 v[50:53], v38
	v_lshrrev_b32_e32 v38, 4, v161
	v_lshrrev_b32_e32 v39, 4, v0
	v_and_or_b32 v38, v38, v206, s0
	v_and_or_b32 v42, v39, v206, s0
	ds_read_b128 v[38:41], v38
	ds_read_b128 v[54:57], v42
	v_lshrrev_b32_e32 v42, 12, v161
	v_lshrrev_b32_e32 v43, 12, v0
	v_and_or_b32 v42, v42, v206, s0
	v_and_or_b32 v46, v43, v206, s0
	ds_read_b128 v[42:45], v42
	ds_read_b128 v[58:61], v46
	v_lshrrev_b32_e32 v46, 20, v161
	v_lshrrev_b32_e32 v0, 20, v0
	v_and_or_b32 v46, v46, v206, s0
	v_and_or_b32 v0, v0, v206, s0
	ds_read_b128 v[46:49], v46
	ds_read_b128 v[62:65], v0

; __device__ __forceinline__ float shfl_xor_f(float v, int mask, int lane) { return __int_as_float(__builtin_amdgcn_ds_bpermute((lane ^ mask) << 2, __float_as_int(v))); }
; __device__ __forceinline__ void quant_rows(unsigned char* ws, size_t xq_off, size_t sar_off, int gw, int NGW, int lane) {
;     ...
;         for (int q = 0; q < 8; ++q) { const u32x4* p = (const u32x4*)(xb + (size_t)(m + q * NGW) * D + 16 * lane); a[q][0] = p[0]; a[q][1] = p[1]; }
;         float ssv = 0.f;
;         if (lane < 32) { const f32x4 s4 = *(const f32x4*)(ssp + (size_t)(m + (lane >> 2) * NGW) * 16 + 4 * (lane & 3)); ssv = (s4[0] + s4[1]) + (s4[2] + s4[3]); }
;         ssv += shfl_xor_f(ssv, 1, lane); ssv += shfl_xor_f(ssv, 2, lane);
; #pragma unroll
;         for (int q = 0; q < 8; ++q) { float t = 0.f;
; #pragma unroll
;             for (int i = 0; i < 8; ++i) { const unsigned wd = a[q][i >> 2][i & 3]; t = __builtin_fmaxf(t, __builtin_fmaxf(__builtin_fabsf(__uint_as_float(wd << 16)), __builtin_fabsf(__uint_as_float(wd & 0xFFFF0000u)))); }
;             mx[q] = t; }
.LBB0_2007:
	s_or_b64 exec, exec, s[24:25]
	ds_bpermute_b32 v80, v75, v73
	s_waitcnt vmcnt(14)
	v_lshlrev_b32_e32 v151, 16, v62
	v_and_b32_e32 v149, 0xffff0000, v62
	v_max_f32_e64 v81, |v149|, |v149|
	v_max_f32_e64 v82, |v151|, |v151|
	v_lshlrev_b32_e32 v152, 16, v63
	v_and_b32_e32 v150, 0xffff0000, v63
	s_waitcnt lgkmcnt(0)
	v_add_f32_e32 v62, v73, v80
	v_max_f32_e32 v80, v82, v81
	v_max_f32_e64 v63, |v150|, |v150|
	v_max_f32_e64 v81, |v152|, |v152|
	v_max_f32_e32 v63, v81, v63
	v_lshlrev_b32_e32 v148, 16, v64
	v_and_b32_e32 v146, 0xffff0000, v64
	v_max3_f32 v63, v80, 0, v63
	v_max_f32_e64 v64, |v146|, |v146|
	v_max_f32_e64 v80, |v148|, |v148|
	v_lshlrev_b32_e32 v147, 16, v65
	v_and_b32_e32 v145, 0xffff0000, v65
	v_max_f32_e32 v64, v80, v64
	v_max_f32_e64 v65, |v145|, |v145|
	v_max_f32_e64 v80, |v147|, |v147|
	v_max_f32_e32 v65, v80, v65
	v_lshlrev_b32_e32 v144, 16, v58
	v_and_b32_e32 v142, 0xffff0000, v58
	v_max3_f32 v63, v63, v64, v65
	v_max_f32_e64 v58, |v142|, |v142|
	v_max_f32_e64 v64, |v144|, |v144|
	v_lshlrev_b32_e32 v143, 16, v59
	v_and_b32_e32 v141, 0xffff0000, v59
	v_max_f32_e32 v58, v64, v58
	v_max_f32_e64 v59, |v141|, |v141|
	v_max_f32_e64 v64, |v143|, |v143|
	v_max_f32_e32 v59, v64, v59
	v_lshlrev_b32_e32 v140, 16, v60
	v_and_b32_e32 v138, 0xffff0000, v60
	v_max3_f32 v58, v63, v58, v59
	v_max_f32_e64 v59, |v138|, |v138|
	v_max_f32_e64 v60, |v140|, |v140|
	v_lshlrev_b32_e32 v139, 16, v61
	v_and_b32_e32 v137, 0xffff0000, v61
	v_max_f32_e32 v59, v60, v59
	v_max_f32_e64 v60, |v137|, |v137|
	v_max_f32_e64 v61, |v139|, |v139|
	v_max_f32_e32 v60, v61, v60
	s_waitcnt vmcnt(12)
	v_lshlrev_b32_e32 v136, 16, v54
	v_and_b32_e32 v134, 0xffff0000, v54
	v_max3_f32 v64, v58, v59, v60
	v_max_f32_e64 v54, |v134|, |v134|
	v_max_f32_e64 v58, |v136|, |v136|
	v_lshlrev_b32_e32 v135, 16, v55
	v_and_b32_e32 v133, 0xffff0000, v55
	v_max_f32_e32 v54, v58, v54
	v_max_f32_e64 v55, |v133|, |v133|
	v_max_f32_e64 v58, |v135|, |v135|
	v_max_f32_e32 v55, v58, v55
	v_lshlrev_b32_e32 v132, 16, v56
	v_and_b32_e32 v130, 0xffff0000, v56
	v_max3_f32 v54, v54, 0, v55
	v_max_f32_e64 v55, |v130|, |v130|
	v_max_f32_e64 v56, |v132|, |v132|
	v_lshlrev_b32_e32 v131, 16, v57
	v_and_b32_e32 v129, 0xffff0000, v57
	v_max_f32_e32 v55, v56, v55
	v_max_f32_e64 v56, |v129|, |v129|
	v_max_f32_e64 v57, |v131|, |v131|
	v_max_f32_e32 v56, v57, v56
	v_lshlrev_b32_e32 v128, 16, v50
	v_and_b32_e32 v126, 0xffff0000, v50
	v_max3_f32 v54, v54, v55, v56
	v_max_f32_e64 v50, |v126|, |v126|
	v_max_f32_e64 v55, |v128|, |v128|
	v_lshlrev_b32_e32 v127, 16, v51
	v_and_b32_e32 v125, 0xffff0000, v51
	v_max_f32_e32 v50, v55, v50
	v_max_f32_e64 v51, |v125|, |v125|
	v_max_f32_e64 v55, |v127|, |v127|
	v_max_f32_e32 v51, v55, v51
	v_lshlrev_b32_e32 v124, 16, v52
	v_and_b32_e32 v122, 0xffff0000, v52
	v_max3_f32 v50, v54, v50, v51
	v_max_f32_e64 v51, |v122|, |v122|
	v_max_f32_e64 v52, |v124|, |v124|
	v_lshlrev_b32_e32 v123, 16, v53
	v_and_b32_e32 v121, 0xffff0000, v53
	v_max_f32_e32 v51, v52, v51
	v_max_f32_e64 v52, |v121|, |v121|
	v_max_f32_e64 v53, |v123|, |v123|
	v_max_f32_e32 v52, v53, v52
	s_waitcnt vmcnt(10)
	v_lshlrev_b32_e32 v120, 16, v46
	v_and_b32_e32 v118, 0xffff0000, v46
	v_max3_f32 v83, v50, v51, v52
	v_max_f32_e64 v46, |v118|, |v118|
	v_max_f32_e64 v50, |v120|, |v120|
	v_lshlrev_b32_e32 v119, 16, v47
	v_and_b32_e32 v117, 0xffff0000, v47
	v_max_f32_e32 v46, v50, v46
	v_max_f32_e64 v47, |v117|, |v117|
	v_max_f32_e64 v50, |v119|, |v119|
	v_max_f32_e32 v47, v50, v47
	v_lshlrev_b32_e32 v116, 16, v48
	v_and_b32_e32 v114, 0xffff0000, v48
	v_max3_f32 v46, v46, 0, v47
	v_max_f32_e64 v47, |v114|, |v114|
	v_max_f32_e64 v48, |v116|, |v116|
	v_lshlrev_b32_e32 v115, 16, v49
	v_and_b32_e32 v113, 0xffff0000, v49
	v_max_f32_e32 v47, v48, v47
	v_max_f32_e64 v48, |v113|, |v113|
	v_max_f32_e64 v49, |v115|, |v115|
	v_max_f32_e32 v48, v49, v48
	v_lshlrev_b32_e32 v112, 16, v42
	v_and_b32_e32 v110, 0xffff0000, v42
	v_max3_f32 v46, v46, v47, v48
	v_max_f32_e64 v42, |v110|, |v110|
	v_max_f32_e64 v47, |v112|, |v112|
	v_lshlrev_b32_e32 v111, 16, v43
	v_and_b32_e32 v109, 0xffff0000, v43
	v_max_f32_e32 v42, v47, v42
	v_max_f32_e64 v43, |v109|, |v109|
	v_max_f32_e64 v47, |v111|, |v111|
	v_max_f32_e32 v43, v47, v43
	v_lshlrev_b32_e32 v108, 16, v44
	v_and_b32_e32 v106, 0xffff0000, v44
	v_max3_f32 v42, v46, v42, v43
	v_max_f32_e64 v43, |v106|, |v106|
	v_max_f32_e64 v44, |v108|, |v108|
	v_lshlrev_b32_e32 v107, 16, v45
	v_and_b32_e32 v105, 0xffff0000, v45
	v_max_f32_e32 v43, v44, v43
	v_max_f32_e64 v44, |v105|, |v105|
	v_max_f32_e64 v45, |v107|, |v107|
	v_max_f32_e32 v44, v45, v44
	s_waitcnt vmcnt(8)
	v_lshlrev_b32_e32 v104, 16, v38
	v_and_b32_e32 v102, 0xffff0000, v38
	v_max3_f32 v84, v42, v43, v44
	v_max_f32_e64 v38, |v102|, |v102|
	v_max_f32_e64 v42, |v104|, |v104|
	v_lshlrev_b32_e32 v103, 16, v39
	v_and_b32_e32 v101, 0xffff0000, v39
	v_max_f32_e32 v38, v42, v38
	v_max_f32_e64 v39, |v101|, |v101|
	v_max_f32_e64 v42, |v103|, |v103|
	v_max_f32_e32 v39, v42, v39
	v_lshlrev_b32_e32 v100, 16, v40
	v_and_b32_e32 v97, 0xffff0000, v40
	v_max3_f32 v38, v38, 0, v39
	v_max_f32_e64 v39, |v97|, |v97|
	v_max_f32_e64 v40, |v100|, |v100|
	v_lshlrev_b32_e32 v98, 16, v41
	v_and_b32_e32 v96, 0xffff0000, v41
	v_max_f32_e32 v39, v40, v39
	v_max_f32_e64 v40, |v96|, |v96|
	v_max_f32_e64 v41, |v98|, |v98|
	v_max_f32_e32 v40, v41, v40
	v_lshlrev_b32_e32 v95, 16, v34
	v_and_b32_e32 v92, 0xffff0000, v34
	v_max3_f32 v38, v38, v39, v40
	v_max_f32_e64 v34, |v92|, |v92|
	v_max_f32_e64 v39, |v95|, |v95|
	v_lshlrev_b32_e32 v94, 16, v35
	v_and_b32_e32 v91, 0xffff0000, v35
	v_max_f32_e32 v34, v39, v34
	v_max_f32_e64 v35, |v91|, |v91|
	v_max_f32_e64 v39, |v94|, |v94|
	v_max_f32_e32 v35, v39, v35
	v_lshlrev_b32_e32 v90, 16, v36
	v_and_b32_e32 v88, 0xffff0000, v36
	v_max3_f32 v34, v38, v34, v35
	v_max_f32_e64 v35, |v88|, |v88|
	v_max_f32_e64 v36, |v90|, |v90|
	v_lshlrev_b32_e32 v89, 16, v37
	v_and_b32_e32 v87, 0xffff0000, v37
	v_max_f32_e32 v35, v36, v35
	v_max_f32_e64 v36, |v87|, |v87|
	v_max_f32_e64 v37, |v89|, |v89|
	v_max_f32_e32 v36, v37, v36
	s_waitcnt vmcnt(6)
; __device__ __forceinline__ float shfl_xor_f(float v, int mask, int lane) { return __int_as_float(__builtin_amdgcn_ds_bpermute((lane ^ mask) << 2, __float_as_int(v))); }
; __device__ __forceinline__ void quant_rows(unsigned char* ws, size_t xq_off, size_t sar_off, int gw, int NGW, int lane) {
;     ...
;         for (int q = 0; q < 8; ++q) { float t = 0.f;
; #pragma unroll
;             for (int i = 0; i < 8; ++i) { const unsigned wd = a[q][i >> 2][i & 3]; t = __builtin_fmaxf(t, __builtin_fmaxf(__builtin_fabsf(__uint_as_float(wd << 16)), __builtin_fabsf(__uint_as_float(wd & 0xFFFF0000u)))); }
;             mx[q] = t; }
; #pragma unroll
;         for (int o = 1; o < 64; o <<= 1) {
; #pragma unroll
;             for (int q = 0; q < 8; ++q) mx[q] = __builtin_fmaxf(mx[q], shfl_xor_f(mx[q], o, lane)); }
	v_lshlrev_b32_e32 v82, 16, v30
	v_and_b32_e32 v80, 0xffff0000, v30
	v_max3_f32 v85, v34, v35, v36
	v_max_f32_e64 v30, |v80|, |v80|
	v_max_f32_e64 v34, |v82|, |v82|
	v_lshlrev_b32_e32 v81, 16, v31
	v_and_b32_e32 v65, 0xffff0000, v31
	v_max_f32_e32 v30, v34, v30
	v_max_f32_e64 v31, |v65|, |v65|
	v_max_f32_e64 v34, |v81|, |v81|
	v_max_f32_e32 v31, v34, v31
	v_lshlrev_b32_e32 v63, 16, v32
	v_and_b32_e32 v60, 0xffff0000, v32
	v_max3_f32 v30, v30, 0, v31
	v_max_f32_e64 v31, |v60|, |v60|
	v_max_f32_e64 v32, |v63|, |v63|
	v_lshlrev_b32_e32 v61, 16, v33
	v_and_b32_e32 v59, 0xffff0000, v33
	v_max_f32_e32 v31, v32, v31
	v_max_f32_e64 v32, |v59|, |v59|
	v_max_f32_e64 v33, |v61|, |v61|
	v_max_f32_e32 v32, v33, v32
	v_lshlrev_b32_e32 v58, 16, v26
	v_and_b32_e32 v56, 0xffff0000, v26
	v_max3_f32 v30, v30, v31, v32
	v_max_f32_e64 v26, |v56|, |v56|
	v_max_f32_e64 v31, |v58|, |v58|
	v_lshlrev_b32_e32 v57, 16, v27
	v_and_b32_e32 v55, 0xffff0000, v27
	v_max_f32_e32 v26, v31, v26
	v_max_f32_e64 v27, |v55|, |v55|
	v_max_f32_e64 v31, |v57|, |v57|
	v_max_f32_e32 v27, v31, v27
	v_lshlrev_b32_e32 v54, 16, v28
	v_and_b32_e32 v52, 0xffff0000, v28
	v_max3_f32 v26, v30, v26, v27
	v_max_f32_e64 v27, |v52|, |v52|
	v_max_f32_e64 v28, |v54|, |v54|
	v_lshlrev_b32_e32 v53, 16, v29
	v_and_b32_e32 v51, 0xffff0000, v29
	v_max_f32_e32 v27, v28, v27
	v_max_f32_e64 v28, |v51|, |v51|
	v_max_f32_e64 v29, |v53|, |v53|
	v_max_f32_e32 v28, v29, v28
	s_waitcnt vmcnt(4)
	v_lshlrev_b32_e32 v50, 16, v22
	v_and_b32_e32 v48, 0xffff0000, v22
	v_max3_f32 v86, v26, v27, v28
	v_max_f32_e64 v22, |v48|, |v48|
	v_max_f32_e64 v26, |v50|, |v50|
	v_lshlrev_b32_e32 v49, 16, v23
	v_and_b32_e32 v47, 0xffff0000, v23
	v_max_f32_e32 v22, v26, v22
	v_max_f32_e64 v23, |v47|, |v47|
	v_max_f32_e64 v26, |v49|, |v49|
	v_max_f32_e32 v23, v26, v23
	v_lshlrev_b32_e32 v46, 16, v24
	v_and_b32_e32 v44, 0xffff0000, v24
	v_max3_f32 v22, v22, 0, v23
	v_max_f32_e64 v23, |v44|, |v44|
	v_max_f32_e64 v24, |v46|, |v46|
	v_lshlrev_b32_e32 v45, 16, v25
	v_and_b32_e32 v43, 0xffff0000, v25
	v_max_f32_e32 v23, v24, v23
	v_max_f32_e64 v24, |v43|, |v43|
	v_max_f32_e64 v25, |v45|, |v45|
	v_max_f32_e32 v24, v25, v24
	v_lshlrev_b32_e32 v42, 16, v18
	v_and_b32_e32 v40, 0xffff0000, v18
	v_max3_f32 v22, v22, v23, v24
	v_max_f32_e64 v18, |v40|, |v40|
	v_max_f32_e64 v23, |v42|, |v42|
	v_lshlrev_b32_e32 v41, 16, v19
	v_and_b32_e32 v39, 0xffff0000, v19
	v_max_f32_e32 v18, v23, v18
	v_max_f32_e64 v19, |v39|, |v39|
	v_max_f32_e64 v23, |v41|, |v41|
	v_max_f32_e32 v19, v23, v19
	v_lshlrev_b32_e32 v38, 16, v20
	v_and_b32_e32 v36, 0xffff0000, v20
	v_max3_f32 v18, v22, v18, v19
	v_max_f32_e64 v19, |v36|, |v36|
	v_max_f32_e64 v20, |v38|, |v38|
	v_lshlrev_b32_e32 v37, 16, v21
	v_and_b32_e32 v35, 0xffff0000, v21
	v_max_f32_e32 v19, v20, v19
	v_max_f32_e64 v20, |v35|, |v35|
	v_max_f32_e64 v21, |v37|, |v37|
	v_max_f32_e32 v20, v21, v20
	s_waitcnt vmcnt(2)
	v_lshlrev_b32_e32 v34, 16, v14
	v_and_b32_e32 v32, 0xffff0000, v14
	v_max3_f32 v93, v18, v19, v20
	v_max_f32_e64 v14, |v32|, |v32|
	v_max_f32_e64 v18, |v34|, |v34|
	v_lshlrev_b32_e32 v33, 16, v15
	v_and_b32_e32 v31, 0xffff0000, v15
	v_max_f32_e32 v14, v18, v14
	v_max_f32_e64 v15, |v31|, |v31|
	v_max_f32_e64 v18, |v33|, |v33|
	v_max_f32_e32 v15, v18, v15
	v_lshlrev_b32_e32 v30, 16, v16
	v_and_b32_e32 v28, 0xffff0000, v16
	v_max3_f32 v14, v14, 0, v15
	v_max_f32_e64 v15, |v28|, |v28|
	v_max_f32_e64 v16, |v30|, |v30|
	v_lshlrev_b32_e32 v29, 16, v17
	v_and_b32_e32 v27, 0xffff0000, v17
	v_max_f32_e32 v15, v16, v15
	v_max_f32_e64 v16, |v27|, |v27|
	v_max_f32_e64 v17, |v29|, |v29|
	v_max_f32_e32 v16, v17, v16
	v_lshlrev_b32_e32 v26, 16, v10
	v_and_b32_e32 v24, 0xffff0000, v10
	v_max3_f32 v14, v14, v15, v16
	v_max_f32_e64 v10, |v24|, |v24|
	v_max_f32_e64 v15, |v26|, |v26|
	v_lshlrev_b32_e32 v25, 16, v11
	v_and_b32_e32 v23, 0xffff0000, v11
	v_max_f32_e32 v10, v15, v10
	v_max_f32_e64 v11, |v23|, |v23|
	v_max_f32_e64 v15, |v25|, |v25|
	v_max_f32_e32 v11, v15, v11
	v_lshlrev_b32_e32 v22, 16, v12
	v_and_b32_e32 v20, 0xffff0000, v12
	v_max3_f32 v10, v14, v10, v11
	v_max_f32_e64 v11, |v20|, |v20|
	v_max_f32_e64 v12, |v22|, |v22|
	v_lshlrev_b32_e32 v21, 16, v13
	v_and_b32_e32 v19, 0xffff0000, v13
	v_max_f32_e32 v11, v12, v11
	v_max_f32_e64 v12, |v19|, |v19|
	v_max_f32_e64 v13, |v21|, |v21|
	v_max_f32_e32 v12, v13, v12
	s_waitcnt vmcnt(0)
	v_lshlrev_b32_e32 v18, 16, v6
	v_and_b32_e32 v16, 0xffff0000, v6
	v_max3_f32 v99, v10, v11, v12
	v_max_f32_e64 v6, |v16|, |v16|
	v_max_f32_e64 v10, |v18|, |v18|
	v_lshlrev_b32_e32 v17, 16, v7
	v_and_b32_e32 v15, 0xffff0000, v7
	v_max_f32_e32 v6, v10, v6
	v_max_f32_e64 v7, |v15|, |v15|
	v_max_f32_e64 v10, |v17|, |v17|
	v_max_f32_e32 v7, v10, v7
	v_lshlrev_b32_e32 v14, 16, v8
	v_and_b32_e32 v12, 0xffff0000, v8
	v_max3_f32 v6, v6, 0, v7
	v_max_f32_e64 v7, |v12|, |v12|
	v_max_f32_e64 v8, |v14|, |v14|
	v_lshlrev_b32_e32 v13, 16, v9
	v_and_b32_e32 v11, 0xffff0000, v9
	v_max_f32_e32 v7, v8, v7
	v_max_f32_e64 v8, |v11|, |v11|
	v_max_f32_e64 v9, |v13|, |v13|
	v_max_f32_e32 v8, v9, v8
	v_max3_f32 v6, v6, v7, v8
	v_lshlrev_b32_e32 v10, 16, v2
	v_and_b32_e32 v8, 0xffff0000, v2
	v_max_f32_e64 v2, |v8|, |v8|
	v_max_f32_e64 v7, |v10|, |v10|
	v_max_f32_e32 v2, v7, v2
	v_lshlrev_b32_e32 v9, 16, v3
	v_and_b32_e32 v7, 0xffff0000, v3
	v_max_f32_e64 v3, |v7|, |v7|
	v_max_f32_e64 v153, |v9|, |v9|
	v_max_f32_e32 v3, v153, v3
	v_max3_f32 v153, v6, v2, v3
	v_lshlrev_b32_e32 v6, 16, v4
	v_and_b32_e32 v3, 0xffff0000, v4
	v_max_f32_e64 v2, |v3|, |v3|
	v_max_f32_e64 v4, |v6|, |v6|
	ds_bpermute_b32 v155, v75, v64
	v_max_f32_e32 v154, v4, v2
	v_lshlrev_b32_e32 v4, 16, v5
	v_and_b32_e32 v2, 0xffff0000, v5
	v_max_f32_e64 v5, |v2|, |v2|
	v_max_f32_e64 v156, |v4|, |v4|
	v_max_f32_e32 v5, v156, v5
	ds_bpermute_b32 v156, v75, v83
	v_max3_f32 v5, v153, v154, v5
	ds_bpermute_b32 v154, v75, v84
	s_waitcnt lgkmcnt(2)
; __device__ __forceinline__ float shfl_xor_f(float v, int mask, int lane) { return __int_as_float(__builtin_amdgcn_ds_bpermute((lane ^ mask) << 2, __float_as_int(v))); }
; __device__ __forceinline__ void quant_rows(unsigned char* ws, size_t xq_off, size_t sar_off, int gw, int NGW, int lane) {
;     ...
; #pragma unroll
;         for (int o = 1; o < 64; o <<= 1) {
; #pragma unroll
;             for (int q = 0; q < 8; ++q) mx[q] = __builtin_fmaxf(mx[q], shfl_xor_f(mx[q], o, lane)); }
	v_max_f32_e32 v153, v155, v155
	ds_bpermute_b32 v155, v75, v85
	v_max_f32_e32 v64, v64, v153
	s_waitcnt lgkmcnt(2)
	v_max_f32_e32 v153, v156, v156
	v_max_f32_e32 v83, v83, v153
	s_waitcnt lgkmcnt(1)
	v_max_f32_e32 v153, v154, v154
	ds_bpermute_b32 v154, v75, v86
	v_max_f32_e32 v84, v84, v153
	s_waitcnt lgkmcnt(1)
	v_max_f32_e32 v153, v155, v155
	ds_bpermute_b32 v155, v75, v93
	v_max_f32_e32 v85, v85, v153
	s_waitcnt lgkmcnt(1)
	v_max_f32_e32 v153, v154, v154
	ds_bpermute_b32 v154, v75, v99
	v_max_f32_e32 v86, v86, v153
	s_waitcnt lgkmcnt(1)
	v_max_f32_e32 v153, v155, v155
	ds_bpermute_b32 v155, v75, v5
	v_max_f32_e32 v93, v93, v153
	s_waitcnt lgkmcnt(1)
	v_max_f32_e32 v153, v154, v154
	ds_bpermute_b32 v154, v76, v64
	v_max_f32_e32 v99, v99, v153
	s_waitcnt lgkmcnt(1)
	v_max_f32_e32 v153, v155, v155
	ds_bpermute_b32 v155, v76, v83
	v_max_f32_e32 v5, v5, v153
	s_waitcnt lgkmcnt(1)
	v_max_f32_e32 v153, v154, v154
	ds_bpermute_b32 v154, v76, v84
	v_max_f32_e32 v64, v64, v153
	s_waitcnt lgkmcnt(1)
	v_max_f32_e32 v153, v155, v155
	ds_bpermute_b32 v155, v76, v85
	v_max_f32_e32 v83, v83, v153
	s_waitcnt lgkmcnt(1)
	v_max_f32_e32 v153, v154, v154
	ds_bpermute_b32 v154, v76, v86
	v_max_f32_e32 v84, v84, v153
	s_waitcnt lgkmcnt(1)
	v_max_f32_e32 v153, v155, v155
	ds_bpermute_b32 v155, v76, v93
	v_max_f32_e32 v85, v85, v153
	s_waitcnt lgkmcnt(1)
	v_max_f32_e32 v153, v154, v154
	ds_bpermute_b32 v154, v76, v99
	v_max_f32_e32 v86, v86, v153
	s_waitcnt lgkmcnt(1)
	v_max_f32_e32 v153, v155, v155
	ds_bpermute_b32 v155, v76, v5
	v_max_f32_e32 v93, v93, v153
	s_waitcnt lgkmcnt(1)
	v_max_f32_e32 v153, v154, v154
	ds_bpermute_b32 v154, v0, v64
	v_max_f32_e32 v99, v99, v153
	s_waitcnt lgkmcnt(1)
	v_max_f32_e32 v153, v155, v155
	ds_bpermute_b32 v155, v0, v83
	v_max_f32_e32 v5, v5, v153
	s_waitcnt lgkmcnt(1)
	v_max_f32_e32 v153, v154, v154
	ds_bpermute_b32 v154, v0, v84
	v_max_f32_e32 v64, v64, v153
	s_waitcnt lgkmcnt(1)
	v_max_f32_e32 v153, v155, v155
	ds_bpermute_b32 v155, v0, v85
	v_max_f32_e32 v83, v83, v153
	s_waitcnt lgkmcnt(1)
	v_max_f32_e32 v153, v154, v154
	ds_bpermute_b32 v154, v0, v86
	v_max_f32_e32 v84, v84, v153
	s_waitcnt lgkmcnt(1)
	v_max_f32_e32 v153, v155, v155
	ds_bpermute_b32 v155, v0, v93
	v_max_f32_e32 v85, v85, v153
	s_waitcnt lgkmcnt(1)
	v_max_f32_e32 v153, v154, v154
	ds_bpermute_b32 v154, v0, v99
	v_max_f32_e32 v86, v86, v153
	s_waitcnt lgkmcnt(1)
	v_max_f32_e32 v153, v155, v155
	ds_bpermute_b32 v155, v0, v5
	v_max_f32_e32 v93, v93, v153
	s_waitcnt lgkmcnt(1)
	v_max_f32_e32 v153, v154, v154
	ds_bpermute_b32 v154, v77, v64
	v_max_f32_e32 v99, v99, v153
	s_waitcnt lgkmcnt(1)
	v_max_f32_e32 v153, v155, v155
	ds_bpermute_b32 v155, v77, v83
	v_max_f32_e32 v5, v5, v153
	s_waitcnt lgkmcnt(1)
	v_max_f32_e32 v153, v154, v154
	ds_bpermute_b32 v154, v77, v84
	v_max_f32_e32 v64, v64, v153
	s_waitcnt lgkmcnt(1)
	v_max_f32_e32 v153, v155, v155
	ds_bpermute_b32 v155, v77, v85
	v_max_f32_e32 v83, v83, v153
	s_waitcnt lgkmcnt(1)
	v_max_f32_e32 v153, v154, v154
	ds_bpermute_b32 v154, v77, v86
	v_max_f32_e32 v84, v84, v153
	s_waitcnt lgkmcnt(1)
	v_max_f32_e32 v153, v155, v155
	ds_bpermute_b32 v155, v77, v93
	v_max_f32_e32 v85, v85, v153
	s_waitcnt lgkmcnt(1)
	v_max_f32_e32 v153, v154, v154
	ds_bpermute_b32 v154, v77, v99
	v_max_f32_e32 v86, v86, v153
	s_waitcnt lgkmcnt(1)
	v_max_f32_e32 v153, v155, v155
	ds_bpermute_b32 v155, v77, v5
	v_max_f32_e32 v93, v93, v153
	s_waitcnt lgkmcnt(1)
	v_max_f32_e32 v153, v154, v154
	ds_bpermute_b32 v154, v78, v64
	v_max_f32_e32 v99, v99, v153
	s_waitcnt lgkmcnt(1)
	v_max_f32_e32 v153, v155, v155
	ds_bpermute_b32 v155, v78, v83
	v_max_f32_e32 v5, v5, v153
	s_waitcnt lgkmcnt(1)
	v_max_f32_e32 v153, v154, v154
	ds_bpermute_b32 v154, v78, v84
	v_max_f32_e32 v64, v64, v153
	s_waitcnt lgkmcnt(1)
	v_max_f32_e32 v153, v155, v155
	ds_bpermute_b32 v155, v78, v85
	v_max_f32_e32 v83, v83, v153
	s_waitcnt lgkmcnt(1)
	v_max_f32_e32 v153, v154, v154
	ds_bpermute_b32 v154, v78, v86
	v_max_f32_e32 v84, v84, v153
	s_waitcnt lgkmcnt(1)
	v_max_f32_e32 v153, v155, v155
	ds_bpermute_b32 v155, v78, v93
	v_max_f32_e32 v85, v85, v153
	s_waitcnt lgkmcnt(1)
	v_max_f32_e32 v153, v154, v154
	ds_bpermute_b32 v154, v78, v99
	v_max_f32_e32 v86, v86, v153
	s_waitcnt lgkmcnt(1)
	v_max_f32_e32 v153, v155, v155
	ds_bpermute_b32 v155, v78, v5
	v_max_f32_e32 v93, v93, v153
	s_waitcnt lgkmcnt(1)
	v_max_f32_e32 v153, v154, v154
	ds_bpermute_b32 v154, v79, v64
	v_max_f32_e32 v99, v99, v153
	s_waitcnt lgkmcnt(1)
	v_max_f32_e32 v153, v155, v155
	ds_bpermute_b32 v155, v79, v83
	v_max_f32_e32 v153, v5, v153
	s_waitcnt lgkmcnt(1)
	v_max_f32_e32 v5, v154, v154
	ds_bpermute_b32 v154, v79, v84
	v_max_f32_e32 v5, v64, v5
	s_waitcnt lgkmcnt(1)
	v_max_f32_e32 v64, v155, v155
	ds_bpermute_b32 v155, v79, v85
	v_max_f32_e32 v64, v83, v64
	s_waitcnt lgkmcnt(1)
	v_max_f32_e32 v83, v154, v154
	ds_bpermute_b32 v154, v79, v86
	v_max_f32_e32 v83, v84, v83
	s_waitcnt lgkmcnt(1)
	v_max_f32_e32 v84, v155, v155
	ds_bpermute_b32 v155, v79, v93
	ds_bpermute_b32 v156, v79, v99
	v_max_f32_e32 v84, v85, v84
	s_waitcnt lgkmcnt(2)
	v_max_f32_e32 v85, v154, v154
	ds_bpermute_b32 v154, v79, v153
	v_max_f32_e32 v85, v86, v85
	s_waitcnt lgkmcnt(2)
	v_max_f32_e32 v86, v155, v155
	v_div_scale_f32 v155, s[24:25], v5, v5, s67
	v_max_f32_e32 v86, v93, v86
	s_waitcnt lgkmcnt(1)
	v_max_f32_e32 v93, v156, v156
	v_rcp_f32_e32 v156, v155
	v_max_f32_e32 v93, v99, v93
	s_waitcnt lgkmcnt(0)
; __device__ __forceinline__ void st16_wt(void* p, u32x4 v) { asm volatile("global_store_dwordx4 %0, %1, off sc1\n\ts_nop 1" :: "v"(p), "v"(v) : "memory"); }
; __device__ __forceinline__ void quant_rows(unsigned char* ws, size_t xq_off, size_t sar_off, int gw, int NGW, int lane) {
;     ...
; #pragma unroll
;         for (int q = 0; q < 8; ++q) { const int row = m + q * NGW;
;             const float inv = mx[q] > 0.f ? 127.0f / mx[q] : 0.f, step = mx[q] > 0.f ? mx[q] * (1.0f / 127.0f) : 1.0f;
;             if (lane == 4 * q) mysar = rsqrtf(ssv * (1.0f / D) + EPS) * step;
;             u32x4 o4;
; #pragma unroll
;             for (int w4 = 0; w4 < 4; ++w4) { const unsigned w0 = a[q][w4 >> 1][2 * (w4 & 1)], w1 = a[q][w4 >> 1][2 * (w4 & 1) + 1];
;                 const int q0 = (int)__builtin_rintf(__uint_as_float(w0 << 16) * inv), q1 = (int)__builtin_rintf(__uint_as_float(w0 & 0xFFFF0000u) * inv);
;                 const int q2 = (int)__builtin_rintf(__uint_as_float(w1 << 16) * inv), q3 = (int)__builtin_rintf(__uint_as_float(w1 & 0xFFFF0000u) * inv);
;                 o4[w4] = ((unsigned)q0 & 0xFFu) | (((unsigned)q1 & 0xFFu) << 8) | (((unsigned)q2 & 0xFFu) << 16) | (((unsigned)q3 & 0xFFu) << 24); }
;             st16_wt(xq + (size_t)row * D + 16 * lane, o4);
	v_max_f32_e32 v99, v154, v154
	v_max_f32_e32 v99, v153, v99
	v_fma_f32 v153, -v155, v156, 1.0
	v_fmac_f32_e32 v156, v153, v156
	v_div_scale_f32 v153, vcc, s67, v5, s67
	v_mul_f32_e32 v154, v153, v156
	v_fma_f32 v157, -v155, v154, v153
	v_fmac_f32_e32 v154, v157, v156
	v_fma_f32 v153, -v155, v154, v153
	v_div_fmas_f32 v153, v153, v156, v154
	v_div_fixup_f32 v153, v153, v5, s67
	v_cmp_lt_f32_e64 s[24:25], 0, v5
	s_lshl_b64 s[26:27], s[26:27], 10
	s_lshl_b64 s[30:31], s[30:31], 10
	v_cndmask_b32_e64 v153, 0, v153, s[24:25]
	v_mul_f32_e32 v138, v153, v138
	v_mul_f32_e32 v140, v153, v140
	v_rndne_f32_e32 v138, v138
	v_mul_f32_e32 v139, v153, v139
	v_mul_f32_e32 v137, v153, v137
	v_rndne_f32_e32 v140, v140
	v_cvt_i32_f32_e32 v138, v138
	v_rndne_f32_e32 v139, v139
	v_rndne_f32_e32 v137, v137
	v_cvt_i32_f32_e32 v140, v140
	v_cvt_i32_f32_sdwa v139, v139 dst_sel:WORD_1 dst_unused:UNUSED_PAD src0_sel:DWORD
	v_cvt_i32_f32_e32 v137, v137
	v_mul_f32_e32 v149, v153, v149
	v_mul_f32_e32 v146, v153, v146
	v_mul_f32_e32 v142, v153, v142
	v_mul_f32_e32 v151, v153, v151
	v_rndne_f32_e32 v149, v149
	v_mul_f32_e32 v152, v153, v152
	v_mul_f32_e32 v150, v153, v150
	v_mul_f32_e32 v148, v153, v148
	v_rndne_f32_e32 v146, v146
	v_mul_f32_e32 v147, v153, v147
	v_mul_f32_e32 v145, v153, v145
	v_mul_f32_e32 v144, v153, v144
	v_rndne_f32_e32 v142, v142
	v_mul_f32_e32 v143, v153, v143
	v_mul_f32_e32 v141, v153, v141
	v_lshlrev_b32_e32 v138, 8, v138
	v_rndne_f32_e32 v151, v151
	v_cvt_i32_f32_e32 v149, v149
	v_rndne_f32_e32 v152, v152
	v_rndne_f32_e32 v150, v150
	v_rndne_f32_e32 v148, v148
	v_cvt_i32_f32_e32 v146, v146
	v_rndne_f32_e32 v147, v147
	v_rndne_f32_e32 v145, v145
	v_rndne_f32_e32 v144, v144
	v_cvt_i32_f32_e32 v142, v142
	v_rndne_f32_e32 v143, v143
	v_rndne_f32_e32 v141, v141
	v_and_b32_e32 v138, 0xff00, v138
	v_and_b32_e32 v139, 0xff0000, v139
	v_perm_b32 v137, v137, v140, s68
	v_cvt_i32_f32_e32 v151, v151
	v_cvt_i32_f32_sdwa v152, v152 dst_sel:WORD_1 dst_unused:UNUSED_PAD src0_sel:DWORD
	v_cvt_i32_f32_e32 v150, v150
	v_cvt_i32_f32_e32 v148, v148
	v_cvt_i32_f32_sdwa v147, v147 dst_sel:WORD_1 dst_unused:UNUSED_PAD src0_sel:DWORD
	v_cvt_i32_f32_e32 v145, v145
	v_cvt_i32_f32_e32 v144, v144
	v_cvt_i32_f32_sdwa v143, v143 dst_sel:WORD_1 dst_unused:UNUSED_PAD src0_sel:DWORD
	v_cvt_i32_f32_e32 v141, v141
	v_or3_b32 v153, v137, v138, v139
	v_div_scale_f32 v137, s[28:29], v64, v64, s67
	v_rcp_f32_e32 v140, v137
	v_lshlrev_b32_e32 v149, 8, v149
	v_lshlrev_b32_e32 v146, 8, v146
	v_lshlrev_b32_e32 v142, 8, v142
	v_and_b32_e32 v149, 0xff00, v149
	v_and_b32_e32 v152, 0xff0000, v152
	v_perm_b32 v150, v150, v151, s68
	v_and_b32_e32 v146, 0xff00, v146
	v_and_b32_e32 v147, 0xff0000, v147
	v_perm_b32 v145, v145, v148, s68
	v_and_b32_e32 v142, 0xff00, v142
	v_and_b32_e32 v143, 0xff0000, v143
	v_perm_b32 v141, v141, v144, s68
	v_lshl_add_u64 v[138:139], v[70:71], 0, s[26:27]
	v_or3_b32 v150, v150, v149, v152
	v_or3_b32 v151, v145, v146, v147
	v_or3_b32 v152, v141, v142, v143
	global_store_dwordx4 v[138:139], v[150:153], off sc1
	s_nop 1
	v_fma_f32 v138, -v137, v140, 1.0
	v_fmac_f32_e32 v140, v138, v140
	v_div_scale_f32 v138, vcc, s67, v64, s67
	v_mul_f32_e32 v139, v138, v140
	v_fma_f32 v141, -v137, v139, v138
	v_fmac_f32_e32 v139, v141, v140
	v_fma_f32 v137, -v137, v139, v138
	v_div_fmas_f32 v137, v137, v140, v139
	v_div_fixup_f32 v137, v137, v64, s67
	v_cmp_lt_f32_e64 s[26:27], 0, v64
	s_lshl_b64 s[34:35], s[34:35], 10
	s_lshl_b64 s[36:37], s[36:37], 10
	v_cndmask_b32_e64 v137, 0, v137, s[26:27]
	v_mul_f32_e32 v122, v137, v122
	v_mul_f32_e32 v124, v137, v124
	v_rndne_f32_e32 v122, v122
	v_mul_f32_e32 v123, v137, v123
	v_mul_f32_e32 v121, v137, v121
	v_rndne_f32_e32 v124, v124
	v_cvt_i32_f32_e32 v122, v122
	v_rndne_f32_e32 v123, v123
	v_rndne_f32_e32 v121, v121
	v_cvt_i32_f32_e32 v124, v124
	v_cvt_i32_f32_sdwa v123, v123 dst_sel:WORD_1 dst_unused:UNUSED_PAD src0_sel:DWORD
	v_cvt_i32_f32_e32 v121, v121
	v_mul_f32_e32 v134, v137, v134
	v_mul_f32_e32 v130, v137, v130
	v_mul_f32_e32 v126, v137, v126
	v_mul_f32_e32 v136, v137, v136
	v_rndne_f32_e32 v134, v134
	v_mul_f32_e32 v135, v137, v135
	v_mul_f32_e32 v133, v137, v133
	v_mul_f32_e32 v132, v137, v132
	v_rndne_f32_e32 v130, v130
	v_mul_f32_e32 v131, v137, v131
	v_mul_f32_e32 v129, v137, v129
	v_mul_f32_e32 v128, v137, v128
	v_rndne_f32_e32 v126, v126
	v_mul_f32_e32 v127, v137, v127
	v_mul_f32_e32 v125, v137, v125
	v_lshlrev_b32_e32 v122, 8, v122
	v_rndne_f32_e32 v136, v136
	v_cvt_i32_f32_e32 v134, v134
	v_rndne_f32_e32 v135, v135
	v_rndne_f32_e32 v133, v133
	v_rndne_f32_e32 v132, v132
	v_cvt_i32_f32_e32 v130, v130
	v_rndne_f32_e32 v131, v131
	v_rndne_f32_e32 v129, v129
	v_rndne_f32_e32 v128, v128
	v_cvt_i32_f32_e32 v126, v126
	v_rndne_f32_e32 v127, v127
	v_rndne_f32_e32 v125, v125
	v_and_b32_e32 v122, 0xff00, v122
	v_and_b32_e32 v123, 0xff0000, v123
	v_perm_b32 v121, v121, v124, s68
	v_cvt_i32_f32_e32 v136, v136
	v_cvt_i32_f32_sdwa v135, v135 dst_sel:WORD_1 dst_unused:UNUSED_PAD src0_sel:DWORD
	v_cvt_i32_f32_e32 v133, v133
	v_cvt_i32_f32_e32 v132, v132
	v_cvt_i32_f32_sdwa v131, v131 dst_sel:WORD_1 dst_unused:UNUSED_PAD src0_sel:DWORD
	v_cvt_i32_f32_e32 v129, v129
	v_cvt_i32_f32_e32 v128, v128
	v_cvt_i32_f32_sdwa v127, v127 dst_sel:WORD_1 dst_unused:UNUSED_PAD src0_sel:DWORD
	v_cvt_i32_f32_e32 v125, v125
	v_or3_b32 v137, v121, v122, v123
	v_div_scale_f32 v121, s[28:29], v83, v83, s67
	v_rcp_f32_e32 v124, v121
	v_lshlrev_b32_e32 v134, 8, v134
	v_lshlrev_b32_e32 v130, 8, v130
	v_lshlrev_b32_e32 v126, 8, v126
	s_lshl_b64 s[28:29], s[44:45], 10
	v_and_b32_e32 v134, 0xff00, v134
	v_and_b32_e32 v135, 0xff0000, v135
	v_perm_b32 v133, v133, v136, s68
; __device__ __forceinline__ void st16_wt(void* p, u32x4 v) { asm volatile("global_store_dwordx4 %0, %1, off sc1\n\ts_nop 1" :: "v"(p), "v"(v) : "memory"); }
; __device__ __forceinline__ void quant_rows(unsigned char* ws, size_t xq_off, size_t sar_off, int gw, int NGW, int lane) {
;     ...
; #pragma unroll
;         for (int q = 0; q < 8; ++q) { const int row = m + q * NGW;
;             const float inv = mx[q] > 0.f ? 127.0f / mx[q] : 0.f, step = mx[q] > 0.f ? mx[q] * (1.0f / 127.0f) : 1.0f;
;             if (lane == 4 * q) mysar = rsqrtf(ssv * (1.0f / D) + EPS) * step;
;             u32x4 o4;
; #pragma unroll
;             for (int w4 = 0; w4 < 4; ++w4) { const unsigned w0 = a[q][w4 >> 1][2 * (w4 & 1)], w1 = a[q][w4 >> 1][2 * (w4 & 1) + 1];
;                 const int q0 = (int)__builtin_rintf(__uint_as_float(w0 << 16) * inv), q1 = (int)__builtin_rintf(__uint_as_float(w0 & 0xFFFF0000u) * inv);
;                 const int q2 = (int)__builtin_rintf(__uint_as_float(w1 << 16) * inv), q3 = (int)__builtin_rintf(__uint_as_float(w1 & 0xFFFF0000u) * inv);
;                 o4[w4] = ((unsigned)q0 & 0xFFu) | (((unsigned)q1 & 0xFFu) << 8) | (((unsigned)q2 & 0xFFu) << 16) | (((unsigned)q3 & 0xFFu) << 24); }
;             st16_wt(xq + (size_t)row * D + 16 * lane, o4);
;         }
	v_and_b32_e32 v130, 0xff00, v130
	v_and_b32_e32 v131, 0xff0000, v131
	v_perm_b32 v129, v129, v132, s68
	v_and_b32_e32 v126, 0xff00, v126
	v_and_b32_e32 v127, 0xff0000, v127
	v_perm_b32 v125, v125, v128, s68
	v_lshl_add_u64 v[122:123], v[70:71], 0, s[28:29]
	v_or3_b32 v134, v133, v134, v135
	v_or3_b32 v135, v129, v130, v131
	v_or3_b32 v136, v125, v126, v127
	global_store_dwordx4 v[122:123], v[134:137], off sc1
	s_nop 1
	v_fma_f32 v122, -v121, v124, 1.0
	v_fmac_f32_e32 v124, v122, v124
	v_div_scale_f32 v122, vcc, s67, v83, s67
	v_mul_f32_e32 v123, v122, v124
	v_fma_f32 v125, -v121, v123, v122
	v_fmac_f32_e32 v123, v125, v124
	v_fma_f32 v121, -v121, v123, v122
	v_div_fmas_f32 v121, v121, v124, v123
	v_div_fixup_f32 v121, v121, v83, s67
	v_cmp_lt_f32_e64 s[28:29], 0, v83
	s_lshl_b64 s[38:39], s[38:39], 10
	s_lshl_b64 s[46:47], s[46:47], 10
	v_cndmask_b32_e64 v121, 0, v121, s[28:29]
	v_mul_f32_e32 v106, v121, v106
	v_mul_f32_e32 v108, v121, v108
	v_rndne_f32_e32 v106, v106
	v_mul_f32_e32 v107, v121, v107
	v_mul_f32_e32 v105, v121, v105
	v_rndne_f32_e32 v108, v108
	v_cvt_i32_f32_e32 v106, v106
	v_rndne_f32_e32 v107, v107
	v_rndne_f32_e32 v105, v105
	v_cvt_i32_f32_e32 v108, v108
	v_cvt_i32_f32_sdwa v107, v107 dst_sel:WORD_1 dst_unused:UNUSED_PAD src0_sel:DWORD
	v_cvt_i32_f32_e32 v105, v105
	v_mul_f32_e32 v118, v121, v118
	v_mul_f32_e32 v114, v121, v114
	v_mul_f32_e32 v110, v121, v110
	v_mul_f32_e32 v120, v121, v120
	v_rndne_f32_e32 v118, v118
	v_mul_f32_e32 v119, v121, v119
	v_mul_f32_e32 v117, v121, v117
	v_mul_f32_e32 v116, v121, v116
	v_rndne_f32_e32 v114, v114
	v_mul_f32_e32 v115, v121, v115
	v_mul_f32_e32 v113, v121, v113
	v_mul_f32_e32 v112, v121, v112
	v_rndne_f32_e32 v110, v110
	v_mul_f32_e32 v111, v121, v111
	v_mul_f32_e32 v109, v121, v109
	v_lshlrev_b32_e32 v106, 8, v106
	v_rndne_f32_e32 v120, v120
	v_cvt_i32_f32_e32 v118, v118
	v_rndne_f32_e32 v119, v119
	v_rndne_f32_e32 v117, v117
	v_rndne_f32_e32 v116, v116
	v_cvt_i32_f32_e32 v114, v114
	v_rndne_f32_e32 v115, v115
	v_rndne_f32_e32 v113, v113
	v_rndne_f32_e32 v112, v112
	v_cvt_i32_f32_e32 v110, v110
	v_rndne_f32_e32 v111, v111
	v_rndne_f32_e32 v109, v109
	v_and_b32_e32 v106, 0xff00, v106
	v_and_b32_e32 v107, 0xff0000, v107
	v_perm_b32 v105, v105, v108, s68
	v_cvt_i32_f32_e32 v120, v120
	v_cvt_i32_f32_sdwa v119, v119 dst_sel:WORD_1 dst_unused:UNUSED_PAD src0_sel:DWORD
	v_cvt_i32_f32_e32 v117, v117
	v_cvt_i32_f32_e32 v116, v116
	v_cvt_i32_f32_sdwa v115, v115 dst_sel:WORD_1 dst_unused:UNUSED_PAD src0_sel:DWORD
	v_cvt_i32_f32_e32 v113, v113
	v_cvt_i32_f32_e32 v112, v112
	v_cvt_i32_f32_sdwa v111, v111 dst_sel:WORD_1 dst_unused:UNUSED_PAD src0_sel:DWORD
	v_cvt_i32_f32_e32 v109, v109
	v_or3_b32 v121, v105, v106, v107
	v_div_scale_f32 v105, s[48:49], v84, v84, s67
	v_rcp_f32_e32 v108, v105
	v_lshlrev_b32_e32 v118, 8, v118
	v_lshlrev_b32_e32 v114, 8, v114
	v_lshlrev_b32_e32 v110, 8, v110
	v_and_b32_e32 v118, 0xff00, v118
	v_and_b32_e32 v119, 0xff0000, v119
	v_perm_b32 v117, v117, v120, s68
	v_and_b32_e32 v114, 0xff00, v114
	v_and_b32_e32 v115, 0xff0000, v115
	v_perm_b32 v113, v113, v116, s68
	v_and_b32_e32 v110, 0xff00, v110
	v_and_b32_e32 v111, 0xff0000, v111
	v_perm_b32 v109, v109, v112, s68
	v_lshl_add_u64 v[106:107], v[70:71], 0, s[30:31]
	v_or3_b32 v118, v117, v118, v119
	v_or3_b32 v119, v113, v114, v115
	v_or3_b32 v120, v109, v110, v111
	global_store_dwordx4 v[106:107], v[118:121], off sc1
	s_nop 1
	v_fma_f32 v106, -v105, v108, 1.0
	v_fmac_f32_e32 v108, v106, v108
	v_div_scale_f32 v106, vcc, s67, v84, s67
	v_mul_f32_e32 v107, v106, v108
	v_fma_f32 v109, -v105, v107, v106
	v_fmac_f32_e32 v107, v109, v108
	v_fma_f32 v105, -v105, v107, v106
	v_div_fmas_f32 v105, v105, v108, v107
	v_div_fixup_f32 v105, v105, v84, s67
	v_cmp_lt_f32_e64 s[30:31], 0, v84
	ds_bpermute_b32 v73, v76, v62
	s_lshl_b64 s[40:41], s[40:41], 10
	v_cndmask_b32_e64 v105, 0, v105, s[30:31]
	v_mul_f32_e32 v88, v105, v88
	v_mul_f32_e32 v90, v105, v90
	v_rndne_f32_e32 v88, v88
	v_mul_f32_e32 v89, v105, v89
	v_mul_f32_e32 v87, v105, v87
	v_rndne_f32_e32 v90, v90
	v_cvt_i32_f32_e32 v88, v88
	v_rndne_f32_e32 v89, v89
	v_rndne_f32_e32 v87, v87
	v_cvt_i32_f32_e32 v90, v90
	v_cvt_i32_f32_sdwa v89, v89 dst_sel:WORD_1 dst_unused:UNUSED_PAD src0_sel:DWORD
	v_cvt_i32_f32_e32 v87, v87
	v_mul_f32_e32 v102, v105, v102
	v_mul_f32_e32 v97, v105, v97
	v_mul_f32_e32 v92, v105, v92
	v_mul_f32_e32 v104, v105, v104
	v_rndne_f32_e32 v102, v102
	v_mul_f32_e32 v103, v105, v103
	v_mul_f32_e32 v101, v105, v101
	v_mul_f32_e32 v100, v105, v100
	v_rndne_f32_e32 v97, v97
	v_mul_f32_e32 v98, v105, v98
	v_mul_f32_e32 v96, v105, v96
	v_mul_f32_e32 v95, v105, v95
	v_rndne_f32_e32 v92, v92
	v_mul_f32_e32 v94, v105, v94
	v_mul_f32_e32 v91, v105, v91
	v_lshlrev_b32_e32 v88, 8, v88
	v_rndne_f32_e32 v104, v104
	v_cvt_i32_f32_e32 v102, v102
	v_rndne_f32_e32 v103, v103
	v_rndne_f32_e32 v101, v101
	v_rndne_f32_e32 v100, v100
	v_cvt_i32_f32_e32 v97, v97
	v_rndne_f32_e32 v98, v98
	v_rndne_f32_e32 v96, v96
	v_rndne_f32_e32 v95, v95
	v_cvt_i32_f32_e32 v92, v92
	v_rndne_f32_e32 v94, v94
	v_rndne_f32_e32 v91, v91
	v_and_b32_e32 v88, 0xff00, v88
	v_and_b32_e32 v89, 0xff0000, v89
	v_perm_b32 v87, v87, v90, s68
	v_cvt_i32_f32_e32 v104, v104
	v_cvt_i32_f32_sdwa v103, v103 dst_sel:WORD_1 dst_unused:UNUSED_PAD src0_sel:DWORD
	v_cvt_i32_f32_e32 v101, v101
	v_cvt_i32_f32_e32 v100, v100
	v_cvt_i32_f32_sdwa v98, v98 dst_sel:WORD_1 dst_unused:UNUSED_PAD src0_sel:DWORD
	v_cvt_i32_f32_e32 v96, v96
	v_cvt_i32_f32_e32 v95, v95
	v_cvt_i32_f32_sdwa v94, v94 dst_sel:WORD_1 dst_unused:UNUSED_PAD src0_sel:DWORD
	v_cvt_i32_f32_e32 v91, v91
	v_or3_b32 v105, v87, v88, v89
; __device__ __forceinline__ void st16_wt(void* p, u32x4 v) { asm volatile("global_store_dwordx4 %0, %1, off sc1\n\ts_nop 1" :: "v"(p), "v"(v) : "memory"); }
; __device__ __forceinline__ void quant_rows(unsigned char* ws, size_t xq_off, size_t sar_off, int gw, int NGW, int lane) {
;     ...
; #pragma unroll
;         for (int q = 0; q < 8; ++q) { const int row = m + q * NGW;
;             const float inv = mx[q] > 0.f ? 127.0f / mx[q] : 0.f, step = mx[q] > 0.f ? mx[q] * (1.0f / 127.0f) : 1.0f;
;             if (lane == 4 * q) mysar = rsqrtf(ssv * (1.0f / D) + EPS) * step;
;             u32x4 o4;
; #pragma unroll
;             for (int w4 = 0; w4 < 4; ++w4) { const unsigned w0 = a[q][w4 >> 1][2 * (w4 & 1)], w1 = a[q][w4 >> 1][2 * (w4 & 1) + 1];
;                 const int q0 = (int)__builtin_rintf(__uint_as_float(w0 << 16) * inv), q1 = (int)__builtin_rintf(__uint_as_float(w0 & 0xFFFF0000u) * inv);
;                 const int q2 = (int)__builtin_rintf(__uint_as_float(w1 << 16) * inv), q3 = (int)__builtin_rintf(__uint_as_float(w1 & 0xFFFF0000u) * inv);
;                 o4[w4] = ((unsigned)q0 & 0xFFu) | (((unsigned)q1 & 0xFFu) << 8) | (((unsigned)q2 & 0xFFu) << 16) | (((unsigned)q3 & 0xFFu) << 24); }
;             st16_wt(xq + (size_t)row * D + 16 * lane, o4);
;         }
	v_div_scale_f32 v87, s[48:49], v85, v85, s67
	v_rcp_f32_e32 v90, v87
	v_lshlrev_b32_e32 v102, 8, v102
	v_lshlrev_b32_e32 v97, 8, v97
	v_lshlrev_b32_e32 v92, 8, v92
	v_and_b32_e32 v102, 0xff00, v102
	v_and_b32_e32 v103, 0xff0000, v103
	v_perm_b32 v101, v101, v104, s68
	v_and_b32_e32 v97, 0xff00, v97
	v_and_b32_e32 v98, 0xff0000, v98
	v_perm_b32 v96, v96, v100, s68
	v_and_b32_e32 v92, 0xff00, v92
	v_and_b32_e32 v94, 0xff0000, v94
	v_perm_b32 v91, v91, v95, s68
	v_lshl_add_u64 v[88:89], v[70:71], 0, s[34:35]
	v_or3_b32 v102, v101, v102, v103
	v_or3_b32 v103, v96, v97, v98
	v_or3_b32 v104, v91, v92, v94
	global_store_dwordx4 v[88:89], v[102:105], off sc1
	s_nop 1
	v_fma_f32 v88, -v87, v90, 1.0
	v_fmac_f32_e32 v90, v88, v90
	v_div_scale_f32 v88, vcc, s67, v85, s67
	v_mul_f32_e32 v89, v88, v90
	v_fma_f32 v91, -v87, v89, v88
	v_fmac_f32_e32 v89, v91, v90
	v_fma_f32 v87, -v87, v89, v88
	v_div_fmas_f32 v87, v87, v90, v89
	v_div_fixup_f32 v87, v87, v85, s67
	v_cmp_lt_f32_e64 s[34:35], 0, v85
	s_nop 1
	v_cndmask_b32_e64 v87, 0, v87, s[34:35]
	v_mul_f32_e32 v52, v87, v52
	v_mul_f32_e32 v54, v87, v54
	v_rndne_f32_e32 v52, v52
	v_mul_f32_e32 v53, v87, v53
	v_mul_f32_e32 v51, v87, v51
	v_rndne_f32_e32 v54, v54
	v_cvt_i32_f32_e32 v52, v52
	v_rndne_f32_e32 v53, v53
	v_rndne_f32_e32 v51, v51
	v_cvt_i32_f32_e32 v54, v54
	v_cvt_i32_f32_sdwa v53, v53 dst_sel:WORD_1 dst_unused:UNUSED_PAD src0_sel:DWORD
	v_cvt_i32_f32_e32 v51, v51
	v_mul_f32_e32 v80, v87, v80
	v_mul_f32_e32 v60, v87, v60
	v_mul_f32_e32 v56, v87, v56
	v_mul_f32_e32 v82, v87, v82
	v_rndne_f32_e32 v80, v80
	v_mul_f32_e32 v81, v87, v81
	v_mul_f32_e32 v65, v87, v65
	v_mul_f32_e32 v63, v87, v63
	v_rndne_f32_e32 v60, v60
	v_mul_f32_e32 v61, v87, v61
	v_mul_f32_e32 v59, v87, v59
	v_mul_f32_e32 v58, v87, v58
	v_rndne_f32_e32 v56, v56
	v_mul_f32_e32 v57, v87, v57
	v_mul_f32_e32 v55, v87, v55
	v_lshlrev_b32_e32 v52, 8, v52
	v_rndne_f32_e32 v82, v82
	v_cvt_i32_f32_e32 v80, v80
	v_rndne_f32_e32 v81, v81
	v_rndne_f32_e32 v65, v65
	v_rndne_f32_e32 v63, v63
	v_cvt_i32_f32_e32 v60, v60
	v_rndne_f32_e32 v61, v61
	v_rndne_f32_e32 v59, v59
	v_rndne_f32_e32 v58, v58
	v_cvt_i32_f32_e32 v56, v56
	v_rndne_f32_e32 v57, v57
	v_rndne_f32_e32 v55, v55
	v_and_b32_e32 v52, 0xff00, v52
	v_and_b32_e32 v53, 0xff0000, v53
	v_perm_b32 v51, v51, v54, s68
	v_cvt_i32_f32_e32 v82, v82
	v_cvt_i32_f32_sdwa v81, v81 dst_sel:WORD_1 dst_unused:UNUSED_PAD src0_sel:DWORD
	v_cvt_i32_f32_e32 v65, v65
	v_cvt_i32_f32_e32 v63, v63
	v_cvt_i32_f32_sdwa v61, v61 dst_sel:WORD_1 dst_unused:UNUSED_PAD src0_sel:DWORD
	v_cvt_i32_f32_e32 v59, v59
	v_cvt_i32_f32_e32 v58, v58
	v_cvt_i32_f32_sdwa v57, v57 dst_sel:WORD_1 dst_unused:UNUSED_PAD src0_sel:DWORD
	v_cvt_i32_f32_e32 v55, v55
	v_or3_b32 v91, v51, v52, v53
	v_div_scale_f32 v51, s[48:49], v86, v86, s67
	v_rcp_f32_e32 v54, v51
	v_lshlrev_b32_e32 v80, 8, v80
	v_lshlrev_b32_e32 v60, 8, v60
	v_lshlrev_b32_e32 v56, 8, v56
	v_and_b32_e32 v80, 0xff00, v80
	v_and_b32_e32 v81, 0xff0000, v81
	v_perm_b32 v65, v65, v82, s68
	v_and_b32_e32 v60, 0xff00, v60
	v_and_b32_e32 v61, 0xff0000, v61
	v_perm_b32 v59, v59, v63, s68
	v_and_b32_e32 v56, 0xff00, v56
	v_and_b32_e32 v57, 0xff0000, v57
	v_perm_b32 v55, v55, v58, s68
	v_lshl_add_u64 v[52:53], v[70:71], 0, s[36:37]
	v_or3_b32 v88, v65, v80, v81
	v_or3_b32 v89, v59, v60, v61
	v_or3_b32 v90, v55, v56, v57
	global_store_dwordx4 v[52:53], v[88:91], off sc1
	s_nop 1
	v_fma_f32 v52, -v51, v54, 1.0
	v_fmac_f32_e32 v54, v52, v54
	v_div_scale_f32 v52, vcc, s67, v86, s67
	v_mul_f32_e32 v53, v52, v54
	v_fma_f32 v55, -v51, v53, v52
	v_fmac_f32_e32 v53, v55, v54
	v_fma_f32 v51, -v51, v53, v52
	v_div_fmas_f32 v51, v51, v54, v53
	v_div_fixup_f32 v51, v51, v86, s67
	v_cmp_lt_f32_e64 s[36:37], 0, v86
	s_nop 1
	v_cndmask_b32_e64 v51, 0, v51, s[36:37]
	v_mul_f32_e32 v36, v51, v36
	v_mul_f32_e32 v38, v51, v38
	v_rndne_f32_e32 v36, v36
	v_mul_f32_e32 v37, v51, v37
	v_mul_f32_e32 v35, v51, v35
	v_rndne_f32_e32 v38, v38
	v_cvt_i32_f32_e32 v36, v36
	v_rndne_f32_e32 v37, v37
	v_rndne_f32_e32 v35, v35
	v_cvt_i32_f32_e32 v38, v38
	v_cvt_i32_f32_sdwa v37, v37 dst_sel:WORD_1 dst_unused:UNUSED_PAD src0_sel:DWORD
	v_cvt_i32_f32_e32 v35, v35
	v_mul_f32_e32 v48, v51, v48
	v_mul_f32_e32 v44, v51, v44
	v_mul_f32_e32 v40, v51, v40
	v_mul_f32_e32 v50, v51, v50
	v_rndne_f32_e32 v48, v48
	v_mul_f32_e32 v49, v51, v49
	v_mul_f32_e32 v47, v51, v47
	v_mul_f32_e32 v46, v51, v46
	v_rndne_f32_e32 v44, v44
	v_mul_f32_e32 v45, v51, v45
	v_mul_f32_e32 v43, v51, v43
	v_mul_f32_e32 v42, v51, v42
	v_rndne_f32_e32 v40, v40
	v_mul_f32_e32 v41, v51, v41
	v_mul_f32_e32 v39, v51, v39
	v_lshlrev_b32_e32 v36, 8, v36
	v_rndne_f32_e32 v50, v50
	v_cvt_i32_f32_e32 v48, v48
	v_rndne_f32_e32 v49, v49
	v_rndne_f32_e32 v47, v47
	v_rndne_f32_e32 v46, v46
	v_cvt_i32_f32_e32 v44, v44
	v_rndne_f32_e32 v45, v45
	v_rndne_f32_e32 v43, v43
	v_rndne_f32_e32 v42, v42
	v_cvt_i32_f32_e32 v40, v40
	v_rndne_f32_e32 v41, v41
	v_rndne_f32_e32 v39, v39
	v_and_b32_e32 v36, 0xff00, v36
	v_and_b32_e32 v37, 0xff0000, v37
	v_perm_b32 v35, v35, v38, s68
	v_cvt_i32_f32_e32 v50, v50
	v_cvt_i32_f32_sdwa v49, v49 dst_sel:WORD_1 dst_unused:UNUSED_PAD src0_sel:DWORD
	v_cvt_i32_f32_e32 v47, v47
	v_cvt_i32_f32_e32 v46, v46
	v_cvt_i32_f32_sdwa v45, v45 dst_sel:WORD_1 dst_unused:UNUSED_PAD src0_sel:DWORD
	v_cvt_i32_f32_e32 v43, v43
	v_cvt_i32_f32_e32 v42, v42
	v_cvt_i32_f32_sdwa v41, v41 dst_sel:WORD_1 dst_unused:UNUSED_PAD src0_sel:DWORD
	v_cvt_i32_f32_e32 v39, v39
	v_or3_b32 v51, v35, v36, v37
	v_div_scale_f32 v35, s[48:49], v93, v93, s67
	v_rcp_f32_e32 v38, v35
	v_lshlrev_b32_e32 v48, 8, v48
	v_lshlrev_b32_e32 v44, 8, v44
	v_lshlrev_b32_e32 v40, 8, v40
; __device__ __forceinline__ void st16_wt(void* p, u32x4 v) { asm volatile("global_store_dwordx4 %0, %1, off sc1\n\ts_nop 1" :: "v"(p), "v"(v) : "memory"); }
; __device__ __forceinline__ void quant_rows(unsigned char* ws, size_t xq_off, size_t sar_off, int gw, int NGW, int lane) {
;     ...
; #pragma unroll
;         for (int q = 0; q < 8; ++q) { const int row = m + q * NGW;
;             const float inv = mx[q] > 0.f ? 127.0f / mx[q] : 0.f, step = mx[q] > 0.f ? mx[q] * (1.0f / 127.0f) : 1.0f;
;             if (lane == 4 * q) mysar = rsqrtf(ssv * (1.0f / D) + EPS) * step;
;             u32x4 o4;
; #pragma unroll
;             for (int w4 = 0; w4 < 4; ++w4) { const unsigned w0 = a[q][w4 >> 1][2 * (w4 & 1)], w1 = a[q][w4 >> 1][2 * (w4 & 1) + 1];
;                 const int q0 = (int)__builtin_rintf(__uint_as_float(w0 << 16) * inv), q1 = (int)__builtin_rintf(__uint_as_float(w0 & 0xFFFF0000u) * inv);
;                 const int q2 = (int)__builtin_rintf(__uint_as_float(w1 << 16) * inv), q3 = (int)__builtin_rintf(__uint_as_float(w1 & 0xFFFF0000u) * inv);
;                 o4[w4] = ((unsigned)q0 & 0xFFu) | (((unsigned)q1 & 0xFFu) << 8) | (((unsigned)q2 & 0xFFu) << 16) | (((unsigned)q3 & 0xFFu) << 24); }
;             st16_wt(xq + (size_t)row * D + 16 * lane, o4);
;         }
	v_and_b32_e32 v48, 0xff00, v48
	v_and_b32_e32 v49, 0xff0000, v49
	v_perm_b32 v47, v47, v50, s68
	v_and_b32_e32 v44, 0xff00, v44
	v_and_b32_e32 v45, 0xff0000, v45
	v_perm_b32 v43, v43, v46, s68
	v_and_b32_e32 v40, 0xff00, v40
	v_and_b32_e32 v41, 0xff0000, v41
	v_perm_b32 v39, v39, v42, s68
	v_lshl_add_u64 v[36:37], v[70:71], 0, s[38:39]
	v_or3_b32 v48, v47, v48, v49
	v_or3_b32 v49, v43, v44, v45
	v_or3_b32 v50, v39, v40, v41
	global_store_dwordx4 v[36:37], v[48:51], off sc1
	s_nop 1
	v_fma_f32 v36, -v35, v38, 1.0
	v_fmac_f32_e32 v38, v36, v38
	v_div_scale_f32 v36, vcc, s67, v93, s67
	v_mul_f32_e32 v37, v36, v38
	v_fma_f32 v39, -v35, v37, v36
	v_fmac_f32_e32 v37, v39, v38
	v_fma_f32 v35, -v35, v37, v36
	v_div_fmas_f32 v35, v35, v38, v37
	v_div_fixup_f32 v35, v35, v93, s67
	v_cmp_lt_f32_e64 s[38:39], 0, v93
	s_nop 1
	v_cndmask_b32_e64 v35, 0, v35, s[38:39]
	v_mul_f32_e32 v20, v35, v20
	v_mul_f32_e32 v22, v35, v22
	v_rndne_f32_e32 v20, v20
	v_mul_f32_e32 v21, v35, v21
	v_mul_f32_e32 v19, v35, v19
	v_rndne_f32_e32 v22, v22
	v_cvt_i32_f32_e32 v20, v20
	v_rndne_f32_e32 v21, v21
	v_rndne_f32_e32 v19, v19
	v_cvt_i32_f32_e32 v22, v22
	v_cvt_i32_f32_sdwa v21, v21 dst_sel:WORD_1 dst_unused:UNUSED_PAD src0_sel:DWORD
	v_cvt_i32_f32_e32 v19, v19
	v_mul_f32_e32 v32, v35, v32
	v_mul_f32_e32 v28, v35, v28
	v_mul_f32_e32 v24, v35, v24
	v_mul_f32_e32 v34, v35, v34
	v_rndne_f32_e32 v32, v32
	v_mul_f32_e32 v33, v35, v33
	v_mul_f32_e32 v31, v35, v31
	v_mul_f32_e32 v30, v35, v30
	v_rndne_f32_e32 v28, v28
	v_mul_f32_e32 v29, v35, v29
	v_mul_f32_e32 v27, v35, v27
	v_mul_f32_e32 v26, v35, v26
	v_rndne_f32_e32 v24, v24
	v_mul_f32_e32 v25, v35, v25
	v_mul_f32_e32 v23, v35, v23
	v_lshlrev_b32_e32 v20, 8, v20
	v_rndne_f32_e32 v34, v34
	v_cvt_i32_f32_e32 v32, v32
	v_rndne_f32_e32 v33, v33
	v_rndne_f32_e32 v31, v31
	v_rndne_f32_e32 v30, v30
	v_cvt_i32_f32_e32 v28, v28
	v_rndne_f32_e32 v29, v29
	v_rndne_f32_e32 v27, v27
	v_rndne_f32_e32 v26, v26
	v_cvt_i32_f32_e32 v24, v24
	v_rndne_f32_e32 v25, v25
	v_rndne_f32_e32 v23, v23
	v_and_b32_e32 v20, 0xff00, v20
	v_and_b32_e32 v21, 0xff0000, v21
	v_perm_b32 v19, v19, v22, s68
	v_cvt_i32_f32_e32 v34, v34
	v_cvt_i32_f32_sdwa v33, v33 dst_sel:WORD_1 dst_unused:UNUSED_PAD src0_sel:DWORD
	v_cvt_i32_f32_e32 v31, v31
	v_cvt_i32_f32_e32 v30, v30
	v_cvt_i32_f32_sdwa v29, v29 dst_sel:WORD_1 dst_unused:UNUSED_PAD src0_sel:DWORD
	v_cvt_i32_f32_e32 v27, v27
	v_cvt_i32_f32_e32 v26, v26
	v_cvt_i32_f32_sdwa v25, v25 dst_sel:WORD_1 dst_unused:UNUSED_PAD src0_sel:DWORD
	v_cvt_i32_f32_e32 v23, v23
	v_or3_b32 v35, v19, v20, v21
	v_div_scale_f32 v19, s[48:49], v99, v99, s67
	v_rcp_f32_e32 v22, v19
	v_lshlrev_b32_e32 v32, 8, v32
	v_lshlrev_b32_e32 v28, 8, v28
	v_lshlrev_b32_e32 v24, 8, v24
	v_and_b32_e32 v32, 0xff00, v32
	v_and_b32_e32 v33, 0xff0000, v33
	v_perm_b32 v31, v31, v34, s68
	v_and_b32_e32 v28, 0xff00, v28
	v_and_b32_e32 v29, 0xff0000, v29
	v_perm_b32 v27, v27, v30, s68
	v_and_b32_e32 v24, 0xff00, v24
	v_and_b32_e32 v25, 0xff0000, v25
	v_perm_b32 v23, v23, v26, s68
	v_lshl_add_u64 v[20:21], v[70:71], 0, s[46:47]
	v_or3_b32 v32, v31, v32, v33
	v_or3_b32 v33, v27, v28, v29
	v_or3_b32 v34, v23, v24, v25
	global_store_dwordx4 v[20:21], v[32:35], off sc1
	s_nop 1
	v_fma_f32 v20, -v19, v22, 1.0
	v_fmac_f32_e32 v22, v20, v22
	v_div_scale_f32 v20, vcc, s67, v99, s67
	v_mul_f32_e32 v21, v20, v22
	v_fma_f32 v23, -v19, v21, v20
	v_fmac_f32_e32 v21, v23, v22
	v_fma_f32 v19, -v19, v21, v20
	v_div_fmas_f32 v19, v19, v22, v21
	v_div_fixup_f32 v19, v19, v99, s67
	v_cmp_lt_f32_e32 vcc, 0, v99
	s_nop 1
	v_cndmask_b32_e32 v19, 0, v19, vcc
	v_mul_f32_e32 v16, v19, v16
	v_mul_f32_e32 v12, v19, v12
	v_mul_f32_e32 v8, v19, v8
	v_mul_f32_e32 v3, v19, v3
	v_mul_f32_e32 v18, v19, v18
	v_rndne_f32_e32 v16, v16
	v_mul_f32_e32 v17, v19, v17
	v_mul_f32_e32 v15, v19, v15
	v_mul_f32_e32 v14, v19, v14
	v_rndne_f32_e32 v12, v12
	v_mul_f32_e32 v13, v19, v13
	v_mul_f32_e32 v11, v19, v11
	v_mul_f32_e32 v10, v19, v10
	v_rndne_f32_e32 v8, v8
	v_mul_f32_e32 v9, v19, v9
	v_mul_f32_e32 v7, v19, v7
	v_mul_f32_e32 v6, v19, v6
	v_rndne_f32_e32 v3, v3
	v_mul_f32_e32 v4, v19, v4
	v_mul_f32_e32 v2, v19, v2
	v_rndne_f32_e32 v18, v18
	v_cvt_i32_f32_e32 v16, v16
	v_rndne_f32_e32 v17, v17
	v_rndne_f32_e32 v15, v15
	v_rndne_f32_e32 v14, v14
	v_cvt_i32_f32_e32 v12, v12
	v_rndne_f32_e32 v13, v13
	v_rndne_f32_e32 v11, v11
	v_rndne_f32_e32 v10, v10
	v_cvt_i32_f32_e32 v8, v8
	v_rndne_f32_e32 v9, v9
	v_rndne_f32_e32 v7, v7
	v_rndne_f32_e32 v6, v6
	v_cvt_i32_f32_e32 v3, v3
	v_rndne_f32_e32 v4, v4
	v_rndne_f32_e32 v2, v2
	v_cvt_i32_f32_e32 v18, v18
	v_cvt_i32_f32_sdwa v17, v17 dst_sel:WORD_1 dst_unused:UNUSED_PAD src0_sel:DWORD
	v_cvt_i32_f32_e32 v15, v15
	v_cvt_i32_f32_e32 v14, v14
	v_cvt_i32_f32_sdwa v13, v13 dst_sel:WORD_1 dst_unused:UNUSED_PAD src0_sel:DWORD
	v_cvt_i32_f32_e32 v11, v11
	v_cvt_i32_f32_e32 v10, v10
	v_cvt_i32_f32_sdwa v9, v9 dst_sel:WORD_1 dst_unused:UNUSED_PAD src0_sel:DWORD
	v_cvt_i32_f32_e32 v7, v7
	v_cvt_i32_f32_e32 v6, v6
	v_cvt_i32_f32_sdwa v4, v4 dst_sel:WORD_1 dst_unused:UNUSED_PAD src0_sel:DWORD
	v_cvt_i32_f32_e32 v2, v2
	v_lshlrev_b32_e32 v16, 8, v16
	v_lshlrev_b32_e32 v12, 8, v12
	v_lshlrev_b32_e32 v8, 8, v8
	v_lshlrev_b32_e32 v3, 8, v3
	v_and_b32_e32 v16, 0xff00, v16
	v_and_b32_e32 v17, 0xff0000, v17
	v_perm_b32 v15, v15, v18, s68
	v_and_b32_e32 v12, 0xff00, v12
	v_and_b32_e32 v13, 0xff0000, v13
	v_perm_b32 v11, v11, v14, s68
	v_and_b32_e32 v8, 0xff00, v8
	v_and_b32_e32 v9, 0xff0000, v9
	v_perm_b32 v7, v7, v10, s68
	v_and_b32_e32 v3, 0xff00, v3
	v_and_b32_e32 v4, 0xff0000, v4
	v_perm_b32 v2, v2, v6, s68
	v_or3_b32 v16, v15, v16, v17
	v_or3_b32 v17, v11, v12, v13
	v_or3_b32 v18, v7, v8, v9
	v_or3_b32 v19, v2, v3, v4
	v_lshl_add_u64 v[2:3], v[70:71], 0, s[40:41]
	global_store_dwordx4 v[2:3], v[16:19], off sc1
	s_nop 1
	s_and_saveexec_b64 s[46:47], s[6:7]
	s_cbranch_execz .LBB0_2004
; __device__ __forceinline__ void st16_wt(void* p, u32x4 v) { asm volatile("global_store_dwordx4 %0, %1, off sc1\n\ts_nop 1" :: "v"(p), "v"(v) : "memory"); }
; __device__ __forceinline__ void quant_rows(unsigned char* ws, size_t xq_off, size_t sar_off, int gw, int NGW, int lane) {
;     ...
;         float mysar = 0.f;
; #pragma unroll
;         for (int q = 0; q < 8; ++q) { const int row = m + q * NGW;
;             const float inv = mx[q] > 0.f ? 127.0f / mx[q] : 0.f, step = mx[q] > 0.f ? mx[q] * (1.0f / 127.0f) : 1.0f;
;             if (lane == 4 * q) mysar = rsqrtf(ssv * (1.0f / D) + EPS) * step;
;             u32x4 o4;
; #pragma unroll
;             for (int w4 = 0; w4 < 4; ++w4) { const unsigned w0 = a[q][w4 >> 1][2 * (w4 & 1)], w1 = a[q][w4 >> 1][2 * (w4 & 1) + 1];
;                 const int q0 = (int)__builtin_rintf(__uint_as_float(w0 << 16) * inv), q1 = (int)__builtin_rintf(__uint_as_float(w0 & 0xFFFF0000u) * inv);
;                 const int q2 = (int)__builtin_rintf(__uint_as_float(w1 << 16) * inv), q3 = (int)__builtin_rintf(__uint_as_float(w1 & 0xFFFF0000u) * inv);
;                 o4[w4] = ((unsigned)q0 & 0xFFu) | (((unsigned)q1 & 0xFFu) << 8) | (((unsigned)q2 & 0xFFu) << 16) | (((unsigned)q3 & 0xFFu) << 24); }
;             st16_wt(xq + (size_t)row * D + 16 * lane, o4);
;         }
;         if (lane < 32 && (lane & 3) == 0) sar[m + (lane >> 2) * NGW] = mysar;
	s_waitcnt lgkmcnt(0)
	v_add_f32_e32 v2, v62, v73
	v_fmamk_f32 v2, v2, 0x3a800000, v228
	v_mul_f32_e32 v3, 0x4b800000, v2
	v_cmp_gt_f32_e64 s[40:41], s84, v2
	v_mul_f32_e32 v6, 0x3c010204, v86
	v_mul_f32_e32 v7, 0x3c010204, v85
	v_cndmask_b32_e64 v2, v2, v3, s[40:41]
	v_rsq_f32_e32 v2, v2
	v_mul_f32_e32 v3, 0x3c010204, v99
	v_mul_f32_e32 v8, 0x3c010204, v84
	v_mul_f32_e32 v9, 0x3c010204, v83
	v_mul_f32_e32 v4, 0x45800000, v2
	v_cndmask_b32_e64 v2, v2, v4, s[40:41]
	v_mul_f32_e32 v4, 0x3c010204, v93
	v_mul_f32_e32 v10, 0x3c010204, v64
	v_mul_f32_e32 v5, 0x3c010204, v5
	v_cndmask_b32_e32 v3, 1.0, v3, vcc
	v_cndmask_b32_e64 v4, 1.0, v4, s[38:39]
	v_cndmask_b32_e64 v6, 1.0, v6, s[36:37]
	v_cndmask_b32_e64 v7, 1.0, v7, s[34:35]
	v_cndmask_b32_e64 v8, 1.0, v8, s[30:31]
	v_cndmask_b32_e64 v9, 1.0, v9, s[28:29]
	v_cndmask_b32_e64 v10, 1.0, v10, s[26:27]
	v_cndmask_b32_e64 v5, 1.0, v5, s[24:25]
	v_mul_f32_e32 v3, v2, v3
	v_mul_f32_e32 v4, v2, v4
	v_mul_f32_e32 v6, v2, v6
	v_mul_f32_e32 v7, v2, v7
	v_mul_f32_e32 v8, v2, v8
	v_mul_f32_e32 v9, v2, v9
	v_mul_f32_e32 v10, v2, v10
	v_mul_f32_e32 v2, v2, v5
	v_cndmask_b32_e64 v2, 0, v2, s[22:23]
	v_cndmask_b32_e64 v2, v2, v10, s[20:21]
	v_cndmask_b32_e64 v2, v2, v9, s[18:19]
	v_cndmask_b32_e64 v2, v2, v8, s[16:17]
	v_cndmask_b32_e64 v2, v2, v7, s[14:15]
	v_cndmask_b32_e64 v2, v2, v6, s[12:13]
	v_cndmask_b32_e64 v2, v2, v4, s[10:11]
	v_ashrrev_i32_e32 v73, 31, v72
	v_cndmask_b32_e64 v4, v2, v3, s[8:9]
	v_lshl_add_u64 v[2:3], v[72:73], 2, s[42:43]
	global_store_dword v[2:3], v4, off sc1
	s_branch .LBB0_2004

; __device__ __forceinline__ unsigned xb_add(unsigned* p, unsigned v) { return __hip_atomic_fetch_add(p, v, __ATOMIC_RELAXED, __HIP_MEMORY_SCOPE_AGENT); }
; __device__ __forceinline__ void xcd_barrier_impl(const XcdBarrier& b, bool leader) {
;     ...
;         const unsigned old = xb_add(&bar[XB_XSUB(b.x)], 1u);
;         const unsigned gen = old / nloc;
;         if (old + 1u == (gen + 1u) * nloc) {
;             __builtin_amdgcn_fence(__ATOMIC_RELEASE, "agent");
;             asm volatile("s_waitcnt vmcnt(0)" ::: "memory");
;             const unsigned og = xb_add(&bar[XB_TOP], 1u);
.LBB0_2042:
	s_or_b64 exec, exec, s[14:15]
	s_waitcnt vmcnt(0)
	s_waitcnt vmcnt(0)
.LBB0_2043:
	s_andn2_saveexec_b64 s[0:1], s[10:11]
	s_cbranch_execz .LBB0_2060
	s_mov_b64 s[12:13], exec
	s_waitcnt lgkmcnt(0)
	s_waitcnt vmcnt(0)
	v_mbcnt_lo_u32_b32 v2, s12, 0
	s_add_u32 s10, s8, 0x7400
	v_mbcnt_hi_u32_b32 v2, s13, v2
	s_addc_u32 s11, s9, 0
	v_cmp_eq_u32_e32 vcc, 0, v2
	s_and_saveexec_b64 s[14:15], vcc
	s_cbranch_execz .LBB0_2046
	s_bcnt1_i32_b64 s0, s[12:13]
	v_mov_b32_e32 v3, s0
	global_atomic_add v3, v1, v3, s[10:11] sc0
